# v16 + first K-loop iteration of each unit peeled with MFMA srcC=0 in 11 GEMM loops; per-unit accumulator zeroing (62 v_mov_b64) deleted
# baseline (speedup 1.0000x reference)
; #define PG8_STAGE(bufoff, rs_, soff_, voff) do { _Pragma("unroll") for (int _i = 0; _i < 2; ++_i) \
;         __builtin_amdgcn_raw_ptr_buffer_load_lds(rs_, (LAS void*)(lds + (bufoff) + ldsw + _i * 8192), 16, (int)(voff)[_i], (int)(soff_), 0, 0); } while (0)
; #define PG8_LDA(dst, b, h) do { _Pragma("unroll") for (int m = 0; m < 4; ++m) dst[m] = PG8_LD2(lds + PG8_SA(b, h) + aoff + m * 2048); } while (0)
; #define PG8_LDB(dst, b, h) do { _Pragma("unroll") for (int n = 0; n < 2; ++n) dst[n] = PG8_LD2(lds + PG8_SB(b, h) + boff + n * 2048); } while (0)
; #define PG8_WAIT_V(n) asm volatile("s_waitcnt vmcnt(" #n ")" ::: "memory")
; #define PG8_WAIT_L(n) asm volatile("s_waitcnt lgkmcnt(" #n ")" ::: "memory")
; #define PG8_BAR __builtin_amdgcn_s_barrier()
; #define PG8_SCHED __builtin_amdgcn_sched_barrier(0)
; template <class Epi, class Sched, bool ALIGN_EPI = false, bool SP2 = false, bool FP8 = false>
; __device__ __forceinline__ void gemm_phase(LAS unsigned char* lds, const Gemm g, const Sched& S, const Epi& E, int wbase) {
;     ...
;             PG8_LDB(B0, 0, 0); PG8_LDB(B1, 0, 1); PG8_SCHED; PG8_LDA(At, 0, 0); PG8_STAGE(PG8_SA(1, 1), rAc, a1 + hstep, voffA);
;             PG8_WAIT_V(8); PG8_WAIT_L(0); PG8_BAR; PG8_MMA(0, 0, At, B0); PG8_MMA(0, 1, At, B1); PG8_BAR; PG8_SCHED;
;             PG8_LDA(At, 0, 1); PG8_STAGE(PG8_SB(0, 0), rB2, b2, voffB); PG8_STAGE(PG8_SB(0, 1), rB2, b2 + hstep, voffB); PG8_STAGE(PG8_SA(0, 0), rA2, a2, voffA);
;             PG8_WAIT_V(8); PG8_WAIT_L(0); PG8_BAR; PG8_MMA(1, 0, At, B0); PG8_MMA(1, 1, At, B1); PG8_BAR; PG8_SCHED;
.LBB0_256:
	s_lshl_b32 s82, s1, 18
	s_andn2_b64 vcc, exec, s[66:67]
	s_lshl_b32 s83, s21, 18
	s_cbranch_vccnz .LBB0_260
	s_and_b64 s[2:3], s[26:27], exec
	s_waitcnt vmcnt(37)
	s_waitcnt vmcnt(36)
	s_waitcnt vmcnt(35)
	s_waitcnt vmcnt(32)
	s_waitcnt vmcnt(31)
	s_waitcnt vmcnt(28)
	s_waitcnt vmcnt(27)
	s_waitcnt vmcnt(24)
	s_waitcnt vmcnt(23)
	s_waitcnt vmcnt(22)
	v_mov_b32_e32 v231, v164
	v_mov_b32_e32 v230, 0xff61b1e6
	v_mov_b32_e32 v175, v233
	s_cselect_b32 s2, s82, s29
	s_cselect_b32 s3, s83, s28
	s_add_i32 s16, s29, 0x80
	s_addk_i32 s28, 0x100
	s_mov_b32 s29, 0
	ds_read_b128 v[128:131], v252
	ds_read_b128 v[132:135], v252 offset:1024
	ds_read_b128 v[136:139], v252 offset:2048
	ds_read_b128 v[140:143], v252 offset:3072
	ds_read_b128 v[144:147], v225
	ds_read_b128 v[148:151], v225 offset:1024
	ds_read_b128 v[152:155], v225 offset:2048
	ds_read_b128 v[156:159], v225 offset:3072
	s_add_i32 s6, s16, 0x80
	s_cmp_eq_u32 s18, s29
	s_cselect_b32 s46, s2, s6
	s_cselect_b32 s31, s3, s28
	s_or_b32 s30, s46, 0x80
	s_add_i32 s6, s41, s16
	s_mov_b32 m0, s19
	ds_read_b128 v[176:179], v172
	ds_read_b128 v[180:183], v172 offset:1024
	ds_read_b128 v[184:187], v172 offset:2048
	ds_read_b128 v[188:191], v172 offset:3072
	ds_read_b128 v[194:197], v172 offset:4096
	ds_read_b128 v[198:201], v172 offset:5120
	ds_read_b128 v[202:205], v172 offset:6144
	ds_read_b128 v[206:209], v172 offset:7168
	buffer_load_dwordx4 v192, s[36:39], s6 offen lds
	s_mov_b32 m0, s20
	s_nop 0
	buffer_load_dwordx4 v223, s[36:39], s6 offen lds
	s_waitcnt vmcnt(8)
	s_waitcnt lgkmcnt(0)
	s_barrier
	s_setprio 1
	v_mfma_f32_16x16x128_f8f6f4 v[124:127], v[128:135], v[176:183], 0
	v_mfma_f32_16x16x128_f8f6f4 v[120:123], v[136:143], v[176:183], 0
	v_mfma_f32_16x16x128_f8f6f4 v[108:111], v[128:135], v[184:191], 0
	v_mfma_f32_16x16x128_f8f6f4 v[104:107], v[136:143], v[184:191], 0
	v_mfma_f32_16x16x128_f8f6f4 v[160:163], v[128:135], v[194:201], 0
	v_mfma_f32_16x16x128_f8f6f4 v[210:213], v[136:143], v[194:201], 0
	v_mfma_f32_16x16x128_f8f6f4 v[214:217], v[128:135], v[202:209], 0
	v_mfma_f32_16x16x128_f8f6f4 v[218:221], v[136:143], v[202:209], 0
	v_mfma_f32_16x16x128_f8f6f4 v[116:119], v[144:151], v[176:183], 0
	v_mfma_f32_16x16x128_f8f6f4 v[112:115], v[152:159], v[176:183], 0
	v_mfma_f32_16x16x128_f8f6f4 v[100:103], v[144:151], v[184:191], 0
	v_mfma_f32_16x16x128_f8f6f4 v[96:99], v[152:159], v[184:191], 0
	v_mfma_f32_16x16x128_f8f6f4 v[176:179], v[144:151], v[194:201], 0
	v_mfma_f32_16x16x128_f8f6f4 v[180:183], v[152:159], v[194:201], 0
	v_mfma_f32_16x16x128_f8f6f4 v[184:187], v[144:151], v[202:209], 0
	v_mfma_f32_16x16x128_f8f6f4 v[188:191], v[152:159], v[202:209], 0
	s_setprio 0
	s_barrier
	s_mov_b32 m0, s43
	s_mov_b32 s6, s38
	s_mov_b32 s7, s39
	s_nop 1
	ds_read_b128 v[64:67], v172 offset:16384
	ds_read_b128 v[68:71], v172 offset:17408
	ds_read_b128 v[72:75], v172 offset:18432
	ds_read_b128 v[76:79], v172 offset:19456
	ds_read_b128 v[80:83], v172 offset:20480
	ds_read_b128 v[84:87], v172 offset:21504
	ds_read_b128 v[88:91], v172 offset:22528
	ds_read_b128 v[92:95], v172 offset:23552
	buffer_load_dwordx4 v222, s[4:7], s31 offen lds
	s_mov_b32 m0, s44
	s_add_i32 s47, s31, s41
	buffer_load_dwordx4 v193, s[4:7], s31 offen lds
	s_mov_b32 m0, s45
	s_nop 0
	buffer_load_dwordx4 v222, s[4:7], s47 offen lds
	s_mov_b32 m0, s52
	s_nop 0
	buffer_load_dwordx4 v193, s[4:7], s47 offen lds
	s_mov_b32 m0, s42
	s_nop 0
	buffer_load_dwordx4 v192, s[36:39], s46 offen lds
	s_mov_b32 m0, s53
	s_nop 0
	buffer_load_dwordx4 v223, s[36:39], s46 offen lds
	s_waitcnt vmcnt(8)
	s_waitcnt lgkmcnt(0)
	s_barrier
	s_setprio 1
	v_mfma_f32_16x16x128_f8f6f4 v[60:63], v[128:135], v[64:71], 0
	v_mfma_f32_16x16x128_f8f6f4 v[56:59], v[136:143], v[64:71], 0
	v_mfma_f32_16x16x128_f8f6f4 v[194:197], v[128:135], v[72:79], 0
	v_mfma_f32_16x16x128_f8f6f4 v[198:201], v[136:143], v[72:79], 0
	v_mfma_f32_16x16x128_f8f6f4 v[202:205], v[128:135], v[80:87], 0
	v_mfma_f32_16x16x128_f8f6f4 v[206:209], v[136:143], v[80:87], 0
	v_mfma_f32_16x16x128_f8f6f4 v[236:239], v[128:135], v[88:95], 0
	v_mfma_f32_16x16x128_f8f6f4 v[240:243], v[136:143], v[88:95], 0
	v_mfma_f32_16x16x128_f8f6f4 v[52:55], v[144:151], v[64:71], 0
	v_mfma_f32_16x16x128_f8f6f4 v[48:51], v[152:159], v[64:71], 0
	v_mfma_f32_16x16x128_f8f6f4 v[244:247], v[144:151], v[72:79], 0
	v_mfma_f32_16x16x128_f8f6f4 v[248:251], v[152:159], v[72:79], 0
	v_mfma_f32_16x16x128_f8f6f4 v[226:229], v[144:151], v[80:87], 0
	v_mfma_f32_16x16x128_f8f6f4 v[232:235], v[152:159], v[80:87], 0
	v_mfma_f32_16x16x128_f8f6f4 v[164:167], v[144:151], v[88:95], 0
	v_mfma_f32_16x16x128_f8f6f4 v[168:171], v[152:159], v[88:95], 0
	s_setprio 0
	s_barrier
; #define PG8_STAGE(bufoff, rs_, soff_, voff) do { _Pragma("unroll") for (int _i = 0; _i < 2; ++_i) \
;         __builtin_amdgcn_raw_ptr_buffer_load_lds(rs_, (LAS void*)(lds + (bufoff) + ldsw + _i * 8192), 16, (int)(voff)[_i], (int)(soff_), 0, 0); } while (0)
; #define PG8_LDA(dst, b, h) do { _Pragma("unroll") for (int m = 0; m < 4; ++m) dst[m] = PG8_LD2(lds + PG8_SA(b, h) + aoff + m * 2048); } while (0)
; #define PG8_LDB(dst, b, h) do { _Pragma("unroll") for (int n = 0; n < 2; ++n) dst[n] = PG8_LD2(lds + PG8_SB(b, h) + boff + n * 2048); } while (0)
; #define PG8_WAIT_V(n) asm volatile("s_waitcnt vmcnt(" #n ")" ::: "memory")
; #define PG8_WAIT_L(n) asm volatile("s_waitcnt lgkmcnt(" #n ")" ::: "memory")
; #define PG8_BAR __builtin_amdgcn_s_barrier()
; #define PG8_SCHED __builtin_amdgcn_sched_barrier(0)
; template <class Epi, class Sched, bool ALIGN_EPI = false, bool SP2 = false, bool FP8 = false>
; __device__ __forceinline__ void gemm_phase(LAS unsigned char* lds, const Gemm g, const Sched& S, const Epi& E, int wbase) {
;     ...
;         for (int t = 0; t < nt; t += 2) {
;     ...
;             PG8_LDB(B0, 1, 0); PG8_LDB(B1, 1, 1); PG8_SCHED; PG8_LDA(At, 1, 0); PG8_STAGE(PG8_SA(0, 1), rA2, a2 + hstep, voffA);
;             PG8_WAIT_V(8); PG8_WAIT_L(0); PG8_BAR; PG8_MMA(0, 0, At, B0); PG8_MMA(0, 1, At, B1); PG8_BAR; PG8_SCHED;
;             PG8_LDA(At, 1, 1); PG8_STAGE(PG8_SB(1, 0), rB2, b3, voffB); PG8_STAGE(PG8_SB(1, 1), rB2, b3 + hstep, voffB); PG8_STAGE(PG8_SA(1, 0), rA2, a3, voffA);
;             PG8_WAIT_V(8); PG8_WAIT_L(0); PG8_BAR; PG8_MMA(1, 0, At, B0); PG8_MMA(1, 1, At, B1); PG8_BAR; PG8_SCHED;
	s_nop 4
	ds_read_b128 v[0:3], v173
	ds_read_b128 v[4:7], v173 offset:1024
	ds_read_b128 v[16:19], v173 offset:2048
	ds_read_b128 v[20:23], v173 offset:3072
	ds_read_b128 v[128:131], v174
	ds_read_b128 v[132:135], v174 offset:1024
	ds_read_b128 v[136:139], v174 offset:2048
	ds_read_b128 v[140:143], v174 offset:3072
	s_add_i32 s46, s46, s41
	s_mov_b32 m0, s56
	ds_read_b128 v[8:11], v172 offset:32768
	ds_read_b128 v[12:15], v172 offset:33792
	ds_read_b128 v[24:27], v172 offset:34816
	ds_read_b128 v[28:31], v172 offset:35840
	ds_read_b128 v[32:35], v172 offset:36864
	ds_read_b128 v[36:39], v172 offset:37888
	ds_read_b128 v[40:43], v172 offset:38912
	ds_read_b128 v[44:47], v172 offset:39936
	buffer_load_dwordx4 v192, s[36:39], s46 offen lds
	s_mov_b32 m0, s57
	s_nop 0
	buffer_load_dwordx4 v223, s[36:39], s46 offen lds
	s_waitcnt vmcnt(8)
	s_waitcnt lgkmcnt(0)
	s_barrier
	s_setprio 1
	v_mfma_f32_16x16x128_f8f6f4 v[124:127], v[0:7], v[8:15], v[124:127]
	v_mfma_f32_16x16x128_f8f6f4 v[120:123], v[16:23], v[8:15], v[120:123]
	v_mfma_f32_16x16x128_f8f6f4 v[108:111], v[0:7], v[24:31], v[108:111]
	v_mfma_f32_16x16x128_f8f6f4 v[104:107], v[16:23], v[24:31], v[104:107]
	v_mfma_f32_16x16x128_f8f6f4 v[92:95], v[0:7], v[32:39], v[160:163]
	v_mfma_f32_16x16x128_f8f6f4 v[88:91], v[16:23], v[32:39], v[210:213]
	v_mfma_f32_16x16x128_f8f6f4 v[76:79], v[0:7], v[40:47], v[214:217]
	v_mfma_f32_16x16x128_f8f6f4 v[72:75], v[16:23], v[40:47], v[218:221]
	v_mfma_f32_16x16x128_f8f6f4 v[116:119], v[128:135], v[8:15], v[116:119]
	v_mfma_f32_16x16x128_f8f6f4 v[112:115], v[136:143], v[8:15], v[112:115]
	v_mfma_f32_16x16x128_f8f6f4 v[100:103], v[128:135], v[24:31], v[100:103]
	v_mfma_f32_16x16x128_f8f6f4 v[96:99], v[136:143], v[24:31], v[96:99]
	v_mfma_f32_16x16x128_f8f6f4 v[84:87], v[128:135], v[32:39], v[176:179]
	v_mfma_f32_16x16x128_f8f6f4 v[80:83], v[136:143], v[32:39], v[180:183]
	v_mfma_f32_16x16x128_f8f6f4 v[68:71], v[128:135], v[40:47], v[184:187]
	v_mfma_f32_16x16x128_f8f6f4 v[64:67], v[136:143], v[40:47], v[188:191]
	s_setprio 0
	s_barrier
	s_mov_b32 m0, s58
	s_bitset1_b32 s31, 7
	ds_read_b128 v[32:35], v172 offset:49152
	ds_read_b128 v[36:39], v172 offset:50176
	ds_read_b128 v[144:147], v172 offset:51200
	ds_read_b128 v[148:151], v172 offset:52224
	ds_read_b128 v[152:155], v172 offset:53248
	ds_read_b128 v[156:159], v172 offset:54272
	ds_read_b128 v[176:179], v172 offset:55296
	ds_read_b128 v[180:183], v172 offset:56320
	buffer_load_dwordx4 v222, s[4:7], s31 offen lds
	s_mov_b32 m0, s59
	s_nop 0
	buffer_load_dwordx4 v193, s[4:7], s31 offen lds
	s_add_i32 s31, s31, s41
	s_mov_b32 m0, s65
	s_nop 0
	buffer_load_dwordx4 v222, s[4:7], s31 offen lds
	s_mov_b32 m0, s33
	s_nop 0
	buffer_load_dwordx4 v193, s[4:7], s31 offen lds
	s_mov_b32 m0, s12
	s_nop 0
	buffer_load_dwordx4 v192, s[36:39], s30 offen lds
	s_mov_b32 m0, s13
	s_nop 0
	buffer_load_dwordx4 v223, s[36:39], s30 offen lds
	s_waitcnt vmcnt(8)
	s_waitcnt lgkmcnt(0)
	s_barrier
	s_setprio 1
	v_mfma_f32_16x16x128_f8f6f4 v[60:63], v[0:7], v[32:39], v[60:63]
	v_mfma_f32_16x16x128_f8f6f4 v[56:59], v[16:23], v[32:39], v[56:59]
	v_mfma_f32_16x16x128_f8f6f4 v[44:47], v[0:7], v[144:151], v[194:197]
	v_mfma_f32_16x16x128_f8f6f4 v[40:43], v[16:23], v[144:151], v[198:201]
	v_mfma_f32_16x16x128_f8f6f4 v[28:31], v[0:7], v[152:159], v[202:205]
	v_mfma_f32_16x16x128_f8f6f4 v[24:27], v[16:23], v[152:159], v[206:209]
	v_mfma_f32_16x16x128_f8f6f4 v[12:15], v[0:7], v[176:183], v[236:239]
	v_mfma_f32_16x16x128_f8f6f4 v[8:11], v[16:23], v[176:183], v[240:243]
	v_mfma_f32_16x16x128_f8f6f4 v[52:55], v[128:135], v[32:39], v[52:55]
	v_mfma_f32_16x16x128_f8f6f4 v[48:51], v[136:143], v[32:39], v[48:51]
	v_mfma_f32_16x16x128_f8f6f4 v[36:39], v[128:135], v[144:151], v[244:247]
	v_mfma_f32_16x16x128_f8f6f4 v[32:35], v[136:143], v[144:151], v[248:251]
	v_mfma_f32_16x16x128_f8f6f4 v[20:23], v[128:135], v[152:159], v[226:229]
	v_mfma_f32_16x16x128_f8f6f4 v[16:19], v[136:143], v[152:159], v[232:235]
	v_mfma_f32_16x16x128_f8f6f4 v[4:7], v[128:135], v[176:183], v[164:167]
	v_mfma_f32_16x16x128_f8f6f4 v[0:3], v[136:143], v[176:183], v[168:171]
	s_setprio 0
	s_barrier
	s_add_i32 s29, s29, 2
	s_addk_i32 s16, 0x100
	s_addk_i32 s28, 0x100
	s_cmp_ge_i32 s29, s77
	s_cbranch_scc0 .LBB0_258
	s_branch .Lzp_after_258

; #define PG8_BAR __builtin_amdgcn_s_barrier()
; template <class Epi, class Sched, bool ALIGN_EPI = false, bool SP2 = false, bool FP8 = false>
; __device__ __forceinline__ void gemm_phase(LAS unsigned char* lds, const Gemm g, const Sched& S, const Epi& E, int wbase) {
;     ...
;         if constexpr (ALIGN_EPI) { if (wr == 0) PG8_BAR; }
;         { int fr_ = fr, fq_ = fq; asm volatile("" : "+v"(fr_), "+v"(fq_));
;           if constexpr (Epi::HAS_PRE) E(acc, cur, wr, wc, fr_, fq_, pre_); else E(acc, cur, wr, wc, fr_, fq_); } S.done(cur);
.Lzp_after_258:
	v_mov_b32_e32 v233, v175
	v_mov_b32_e32 v234, v230
	v_mov_b32_e32 v164, v231
	v_mov_b32_e32 v231, 1
	v_mov_b32_e32 v230, 0x358637bd
	s_and_b64 vcc, exec, s[78:79]
	s_cbranch_vccnz .LBB0_261
	s_branch .LBB0_262

; #define PG8_STAGE(bufoff, rs_, soff_, voff) do { _Pragma("unroll") for (int _i = 0; _i < 2; ++_i) \
;         __builtin_amdgcn_raw_ptr_buffer_load_lds(rs_, (LAS void*)(lds + (bufoff) + ldsw + _i * 8192), 16, (int)(voff)[_i], (int)(soff_), 0, 0); } while (0)
; #define PG8_LDA(dst, b, h) do { _Pragma("unroll") for (int m = 0; m < 4; ++m) dst[m] = PG8_LD2(lds + PG8_SA(b, h) + aoff + m * 2048); } while (0)
; #define PG8_LDB(dst, b, h) do { _Pragma("unroll") for (int n = 0; n < 2; ++n) dst[n] = PG8_LD2(lds + PG8_SB(b, h) + boff + n * 2048); } while (0)
; #define PG8_WAIT_V(n) asm volatile("s_waitcnt vmcnt(" #n ")" ::: "memory")
; #define PG8_WAIT_L(n) asm volatile("s_waitcnt lgkmcnt(" #n ")" ::: "memory")
; #define PG8_BAR __builtin_amdgcn_s_barrier()
; #define PG8_SCHED __builtin_amdgcn_sched_barrier(0)
; template <class Epi, class Sched, bool ALIGN_EPI = false, bool SP2 = false, bool FP8 = false>
; __device__ __forceinline__ void gemm_phase(LAS unsigned char* lds, const Gemm g, const Sched& S, const Epi& E, int wbase) {
;     ...
;             PG8_LDB(B0, 0, 0); PG8_LDB(B1, 0, 1); PG8_SCHED; PG8_LDA(At, 0, 0); PG8_STAGE(PG8_SA(1, 1), rAc, a1 + hstep, voffA);
;             PG8_WAIT_V(8); PG8_WAIT_L(0); PG8_BAR; PG8_MMA(0, 0, At, B0); PG8_MMA(0, 1, At, B1); PG8_BAR; PG8_SCHED;
;             PG8_LDA(At, 0, 1); PG8_STAGE(PG8_SB(0, 0), rB2, b2, voffB); PG8_STAGE(PG8_SB(0, 1), rB2, b2 + hstep, voffB); PG8_STAGE(PG8_SA(0, 0), rA2, a2, voffA);
.LBB0_350:
	s_lshl_b32 s20, s19, 19
	s_andn2_b64 vcc, exec, s[66:67]
	s_lshl_b32 s21, s18, 19
	s_cbranch_vccnz .LBB0_430
	s_and_b64 s[2:3], s[26:27], exec
	s_waitcnt vmcnt(37)
	s_waitcnt vmcnt(36)
	s_waitcnt vmcnt(35)
	s_waitcnt vmcnt(32)
	s_waitcnt vmcnt(31)
	s_waitcnt vmcnt(28)
	s_waitcnt vmcnt(27)
	s_waitcnt vmcnt(24)
	s_waitcnt vmcnt(23)
	s_waitcnt vmcnt(22)
	s_cselect_b32 s2, s20, s29
	s_cselect_b32 s3, s21, s28
	s_add_i32 s16, s29, 0x80
	s_addk_i32 s28, 0x100
	s_mov_b32 s29, 0
	v_add_u32_e32 v140, 0x10000, v170
	v_add_u32_e32 v156, 0x14000, v170
	ds_read_b128 v[128:131], v140
	ds_read_b128 v[132:135], v140 offset:1024
	ds_read_b128 v[136:139], v140 offset:2048
	ds_read_b128 v[140:143], v140 offset:3072
	ds_read_b128 v[144:147], v156
	ds_read_b128 v[148:151], v156 offset:1024
	ds_read_b128 v[152:155], v156 offset:2048
	ds_read_b128 v[156:159], v156 offset:3072
	s_add_i32 s6, s16, 0x80
	s_cmp_eq_u32 s12, s29
	s_cselect_b32 s46, s2, s6
	s_cselect_b32 s31, s3, s28
	s_or_b32 s30, s46, 0x80
	s_add_i32 s6, s33, s16
	s_mov_b32 m0, s13
	ds_read_b128 v[160:163], v171
	ds_read_b128 v[172:175], v171 offset:1024
	ds_read_b128 v[176:179], v171 offset:2048
	ds_read_b128 v[180:183], v171 offset:3072
	ds_read_b128 v[184:187], v171 offset:4096
	ds_read_b128 v[188:191], v171 offset:5120
	ds_read_b128 v[194:197], v171 offset:6144
	ds_read_b128 v[198:201], v171 offset:7168
	buffer_load_dwordx4 v164, s[36:39], s6 offen lds
	s_mov_b32 m0, s83
	s_nop 0
	buffer_load_dwordx4 v166, s[36:39], s6 offen lds
	s_waitcnt vmcnt(8)
	s_waitcnt lgkmcnt(0)
	s_barrier
	s_setprio 1
	v_mfma_f32_16x16x32_bf16 v[124:127], v[128:131], v[160:163], 0
	v_mfma_f32_16x16x32_bf16 v[120:123], v[136:139], v[160:163], 0
	v_mfma_f32_16x16x32_bf16 v[108:111], v[128:131], v[176:179], 0
	v_mfma_f32_16x16x32_bf16 v[104:107], v[136:139], v[176:179], 0
	v_mfma_f32_16x16x32_bf16 v[92:95], v[128:131], v[184:187], 0
	v_mfma_f32_16x16x32_bf16 v[88:91], v[136:139], v[184:187], 0
	v_mfma_f32_16x16x32_bf16 v[76:79], v[128:131], v[194:197], 0
	v_mfma_f32_16x16x32_bf16 v[72:75], v[136:139], v[194:197], 0
	v_mfma_f32_16x16x32_bf16 v[124:127], v[132:135], v[172:175], v[124:127]
	v_mfma_f32_16x16x32_bf16 v[120:123], v[140:143], v[172:175], v[120:123]
	v_mfma_f32_16x16x32_bf16 v[108:111], v[132:135], v[180:183], v[108:111]
	v_mfma_f32_16x16x32_bf16 v[104:107], v[140:143], v[180:183], v[104:107]
	v_mfma_f32_16x16x32_bf16 v[92:95], v[132:135], v[188:191], v[92:95]
	v_mfma_f32_16x16x32_bf16 v[88:91], v[140:143], v[188:191], v[88:91]
	v_mfma_f32_16x16x32_bf16 v[76:79], v[132:135], v[198:201], v[76:79]
	v_mfma_f32_16x16x32_bf16 v[72:75], v[140:143], v[198:201], v[72:75]
	v_mfma_f32_16x16x32_bf16 v[116:119], v[144:147], v[160:163], 0
	v_mfma_f32_16x16x32_bf16 v[112:115], v[152:155], v[160:163], 0
	v_mfma_f32_16x16x32_bf16 v[100:103], v[144:147], v[176:179], 0
	v_mfma_f32_16x16x32_bf16 v[96:99], v[152:155], v[176:179], 0
	v_mfma_f32_16x16x32_bf16 v[84:87], v[144:147], v[184:187], 0
	v_mfma_f32_16x16x32_bf16 v[80:83], v[152:155], v[184:187], 0
	v_mfma_f32_16x16x32_bf16 v[68:71], v[144:147], v[194:197], 0
	v_mfma_f32_16x16x32_bf16 v[64:67], v[152:155], v[194:197], 0
	v_mfma_f32_16x16x32_bf16 v[116:119], v[148:151], v[172:175], v[116:119]
	v_mfma_f32_16x16x32_bf16 v[112:115], v[156:159], v[172:175], v[112:115]
	v_mfma_f32_16x16x32_bf16 v[100:103], v[148:151], v[180:183], v[100:103]
	v_mfma_f32_16x16x32_bf16 v[96:99], v[156:159], v[180:183], v[96:99]
	v_mfma_f32_16x16x32_bf16 v[84:87], v[148:151], v[188:191], v[84:87]
	v_mfma_f32_16x16x32_bf16 v[80:83], v[156:159], v[188:191], v[80:83]
	v_mfma_f32_16x16x32_bf16 v[68:71], v[148:151], v[198:201], v[68:71]
	v_mfma_f32_16x16x32_bf16 v[64:67], v[156:159], v[198:201], v[64:67]
	s_setprio 0
	s_barrier
	s_mov_b32 m0, s42
	s_mov_b32 s6, s38
	s_mov_b32 s7, s39
	ds_read_b128 v[160:163], v171 offset:16384
	ds_read_b128 v[172:175], v171 offset:17408
	ds_read_b128 v[176:179], v171 offset:18432
	ds_read_b128 v[180:183], v171 offset:19456
	ds_read_b128 v[184:187], v171 offset:20480
	ds_read_b128 v[188:191], v171 offset:21504
	ds_read_b128 v[194:197], v171 offset:22528
	ds_read_b128 v[198:201], v171 offset:23552
	buffer_load_dwordx4 v165, s[4:7], s31 offen lds
	s_mov_b32 m0, s43
	s_add_i32 s47, s31, s33
	buffer_load_dwordx4 v167, s[4:7], s31 offen lds
	s_mov_b32 m0, s44
	s_nop 0
	buffer_load_dwordx4 v165, s[4:7], s47 offen lds
	s_mov_b32 m0, s45
	s_nop 0
	buffer_load_dwordx4 v167, s[4:7], s47 offen lds
	s_mov_b32 m0, s41
	s_nop 0
	buffer_load_dwordx4 v164, s[36:39], s46 offen lds
	s_mov_b32 m0, s52
	s_nop 0
	buffer_load_dwordx4 v166, s[36:39], s46 offen lds
	s_waitcnt vmcnt(8)
	s_waitcnt lgkmcnt(0)
	s_barrier
; #define PG8_STAGE(bufoff, rs_, soff_, voff) do { _Pragma("unroll") for (int _i = 0; _i < 2; ++_i) \
;         __builtin_amdgcn_raw_ptr_buffer_load_lds(rs_, (LAS void*)(lds + (bufoff) + ldsw + _i * 8192), 16, (int)(voff)[_i], (int)(soff_), 0, 0); } while (0)
; #define PG8_LDA(dst, b, h) do { _Pragma("unroll") for (int m = 0; m < 4; ++m) dst[m] = PG8_LD2(lds + PG8_SA(b, h) + aoff + m * 2048); } while (0)
; #define PG8_LDB(dst, b, h) do { _Pragma("unroll") for (int n = 0; n < 2; ++n) dst[n] = PG8_LD2(lds + PG8_SB(b, h) + boff + n * 2048); } while (0)
; #define PG8_WAIT_V(n) asm volatile("s_waitcnt vmcnt(" #n ")" ::: "memory")
; #define PG8_WAIT_L(n) asm volatile("s_waitcnt lgkmcnt(" #n ")" ::: "memory")
; #define PG8_BAR __builtin_amdgcn_s_barrier()
; #define PG8_SCHED __builtin_amdgcn_sched_barrier(0)
; template <class Epi, class Sched, bool ALIGN_EPI = false, bool SP2 = false, bool FP8 = false>
; __device__ __forceinline__ void gemm_phase(LAS unsigned char* lds, const Gemm g, const Sched& S, const Epi& E, int wbase) {
;     ...
;             PG8_WAIT_V(8); PG8_WAIT_L(0); PG8_BAR; PG8_MMA(1, 0, At, B0); PG8_MMA(1, 1, At, B1); PG8_BAR; PG8_SCHED;
;             PG8_LDB(B0, 1, 0); PG8_LDB(B1, 1, 1); PG8_SCHED; PG8_LDA(At, 1, 0); PG8_STAGE(PG8_SA(0, 1), rA2, a2 + hstep, voffA);
;             PG8_WAIT_V(8); PG8_WAIT_L(0); PG8_BAR; PG8_MMA(0, 0, At, B0); PG8_MMA(0, 1, At, B1); PG8_BAR; PG8_SCHED;
	s_setprio 1
	v_mfma_f32_16x16x32_bf16 v[60:63], v[128:131], v[160:163], 0
	v_mfma_f32_16x16x32_bf16 v[56:59], v[136:139], v[160:163], 0
	v_mfma_f32_16x16x32_bf16 v[44:47], v[128:131], v[176:179], 0
	v_mfma_f32_16x16x32_bf16 v[40:43], v[136:139], v[176:179], 0
	v_mfma_f32_16x16x32_bf16 v[28:31], v[128:131], v[184:187], 0
	v_mfma_f32_16x16x32_bf16 v[24:27], v[136:139], v[184:187], 0
	v_mfma_f32_16x16x32_bf16 v[12:15], v[128:131], v[194:197], 0
	v_mfma_f32_16x16x32_bf16 v[8:11], v[136:139], v[194:197], 0
	v_mfma_f32_16x16x32_bf16 v[60:63], v[132:135], v[172:175], v[60:63]
	v_mfma_f32_16x16x32_bf16 v[56:59], v[140:143], v[172:175], v[56:59]
	v_mfma_f32_16x16x32_bf16 v[44:47], v[132:135], v[180:183], v[44:47]
	v_mfma_f32_16x16x32_bf16 v[40:43], v[140:143], v[180:183], v[40:43]
	v_mfma_f32_16x16x32_bf16 v[28:31], v[132:135], v[188:191], v[28:31]
	v_mfma_f32_16x16x32_bf16 v[24:27], v[140:143], v[188:191], v[24:27]
	v_mfma_f32_16x16x32_bf16 v[12:15], v[132:135], v[198:201], v[12:15]
	v_mfma_f32_16x16x32_bf16 v[8:11], v[140:143], v[198:201], v[8:11]
	v_mfma_f32_16x16x32_bf16 v[52:55], v[144:147], v[160:163], 0
	v_mfma_f32_16x16x32_bf16 v[48:51], v[152:155], v[160:163], 0
	v_mfma_f32_16x16x32_bf16 v[36:39], v[144:147], v[176:179], 0
	v_mfma_f32_16x16x32_bf16 v[32:35], v[152:155], v[176:179], 0
	v_mfma_f32_16x16x32_bf16 v[20:23], v[144:147], v[184:187], 0
	v_mfma_f32_16x16x32_bf16 v[16:19], v[152:155], v[184:187], 0
	v_mfma_f32_16x16x32_bf16 v[4:7], v[144:147], v[194:197], 0
	v_mfma_f32_16x16x32_bf16 v[0:3], v[152:155], v[194:197], 0
	v_mfma_f32_16x16x32_bf16 v[52:55], v[148:151], v[172:175], v[52:55]
	v_mfma_f32_16x16x32_bf16 v[48:51], v[156:159], v[172:175], v[48:51]
	v_mfma_f32_16x16x32_bf16 v[36:39], v[148:151], v[180:183], v[36:39]
	v_mfma_f32_16x16x32_bf16 v[32:35], v[156:159], v[180:183], v[32:35]
	v_mfma_f32_16x16x32_bf16 v[20:23], v[148:151], v[188:191], v[20:23]
	v_mfma_f32_16x16x32_bf16 v[16:19], v[156:159], v[188:191], v[16:19]
	v_mfma_f32_16x16x32_bf16 v[4:7], v[148:151], v[198:201], v[4:7]
	v_mfma_f32_16x16x32_bf16 v[0:3], v[156:159], v[198:201], v[0:3]
	s_setprio 0
	s_barrier
	v_add_u32_e32 v140, 0x18000, v170
	v_add_u32_e32 v156, 0x1c000, v170
	ds_read_b128 v[128:131], v140
	ds_read_b128 v[132:135], v140 offset:1024
	ds_read_b128 v[136:139], v140 offset:2048
	ds_read_b128 v[140:143], v140 offset:3072
	ds_read_b128 v[144:147], v156
	ds_read_b128 v[148:151], v156 offset:1024
	ds_read_b128 v[152:155], v156 offset:2048
	ds_read_b128 v[156:159], v156 offset:3072
	s_add_i32 s46, s46, s33
	s_mov_b32 m0, s53
	ds_read_b128 v[160:163], v171 offset:32768
	ds_read_b128 v[172:175], v171 offset:33792
	ds_read_b128 v[176:179], v171 offset:34816
	ds_read_b128 v[180:183], v171 offset:35840
	ds_read_b128 v[184:187], v171 offset:36864
	ds_read_b128 v[188:191], v171 offset:37888
	ds_read_b128 v[194:197], v171 offset:38912
	ds_read_b128 v[198:201], v171 offset:39936
	buffer_load_dwordx4 v164, s[36:39], s46 offen lds
	s_mov_b32 m0, s1
	s_nop 0
	buffer_load_dwordx4 v166, s[36:39], s46 offen lds
	s_waitcnt vmcnt(8)
	s_waitcnt lgkmcnt(0)
	s_barrier
	s_setprio 1
	v_mfma_f32_16x16x32_bf16 v[124:127], v[128:131], v[160:163], v[124:127]
	v_mfma_f32_16x16x32_bf16 v[120:123], v[136:139], v[160:163], v[120:123]
	v_mfma_f32_16x16x32_bf16 v[108:111], v[128:131], v[176:179], v[108:111]
	v_mfma_f32_16x16x32_bf16 v[104:107], v[136:139], v[176:179], v[104:107]
	v_mfma_f32_16x16x32_bf16 v[92:95], v[128:131], v[184:187], v[92:95]
	v_mfma_f32_16x16x32_bf16 v[88:91], v[136:139], v[184:187], v[88:91]
	v_mfma_f32_16x16x32_bf16 v[76:79], v[128:131], v[194:197], v[76:79]
	v_mfma_f32_16x16x32_bf16 v[72:75], v[136:139], v[194:197], v[72:75]
	v_mfma_f32_16x16x32_bf16 v[124:127], v[132:135], v[172:175], v[124:127]
	v_mfma_f32_16x16x32_bf16 v[120:123], v[140:143], v[172:175], v[120:123]
	v_mfma_f32_16x16x32_bf16 v[108:111], v[132:135], v[180:183], v[108:111]
	v_mfma_f32_16x16x32_bf16 v[104:107], v[140:143], v[180:183], v[104:107]
	v_mfma_f32_16x16x32_bf16 v[92:95], v[132:135], v[188:191], v[92:95]
	v_mfma_f32_16x16x32_bf16 v[88:91], v[140:143], v[188:191], v[88:91]
	v_mfma_f32_16x16x32_bf16 v[76:79], v[132:135], v[198:201], v[76:79]
	v_mfma_f32_16x16x32_bf16 v[72:75], v[140:143], v[198:201], v[72:75]
	v_mfma_f32_16x16x32_bf16 v[116:119], v[144:147], v[160:163], v[116:119]
	v_mfma_f32_16x16x32_bf16 v[112:115], v[152:155], v[160:163], v[112:115]
	v_mfma_f32_16x16x32_bf16 v[100:103], v[144:147], v[176:179], v[100:103]
	v_mfma_f32_16x16x32_bf16 v[96:99], v[152:155], v[176:179], v[96:99]
	v_mfma_f32_16x16x32_bf16 v[84:87], v[144:147], v[184:187], v[84:87]
	v_mfma_f32_16x16x32_bf16 v[80:83], v[152:155], v[184:187], v[80:83]
	v_mfma_f32_16x16x32_bf16 v[68:71], v[144:147], v[194:197], v[68:71]
	v_mfma_f32_16x16x32_bf16 v[64:67], v[152:155], v[194:197], v[64:67]
	v_mfma_f32_16x16x32_bf16 v[116:119], v[148:151], v[172:175], v[116:119]
	v_mfma_f32_16x16x32_bf16 v[112:115], v[156:159], v[172:175], v[112:115]
	v_mfma_f32_16x16x32_bf16 v[100:103], v[148:151], v[180:183], v[100:103]
	v_mfma_f32_16x16x32_bf16 v[96:99], v[156:159], v[180:183], v[96:99]
	v_mfma_f32_16x16x32_bf16 v[84:87], v[148:151], v[188:191], v[84:87]
	v_mfma_f32_16x16x32_bf16 v[80:83], v[156:159], v[188:191], v[80:83]
	v_mfma_f32_16x16x32_bf16 v[68:71], v[148:151], v[198:201], v[68:71]
	v_mfma_f32_16x16x32_bf16 v[64:67], v[156:159], v[198:201], v[64:67]
	s_setprio 0
	s_barrier
; #define PG8_STAGE(bufoff, rs_, soff_, voff) do { _Pragma("unroll") for (int _i = 0; _i < 2; ++_i) \
;         __builtin_amdgcn_raw_ptr_buffer_load_lds(rs_, (LAS void*)(lds + (bufoff) + ldsw + _i * 8192), 16, (int)(voff)[_i], (int)(soff_), 0, 0); } while (0)
; #define PG8_LDA(dst, b, h) do { _Pragma("unroll") for (int m = 0; m < 4; ++m) dst[m] = PG8_LD2(lds + PG8_SA(b, h) + aoff + m * 2048); } while (0)
; #define PG8_WAIT_V(n) asm volatile("s_waitcnt vmcnt(" #n ")" ::: "memory")
; #define PG8_WAIT_L(n) asm volatile("s_waitcnt lgkmcnt(" #n ")" ::: "memory")
; #define PG8_BAR __builtin_amdgcn_s_barrier()
; #define PG8_SCHED __builtin_amdgcn_sched_barrier(0)
; template <class Epi, class Sched, bool ALIGN_EPI = false, bool SP2 = false, bool FP8 = false>
; __device__ __forceinline__ void gemm_phase(LAS unsigned char* lds, const Gemm g, const Sched& S, const Epi& E, int wbase) {
;     ...
;         for (int t = 0; t < nt; t += 2) {
;     ...
;             PG8_LDA(At, 1, 1); PG8_STAGE(PG8_SB(1, 0), rB2, b3, voffB); PG8_STAGE(PG8_SB(1, 1), rB2, b3 + hstep, voffB); PG8_STAGE(PG8_SA(1, 0), rA2, a3, voffA);
;             PG8_WAIT_V(8); PG8_WAIT_L(0); PG8_BAR; PG8_MMA(1, 0, At, B0); PG8_MMA(1, 1, At, B1); PG8_BAR; PG8_SCHED;
	s_mov_b32 m0, s56
	s_bitset1_b32 s31, 7
	ds_read_b128 v[160:163], v171 offset:49152
	ds_read_b128 v[172:175], v171 offset:50176
	ds_read_b128 v[176:179], v171 offset:51200
	ds_read_b128 v[180:183], v171 offset:52224
	ds_read_b128 v[184:187], v171 offset:53248
	ds_read_b128 v[188:191], v171 offset:54272
	ds_read_b128 v[194:197], v171 offset:55296
	ds_read_b128 v[198:201], v171 offset:56320
	buffer_load_dwordx4 v165, s[4:7], s31 offen lds
	s_mov_b32 m0, s57
	s_nop 0
	buffer_load_dwordx4 v167, s[4:7], s31 offen lds
	s_add_i32 s31, s31, s33
	s_mov_b32 m0, s65
	s_nop 0
	buffer_load_dwordx4 v165, s[4:7], s31 offen lds
	s_mov_b32 m0, s76
	s_nop 0
	buffer_load_dwordx4 v167, s[4:7], s31 offen lds
	s_mov_b32 m0, s58
	s_nop 0
	buffer_load_dwordx4 v164, s[36:39], s30 offen lds
	s_mov_b32 m0, s59
	s_nop 0
	buffer_load_dwordx4 v166, s[36:39], s30 offen lds
	s_waitcnt vmcnt(8)
	s_waitcnt lgkmcnt(0)
	s_barrier
	s_setprio 1
	v_mfma_f32_16x16x32_bf16 v[60:63], v[128:131], v[160:163], v[60:63]
	v_mfma_f32_16x16x32_bf16 v[56:59], v[136:139], v[160:163], v[56:59]
	v_mfma_f32_16x16x32_bf16 v[44:47], v[128:131], v[176:179], v[44:47]
	v_mfma_f32_16x16x32_bf16 v[40:43], v[136:139], v[176:179], v[40:43]
	v_mfma_f32_16x16x32_bf16 v[28:31], v[128:131], v[184:187], v[28:31]
	v_mfma_f32_16x16x32_bf16 v[24:27], v[136:139], v[184:187], v[24:27]
	v_mfma_f32_16x16x32_bf16 v[12:15], v[128:131], v[194:197], v[12:15]
	v_mfma_f32_16x16x32_bf16 v[8:11], v[136:139], v[194:197], v[8:11]
	v_mfma_f32_16x16x32_bf16 v[60:63], v[132:135], v[172:175], v[60:63]
	v_mfma_f32_16x16x32_bf16 v[56:59], v[140:143], v[172:175], v[56:59]
	v_mfma_f32_16x16x32_bf16 v[44:47], v[132:135], v[180:183], v[44:47]
	v_mfma_f32_16x16x32_bf16 v[40:43], v[140:143], v[180:183], v[40:43]
	v_mfma_f32_16x16x32_bf16 v[28:31], v[132:135], v[188:191], v[28:31]
	v_mfma_f32_16x16x32_bf16 v[24:27], v[140:143], v[188:191], v[24:27]
	v_mfma_f32_16x16x32_bf16 v[12:15], v[132:135], v[198:201], v[12:15]
	v_mfma_f32_16x16x32_bf16 v[8:11], v[140:143], v[198:201], v[8:11]
	v_mfma_f32_16x16x32_bf16 v[52:55], v[144:147], v[160:163], v[52:55]
	v_mfma_f32_16x16x32_bf16 v[48:51], v[152:155], v[160:163], v[48:51]
	v_mfma_f32_16x16x32_bf16 v[36:39], v[144:147], v[176:179], v[36:39]
	v_mfma_f32_16x16x32_bf16 v[32:35], v[152:155], v[176:179], v[32:35]
	v_mfma_f32_16x16x32_bf16 v[20:23], v[144:147], v[184:187], v[20:23]
	v_mfma_f32_16x16x32_bf16 v[16:19], v[152:155], v[184:187], v[16:19]
	v_mfma_f32_16x16x32_bf16 v[4:7], v[144:147], v[194:197], v[4:7]
	v_mfma_f32_16x16x32_bf16 v[0:3], v[152:155], v[194:197], v[0:3]
	v_mfma_f32_16x16x32_bf16 v[52:55], v[148:151], v[172:175], v[52:55]
	v_mfma_f32_16x16x32_bf16 v[48:51], v[156:159], v[172:175], v[48:51]
	v_mfma_f32_16x16x32_bf16 v[36:39], v[148:151], v[180:183], v[36:39]
	v_mfma_f32_16x16x32_bf16 v[32:35], v[156:159], v[180:183], v[32:35]
	v_mfma_f32_16x16x32_bf16 v[20:23], v[148:151], v[188:191], v[20:23]
	v_mfma_f32_16x16x32_bf16 v[16:19], v[156:159], v[188:191], v[16:19]
	v_mfma_f32_16x16x32_bf16 v[4:7], v[148:151], v[198:201], v[4:7]
	v_mfma_f32_16x16x32_bf16 v[0:3], v[156:159], v[198:201], v[0:3]
	s_setprio 0
	s_barrier
	s_add_i32 s29, s29, 2
	s_addk_i32 s16, 0x100
	s_addk_i32 s28, 0x100
	s_cmp_ge_i32 s29, s82
	s_cbranch_scc0 .LBB0_352
	s_branch .Lzp_after_352

; #define PG8_BAR __builtin_amdgcn_s_barrier()
; template <class Epi, class Sched, bool ALIGN_EPI = false, bool SP2 = false, bool FP8 = false>
; __device__ __forceinline__ void gemm_phase(LAS unsigned char* lds, const Gemm g, const Sched& S, const Epi& E, int wbase) {
;     ...
;         if constexpr (ALIGN_EPI) { if (wr == 0) PG8_BAR; }
;         { int fr_ = fr, fq_ = fq; asm volatile("" : "+v"(fr_), "+v"(fq_));
;           if constexpr (Epi::HAS_PRE) E(acc, cur, wr, wc, fr_, fq_, pre_); else E(acc, cur, wr, wc, fr_, fq_); } S.done(cur);
.Lzp_after_352:
	s_and_b64 vcc, exec, s[78:79]
	s_cbranch_vccz .LBB0_355

; #define PG8_STAGE(bufoff, rs_, soff_, voff) do { _Pragma("unroll") for (int _i = 0; _i < 2; ++_i) \
;         __builtin_amdgcn_raw_ptr_buffer_load_lds(rs_, (LAS void*)(lds + (bufoff) + ldsw + _i * 8192), 16, (int)(voff)[_i], (int)(soff_), 0, 0); } while (0)
; #define PG8_LDA(dst, b, h) do { _Pragma("unroll") for (int m = 0; m < 4; ++m) dst[m] = PG8_LD2(lds + PG8_SA(b, h) + aoff + m * 2048); } while (0)
; #define PG8_LDB(dst, b, h) do { _Pragma("unroll") for (int n = 0; n < 2; ++n) dst[n] = PG8_LD2(lds + PG8_SB(b, h) + boff + n * 2048); } while (0)
; #define PG8_WAIT_V(n) asm volatile("s_waitcnt vmcnt(" #n ")" ::: "memory")
; #define PG8_WAIT_L(n) asm volatile("s_waitcnt lgkmcnt(" #n ")" ::: "memory")
; #define PG8_BAR __builtin_amdgcn_s_barrier()
; #define PG8_SCHED __builtin_amdgcn_sched_barrier(0)
; template <class Epi, class Sched, bool ALIGN_EPI = false, bool SP2 = false, bool FP8 = false>
; __device__ __forceinline__ void gemm_phase(LAS unsigned char* lds, const Gemm g, const Sched& S, const Epi& E, int wbase) {
;     ...
;             PG8_LDB(B0, 0, 0); PG8_LDB(B1, 0, 1); PG8_SCHED; PG8_LDA(At, 0, 0); PG8_STAGE(PG8_SA(1, 1), rAc, a1 + hstep, voffA);
;             PG8_WAIT_V(8); PG8_WAIT_L(0); PG8_BAR; PG8_MMA(0, 0, At, B0); PG8_MMA(0, 1, At, B1); PG8_BAR; PG8_SCHED;
;             PG8_LDA(At, 0, 1); PG8_STAGE(PG8_SB(0, 0), rB2, b2, voffB); PG8_STAGE(PG8_SB(0, 1), rB2, b2 + hstep, voffB); PG8_STAGE(PG8_SA(0, 0), rA2, a2, voffA);
.LBB0_448:
	s_lshl_b32 s48, s47, 17
	s_andn2_b64 vcc, exec, s[10:11]
	s_lshl_b32 s52, s46, 17
	s_cbranch_vccnz .LBB0_456
	s_and_b64 s[6:7], s[16:17], exec
	s_waitcnt vmcnt(37)
	s_waitcnt vmcnt(36)
	s_waitcnt vmcnt(35)
	s_waitcnt vmcnt(32)
	s_waitcnt vmcnt(31)
	s_waitcnt vmcnt(28)
	s_waitcnt vmcnt(27)
	s_waitcnt vmcnt(24)
	s_waitcnt vmcnt(23)
	s_waitcnt vmcnt(22)
	s_cselect_b32 s56, s48, s55
	s_cselect_b32 s57, s52, s54
	s_add_i32 s58, s55, 0x80
	s_add_i32 s59, s54, 0x100
	s_mov_b32 s60, 0
	v_add_u32_e32 v148, 0x10000, v138
	v_add_u32_e32 v164, 0x14000, v138
	ds_read_b128 v[128:131], v148
	ds_read_b128 v[140:143], v148 offset:1024
	ds_read_b128 v[144:147], v148 offset:2048
	ds_read_b128 v[148:151], v148 offset:3072
	ds_read_b128 v[152:155], v164
	ds_read_b128 v[156:159], v164 offset:1024
	ds_read_b128 v[160:163], v164 offset:2048
	ds_read_b128 v[164:167], v164 offset:3072
	s_add_i32 s6, s58, 0x80
	s_cmp_eq_u32 s42, s60
	s_cselect_b32 s61, s56, s6
	s_cselect_b32 s55, s57, s59
	s_or_b32 s54, s61, 0x80
	s_add_i32 s6, s19, s58
	s_mov_b32 m0, s43
	ds_read_b128 v[168:171], v139
	ds_read_b128 v[172:175], v139 offset:1024
	ds_read_b128 v[176:179], v139 offset:2048
	ds_read_b128 v[180:183], v139 offset:3072
	ds_read_b128 v[184:187], v139 offset:4096
	ds_read_b128 v[188:191], v139 offset:5120
	ds_read_b128 v[194:197], v139 offset:6144
	ds_read_b128 v[198:201], v139 offset:7168
	buffer_load_dwordx4 v132, s[36:39], s6 offen lds
	s_mov_b32 m0, s44
	s_nop 0
	buffer_load_dwordx4 v134, s[36:39], s6 offen lds
	s_waitcnt vmcnt(8)
	s_waitcnt lgkmcnt(0)
	s_barrier
	s_setprio 1
	v_mfma_f32_16x16x32_bf16 v[124:127], v[128:131], v[168:171], 0
	v_mfma_f32_16x16x32_bf16 v[120:123], v[144:147], v[168:171], 0
	v_mfma_f32_16x16x32_bf16 v[108:111], v[128:131], v[176:179], 0
	v_mfma_f32_16x16x32_bf16 v[104:107], v[144:147], v[176:179], 0
	v_mfma_f32_16x16x32_bf16 v[92:95], v[128:131], v[184:187], 0
	v_mfma_f32_16x16x32_bf16 v[88:91], v[144:147], v[184:187], 0
	v_mfma_f32_16x16x32_bf16 v[76:79], v[128:131], v[194:197], 0
	v_mfma_f32_16x16x32_bf16 v[72:75], v[144:147], v[194:197], 0
	v_mfma_f32_16x16x32_bf16 v[124:127], v[140:143], v[172:175], v[124:127]
	v_mfma_f32_16x16x32_bf16 v[120:123], v[148:151], v[172:175], v[120:123]
	v_mfma_f32_16x16x32_bf16 v[108:111], v[140:143], v[180:183], v[108:111]
	v_mfma_f32_16x16x32_bf16 v[104:107], v[148:151], v[180:183], v[104:107]
	v_mfma_f32_16x16x32_bf16 v[92:95], v[140:143], v[188:191], v[92:95]
	v_mfma_f32_16x16x32_bf16 v[88:91], v[148:151], v[188:191], v[88:91]
	v_mfma_f32_16x16x32_bf16 v[76:79], v[140:143], v[198:201], v[76:79]
	v_mfma_f32_16x16x32_bf16 v[72:75], v[148:151], v[198:201], v[72:75]
	v_mfma_f32_16x16x32_bf16 v[116:119], v[152:155], v[168:171], 0
	v_mfma_f32_16x16x32_bf16 v[112:115], v[160:163], v[168:171], 0
	v_mfma_f32_16x16x32_bf16 v[100:103], v[152:155], v[176:179], 0
	v_mfma_f32_16x16x32_bf16 v[96:99], v[160:163], v[176:179], 0
	v_mfma_f32_16x16x32_bf16 v[84:87], v[152:155], v[184:187], 0
	v_mfma_f32_16x16x32_bf16 v[80:83], v[160:163], v[184:187], 0
	v_mfma_f32_16x16x32_bf16 v[68:71], v[152:155], v[194:197], 0
	v_mfma_f32_16x16x32_bf16 v[64:67], v[160:163], v[194:197], 0
	v_mfma_f32_16x16x32_bf16 v[116:119], v[156:159], v[172:175], v[116:119]
	v_mfma_f32_16x16x32_bf16 v[112:115], v[164:167], v[172:175], v[112:115]
	v_mfma_f32_16x16x32_bf16 v[100:103], v[156:159], v[180:183], v[100:103]
	v_mfma_f32_16x16x32_bf16 v[96:99], v[164:167], v[180:183], v[96:99]
	v_mfma_f32_16x16x32_bf16 v[84:87], v[156:159], v[188:191], v[84:87]
	v_mfma_f32_16x16x32_bf16 v[80:83], v[164:167], v[188:191], v[80:83]
	v_mfma_f32_16x16x32_bf16 v[68:71], v[156:159], v[198:201], v[68:71]
	v_mfma_f32_16x16x32_bf16 v[64:67], v[164:167], v[198:201], v[64:67]
	s_setprio 0
	s_barrier
	s_mov_b32 m0, s21
	s_mov_b32 s6, s38
	s_mov_b32 s7, s39
	ds_read_b128 v[168:171], v139 offset:16384
	ds_read_b128 v[172:175], v139 offset:17408
	ds_read_b128 v[176:179], v139 offset:18432
	ds_read_b128 v[180:183], v139 offset:19456
	ds_read_b128 v[184:187], v139 offset:20480
	ds_read_b128 v[188:191], v139 offset:21504
	ds_read_b128 v[194:197], v139 offset:22528
	ds_read_b128 v[198:201], v139 offset:23552
	buffer_load_dwordx4 v133, s[4:7], s55 offen lds
	s_mov_b32 m0, s22
	s_add_i32 s62, s55, s19
	buffer_load_dwordx4 v135, s[4:7], s55 offen lds
	s_mov_b32 m0, s23
	s_nop 0
	buffer_load_dwordx4 v133, s[4:7], s62 offen lds
	s_mov_b32 m0, s24
	s_nop 0
	buffer_load_dwordx4 v135, s[4:7], s62 offen lds
	s_mov_b32 m0, s20
	s_nop 0
	buffer_load_dwordx4 v132, s[36:39], s61 offen lds
	s_mov_b32 m0, s25
	s_nop 0
	buffer_load_dwordx4 v134, s[36:39], s61 offen lds
	s_waitcnt vmcnt(8)
	s_waitcnt lgkmcnt(0)
	s_barrier
; #define PG8_STAGE(bufoff, rs_, soff_, voff) do { _Pragma("unroll") for (int _i = 0; _i < 2; ++_i) \
;         __builtin_amdgcn_raw_ptr_buffer_load_lds(rs_, (LAS void*)(lds + (bufoff) + ldsw + _i * 8192), 16, (int)(voff)[_i], (int)(soff_), 0, 0); } while (0)
; #define PG8_LDA(dst, b, h) do { _Pragma("unroll") for (int m = 0; m < 4; ++m) dst[m] = PG8_LD2(lds + PG8_SA(b, h) + aoff + m * 2048); } while (0)
; #define PG8_LDB(dst, b, h) do { _Pragma("unroll") for (int n = 0; n < 2; ++n) dst[n] = PG8_LD2(lds + PG8_SB(b, h) + boff + n * 2048); } while (0)
; #define PG8_WAIT_V(n) asm volatile("s_waitcnt vmcnt(" #n ")" ::: "memory")
; #define PG8_WAIT_L(n) asm volatile("s_waitcnt lgkmcnt(" #n ")" ::: "memory")
; #define PG8_BAR __builtin_amdgcn_s_barrier()
; #define PG8_SCHED __builtin_amdgcn_sched_barrier(0)
; template <class Epi, class Sched, bool ALIGN_EPI = false, bool SP2 = false, bool FP8 = false>
; __device__ __forceinline__ void gemm_phase(LAS unsigned char* lds, const Gemm g, const Sched& S, const Epi& E, int wbase) {
;     ...
;             PG8_WAIT_V(8); PG8_WAIT_L(0); PG8_BAR; PG8_MMA(1, 0, At, B0); PG8_MMA(1, 1, At, B1); PG8_BAR; PG8_SCHED;
;             PG8_LDB(B0, 1, 0); PG8_LDB(B1, 1, 1); PG8_SCHED; PG8_LDA(At, 1, 0); PG8_STAGE(PG8_SA(0, 1), rA2, a2 + hstep, voffA);
;             PG8_WAIT_V(8); PG8_WAIT_L(0); PG8_BAR; PG8_MMA(0, 0, At, B0); PG8_MMA(0, 1, At, B1); PG8_BAR; PG8_SCHED;
	s_setprio 1
	v_mfma_f32_16x16x32_bf16 v[60:63], v[128:131], v[168:171], 0
	v_mfma_f32_16x16x32_bf16 v[56:59], v[144:147], v[168:171], 0
	v_mfma_f32_16x16x32_bf16 v[44:47], v[128:131], v[176:179], 0
	v_mfma_f32_16x16x32_bf16 v[40:43], v[144:147], v[176:179], 0
	v_mfma_f32_16x16x32_bf16 v[28:31], v[128:131], v[184:187], 0
	v_mfma_f32_16x16x32_bf16 v[24:27], v[144:147], v[184:187], 0
	v_mfma_f32_16x16x32_bf16 v[12:15], v[128:131], v[194:197], 0
	v_mfma_f32_16x16x32_bf16 v[8:11], v[144:147], v[194:197], 0
	v_mfma_f32_16x16x32_bf16 v[60:63], v[140:143], v[172:175], v[60:63]
	v_mfma_f32_16x16x32_bf16 v[56:59], v[148:151], v[172:175], v[56:59]
	v_mfma_f32_16x16x32_bf16 v[44:47], v[140:143], v[180:183], v[44:47]
	v_mfma_f32_16x16x32_bf16 v[40:43], v[148:151], v[180:183], v[40:43]
	v_mfma_f32_16x16x32_bf16 v[28:31], v[140:143], v[188:191], v[28:31]
	v_mfma_f32_16x16x32_bf16 v[24:27], v[148:151], v[188:191], v[24:27]
	v_mfma_f32_16x16x32_bf16 v[12:15], v[140:143], v[198:201], v[12:15]
	v_mfma_f32_16x16x32_bf16 v[8:11], v[148:151], v[198:201], v[8:11]
	v_mfma_f32_16x16x32_bf16 v[52:55], v[152:155], v[168:171], 0
	v_mfma_f32_16x16x32_bf16 v[48:51], v[160:163], v[168:171], 0
	v_mfma_f32_16x16x32_bf16 v[36:39], v[152:155], v[176:179], 0
	v_mfma_f32_16x16x32_bf16 v[32:35], v[160:163], v[176:179], 0
	v_mfma_f32_16x16x32_bf16 v[20:23], v[152:155], v[184:187], 0
	v_mfma_f32_16x16x32_bf16 v[16:19], v[160:163], v[184:187], 0
	v_mfma_f32_16x16x32_bf16 v[4:7], v[152:155], v[194:197], 0
	v_mfma_f32_16x16x32_bf16 v[0:3], v[160:163], v[194:197], 0
	v_mfma_f32_16x16x32_bf16 v[52:55], v[156:159], v[172:175], v[52:55]
	v_mfma_f32_16x16x32_bf16 v[48:51], v[164:167], v[172:175], v[48:51]
	v_mfma_f32_16x16x32_bf16 v[36:39], v[156:159], v[180:183], v[36:39]
	v_mfma_f32_16x16x32_bf16 v[32:35], v[164:167], v[180:183], v[32:35]
	v_mfma_f32_16x16x32_bf16 v[20:23], v[156:159], v[188:191], v[20:23]
	v_mfma_f32_16x16x32_bf16 v[16:19], v[164:167], v[188:191], v[16:19]
	v_mfma_f32_16x16x32_bf16 v[4:7], v[156:159], v[198:201], v[4:7]
	v_mfma_f32_16x16x32_bf16 v[0:3], v[164:167], v[198:201], v[0:3]
	s_setprio 0
	s_barrier
	v_add_u32_e32 v148, 0x18000, v138
	v_add_u32_e32 v164, 0x1c000, v138
	ds_read_b128 v[128:131], v148
	ds_read_b128 v[140:143], v148 offset:1024
	ds_read_b128 v[144:147], v148 offset:2048
	ds_read_b128 v[148:151], v148 offset:3072
	ds_read_b128 v[152:155], v164
	ds_read_b128 v[156:159], v164 offset:1024
	ds_read_b128 v[160:163], v164 offset:2048
	ds_read_b128 v[164:167], v164 offset:3072
	s_add_i32 s61, s61, s19
	s_mov_b32 m0, s26
	ds_read_b128 v[168:171], v139 offset:32768
	ds_read_b128 v[172:175], v139 offset:33792
	ds_read_b128 v[176:179], v139 offset:34816
	ds_read_b128 v[180:183], v139 offset:35840
	ds_read_b128 v[184:187], v139 offset:36864
	ds_read_b128 v[188:191], v139 offset:37888
	ds_read_b128 v[194:197], v139 offset:38912
	ds_read_b128 v[198:201], v139 offset:39936
	buffer_load_dwordx4 v132, s[36:39], s61 offen lds
	s_mov_b32 m0, s27
	s_nop 0
	buffer_load_dwordx4 v134, s[36:39], s61 offen lds
	s_waitcnt vmcnt(8)
	s_waitcnt lgkmcnt(0)
	s_barrier
	s_setprio 1
	v_mfma_f32_16x16x32_bf16 v[124:127], v[128:131], v[168:171], v[124:127]
	v_mfma_f32_16x16x32_bf16 v[120:123], v[144:147], v[168:171], v[120:123]
	v_mfma_f32_16x16x32_bf16 v[108:111], v[128:131], v[176:179], v[108:111]
	v_mfma_f32_16x16x32_bf16 v[104:107], v[144:147], v[176:179], v[104:107]
	v_mfma_f32_16x16x32_bf16 v[92:95], v[128:131], v[184:187], v[92:95]
	v_mfma_f32_16x16x32_bf16 v[88:91], v[144:147], v[184:187], v[88:91]
	v_mfma_f32_16x16x32_bf16 v[76:79], v[128:131], v[194:197], v[76:79]
	v_mfma_f32_16x16x32_bf16 v[72:75], v[144:147], v[194:197], v[72:75]
	v_mfma_f32_16x16x32_bf16 v[124:127], v[140:143], v[172:175], v[124:127]
	v_mfma_f32_16x16x32_bf16 v[120:123], v[148:151], v[172:175], v[120:123]
	v_mfma_f32_16x16x32_bf16 v[108:111], v[140:143], v[180:183], v[108:111]
	v_mfma_f32_16x16x32_bf16 v[104:107], v[148:151], v[180:183], v[104:107]
	v_mfma_f32_16x16x32_bf16 v[92:95], v[140:143], v[188:191], v[92:95]
	v_mfma_f32_16x16x32_bf16 v[88:91], v[148:151], v[188:191], v[88:91]
	v_mfma_f32_16x16x32_bf16 v[76:79], v[140:143], v[198:201], v[76:79]
	v_mfma_f32_16x16x32_bf16 v[72:75], v[148:151], v[198:201], v[72:75]
	v_mfma_f32_16x16x32_bf16 v[116:119], v[152:155], v[168:171], v[116:119]
	v_mfma_f32_16x16x32_bf16 v[112:115], v[160:163], v[168:171], v[112:115]
	v_mfma_f32_16x16x32_bf16 v[100:103], v[152:155], v[176:179], v[100:103]
	v_mfma_f32_16x16x32_bf16 v[96:99], v[160:163], v[176:179], v[96:99]
	v_mfma_f32_16x16x32_bf16 v[84:87], v[152:155], v[184:187], v[84:87]
	v_mfma_f32_16x16x32_bf16 v[80:83], v[160:163], v[184:187], v[80:83]
	v_mfma_f32_16x16x32_bf16 v[68:71], v[152:155], v[194:197], v[68:71]
	v_mfma_f32_16x16x32_bf16 v[64:67], v[160:163], v[194:197], v[64:67]
	v_mfma_f32_16x16x32_bf16 v[116:119], v[156:159], v[172:175], v[116:119]
	v_mfma_f32_16x16x32_bf16 v[112:115], v[164:167], v[172:175], v[112:115]
	v_mfma_f32_16x16x32_bf16 v[100:103], v[156:159], v[180:183], v[100:103]
	v_mfma_f32_16x16x32_bf16 v[96:99], v[164:167], v[180:183], v[96:99]
	v_mfma_f32_16x16x32_bf16 v[84:87], v[156:159], v[188:191], v[84:87]
	v_mfma_f32_16x16x32_bf16 v[80:83], v[164:167], v[188:191], v[80:83]
	v_mfma_f32_16x16x32_bf16 v[68:71], v[156:159], v[198:201], v[68:71]
	v_mfma_f32_16x16x32_bf16 v[64:67], v[164:167], v[198:201], v[64:67]
	s_setprio 0
	s_barrier
; #define PG8_STAGE(bufoff, rs_, soff_, voff) do { _Pragma("unroll") for (int _i = 0; _i < 2; ++_i) \
;         __builtin_amdgcn_raw_ptr_buffer_load_lds(rs_, (LAS void*)(lds + (bufoff) + ldsw + _i * 8192), 16, (int)(voff)[_i], (int)(soff_), 0, 0); } while (0)
; #define PG8_LDA(dst, b, h) do { _Pragma("unroll") for (int m = 0; m < 4; ++m) dst[m] = PG8_LD2(lds + PG8_SA(b, h) + aoff + m * 2048); } while (0)
; #define PG8_WAIT_V(n) asm volatile("s_waitcnt vmcnt(" #n ")" ::: "memory")
; #define PG8_WAIT_L(n) asm volatile("s_waitcnt lgkmcnt(" #n ")" ::: "memory")
; #define PG8_BAR __builtin_amdgcn_s_barrier()
; #define PG8_SCHED __builtin_amdgcn_sched_barrier(0)
; template <class Epi, class Sched, bool ALIGN_EPI = false, bool SP2 = false, bool FP8 = false>
; __device__ __forceinline__ void gemm_phase(LAS unsigned char* lds, const Gemm g, const Sched& S, const Epi& E, int wbase) {
;     ...
;         for (int t = 0; t < nt; t += 2) {
;     ...
;             PG8_LDA(At, 1, 1); PG8_STAGE(PG8_SB(1, 0), rB2, b3, voffB); PG8_STAGE(PG8_SB(1, 1), rB2, b3 + hstep, voffB); PG8_STAGE(PG8_SA(1, 0), rA2, a3, voffA);
;             PG8_WAIT_V(8); PG8_WAIT_L(0); PG8_BAR; PG8_MMA(1, 0, At, B0); PG8_MMA(1, 1, At, B1); PG8_BAR; PG8_SCHED;
	s_mov_b32 m0, s28
	s_bitset1_b32 s55, 7
	ds_read_b128 v[168:171], v139 offset:49152
	ds_read_b128 v[172:175], v139 offset:50176
	ds_read_b128 v[176:179], v139 offset:51200
	ds_read_b128 v[180:183], v139 offset:52224
	ds_read_b128 v[184:187], v139 offset:53248
	ds_read_b128 v[188:191], v139 offset:54272
	ds_read_b128 v[194:197], v139 offset:55296
	ds_read_b128 v[198:201], v139 offset:56320
	buffer_load_dwordx4 v133, s[4:7], s55 offen lds
	s_mov_b32 m0, s29
	s_nop 0
	buffer_load_dwordx4 v135, s[4:7], s55 offen lds
	s_add_i32 s55, s55, s19
	s_mov_b32 m0, s33
	s_nop 0
	buffer_load_dwordx4 v133, s[4:7], s55 offen lds
	s_mov_b32 m0, s34
	s_nop 0
	buffer_load_dwordx4 v135, s[4:7], s55 offen lds
	s_mov_b32 m0, s30
	s_nop 0
	buffer_load_dwordx4 v132, s[36:39], s54 offen lds
	s_mov_b32 m0, s31
	s_nop 0
	buffer_load_dwordx4 v134, s[36:39], s54 offen lds
	s_waitcnt vmcnt(8)
	s_waitcnt lgkmcnt(0)
	s_barrier
	s_setprio 1
	v_mfma_f32_16x16x32_bf16 v[60:63], v[128:131], v[168:171], v[60:63]
	v_mfma_f32_16x16x32_bf16 v[56:59], v[144:147], v[168:171], v[56:59]
	v_mfma_f32_16x16x32_bf16 v[44:47], v[128:131], v[176:179], v[44:47]
	v_mfma_f32_16x16x32_bf16 v[40:43], v[144:147], v[176:179], v[40:43]
	v_mfma_f32_16x16x32_bf16 v[28:31], v[128:131], v[184:187], v[28:31]
	v_mfma_f32_16x16x32_bf16 v[24:27], v[144:147], v[184:187], v[24:27]
	v_mfma_f32_16x16x32_bf16 v[12:15], v[128:131], v[194:197], v[12:15]
	v_mfma_f32_16x16x32_bf16 v[8:11], v[144:147], v[194:197], v[8:11]
	v_mfma_f32_16x16x32_bf16 v[60:63], v[140:143], v[172:175], v[60:63]
	v_mfma_f32_16x16x32_bf16 v[56:59], v[148:151], v[172:175], v[56:59]
	v_mfma_f32_16x16x32_bf16 v[44:47], v[140:143], v[180:183], v[44:47]
	v_mfma_f32_16x16x32_bf16 v[40:43], v[148:151], v[180:183], v[40:43]
	v_mfma_f32_16x16x32_bf16 v[28:31], v[140:143], v[188:191], v[28:31]
	v_mfma_f32_16x16x32_bf16 v[24:27], v[148:151], v[188:191], v[24:27]
	v_mfma_f32_16x16x32_bf16 v[12:15], v[140:143], v[198:201], v[12:15]
	v_mfma_f32_16x16x32_bf16 v[8:11], v[148:151], v[198:201], v[8:11]
	v_mfma_f32_16x16x32_bf16 v[52:55], v[152:155], v[168:171], v[52:55]
	v_mfma_f32_16x16x32_bf16 v[48:51], v[160:163], v[168:171], v[48:51]
	v_mfma_f32_16x16x32_bf16 v[36:39], v[152:155], v[176:179], v[36:39]
	v_mfma_f32_16x16x32_bf16 v[32:35], v[160:163], v[176:179], v[32:35]
	v_mfma_f32_16x16x32_bf16 v[20:23], v[152:155], v[184:187], v[20:23]
	v_mfma_f32_16x16x32_bf16 v[16:19], v[160:163], v[184:187], v[16:19]
	v_mfma_f32_16x16x32_bf16 v[4:7], v[152:155], v[194:197], v[4:7]
	v_mfma_f32_16x16x32_bf16 v[0:3], v[160:163], v[194:197], v[0:3]
	v_mfma_f32_16x16x32_bf16 v[52:55], v[156:159], v[172:175], v[52:55]
	v_mfma_f32_16x16x32_bf16 v[48:51], v[164:167], v[172:175], v[48:51]
	v_mfma_f32_16x16x32_bf16 v[36:39], v[156:159], v[180:183], v[36:39]
	v_mfma_f32_16x16x32_bf16 v[32:35], v[164:167], v[180:183], v[32:35]
	v_mfma_f32_16x16x32_bf16 v[20:23], v[156:159], v[188:191], v[20:23]
	v_mfma_f32_16x16x32_bf16 v[16:19], v[164:167], v[188:191], v[16:19]
	v_mfma_f32_16x16x32_bf16 v[4:7], v[156:159], v[198:201], v[4:7]
	v_mfma_f32_16x16x32_bf16 v[0:3], v[164:167], v[198:201], v[0:3]
	s_setprio 0
	s_barrier
	s_add_i32 s60, s60, 2
	s_addk_i32 s58, 0x100
	s_addk_i32 s59, 0x100
	s_cmp_ge_i32 s60, s35
	s_cbranch_scc0 .LBB0_450
	s_branch .Lzp_after_450

; #define PG8_BAR __builtin_amdgcn_s_barrier()
; template <class Epi, class Sched, bool ALIGN_EPI = false, bool SP2 = false, bool FP8 = false>
; __device__ __forceinline__ void gemm_phase(LAS unsigned char* lds, const Gemm g, const Sched& S, const Epi& E, int wbase) {
;     ...
;         if constexpr (ALIGN_EPI) { if (wr == 0) PG8_BAR; }
;         { int fr_ = fr, fq_ = fq; asm volatile("" : "+v"(fr_), "+v"(fq_));
;           if constexpr (Epi::HAS_PRE) E(acc, cur, wr, wc, fr_, fq_, pre_); else E(acc, cur, wr, wc, fr_, fq_); } S.done(cur);
.Lzp_after_450:
	s_and_b64 vcc, exec, s[12:13]
	s_cbranch_vccz .LBB0_453

; #define PG8_STAGE(bufoff, rs_, soff_, voff) do { _Pragma("unroll") for (int _i = 0; _i < 2; ++_i) \
;         __builtin_amdgcn_raw_ptr_buffer_load_lds(rs_, (LAS void*)(lds + (bufoff) + ldsw + _i * 8192), 16, (int)(voff)[_i], (int)(soff_), 0, 0); } while (0)
; #define PG8_LDA(dst, b, h) do { _Pragma("unroll") for (int m = 0; m < 4; ++m) dst[m] = PG8_LD2(lds + PG8_SA(b, h) + aoff + m * 2048); } while (0)
; #define PG8_LDB(dst, b, h) do { _Pragma("unroll") for (int n = 0; n < 2; ++n) dst[n] = PG8_LD2(lds + PG8_SB(b, h) + boff + n * 2048); } while (0)
; #define PG8_WAIT_V(n) asm volatile("s_waitcnt vmcnt(" #n ")" ::: "memory")
; #define PG8_WAIT_L(n) asm volatile("s_waitcnt lgkmcnt(" #n ")" ::: "memory")
; #define PG8_BAR __builtin_amdgcn_s_barrier()
; #define PG8_SCHED __builtin_amdgcn_sched_barrier(0)
; template <class Epi, class Sched, bool ALIGN_EPI = false, bool SP2 = false, bool FP8 = false>
; __device__ __forceinline__ void gemm_phase(LAS unsigned char* lds, const Gemm g, const Sched& S, const Epi& E, int wbase) {
;     ...
;             PG8_LDB(B0, 0, 0); PG8_LDB(B1, 0, 1); PG8_SCHED; PG8_LDA(At, 0, 0); PG8_STAGE(PG8_SA(1, 1), rAc, a1 + hstep, voffA);
;             PG8_WAIT_V(8); PG8_WAIT_L(0); PG8_BAR; PG8_MMA(0, 0, At, B0); PG8_MMA(0, 1, At, B1); PG8_BAR; PG8_SCHED;
;             PG8_LDA(At, 0, 1); PG8_STAGE(PG8_SB(0, 0), rB2, b2, voffB); PG8_STAGE(PG8_SB(0, 1), rB2, b2 + hstep, voffB); PG8_STAGE(PG8_SA(0, 0), rA2, a2, voffA);
;             PG8_WAIT_V(8); PG8_WAIT_L(0); PG8_BAR; PG8_MMA(1, 0, At, B0); PG8_MMA(1, 1, At, B1); PG8_BAR; PG8_SCHED;
.LBB0_924:
	s_lshl_b32 s79, s77, 18
	s_andn2_b64 vcc, exec, s[22:23]
	s_lshl_b32 s80, s76, 18
	s_cbranch_vccnz .LBB0_928
	s_and_b64 s[2:3], s[26:27], exec
	s_waitcnt vmcnt(37)
	s_waitcnt vmcnt(36)
	s_waitcnt vmcnt(35)
	s_waitcnt vmcnt(32)
	s_waitcnt vmcnt(31)
	s_waitcnt vmcnt(28)
	s_waitcnt vmcnt(27)
	s_waitcnt vmcnt(24)
	s_waitcnt vmcnt(23)
	v_mov_b32_e32 v159, v233
	s_cselect_b32 s2, s79, s4
	s_cselect_b32 s3, s80, s5
	s_addk_i32 s4, 0x80
	s_addk_i32 s5, 0x100
	s_mov_b32 s11, 0
	s_waitcnt vmcnt(0)
	v_add_u32_e32 v120, 0x10000, v160
	ds_read_b128 v[132:135], v120
	ds_read_b128 v[136:139], v120 offset:1024
	ds_read_b128 v[140:143], v120 offset:2048
	ds_read_b128 v[144:147], v120 offset:3072
	v_add_u32_e32 v120, 0x14000, v160
	ds_read_b128 v[162:165], v120
	ds_read_b128 v[166:169], v120 offset:1024
	ds_read_b128 v[170:173], v120 offset:2048
	ds_read_b128 v[174:177], v120 offset:3072
	s_add_i32 s14, s4, 0x80
	s_cmp_eq_u32 s60, s11
	s_cselect_b32 s66, s2, s14
	s_cselect_b32 s55, s3, s5
	s_or_b32 s54, s66, 0x80
	s_add_i32 s14, s30, s4
	s_mov_b32 m0, s61
	ds_read_b128 v[178:181], v161
	ds_read_b128 v[182:185], v161 offset:1024
	ds_read_b128 v[194:197], v161 offset:2048
	ds_read_b128 v[198:201], v161 offset:3072
	ds_read_b128 v[202:205], v161 offset:4096
	ds_read_b128 v[206:209], v161 offset:5120
	ds_read_b128 v[210:213], v161 offset:6144
	ds_read_b128 v[214:217], v161 offset:7168
	buffer_load_dwordx4 v222, s[36:39], s14 offen lds
	s_mov_b32 m0, s62
	s_nop 0
	buffer_load_dwordx4 v156, s[36:39], s14 offen lds
	s_waitcnt vmcnt(8)
	s_waitcnt lgkmcnt(0)
	s_barrier
	s_setprio 1
	v_mfma_f32_16x16x128_f8f6f4 v[124:127], v[140:147], v[178:185], 0
	v_mfma_f32_16x16x128_f8f6f4 v[108:111], v[132:139], v[194:201], 0
	v_mfma_f32_16x16x128_f8f6f4 v[104:107], v[140:147], v[194:201], 0
	v_mfma_f32_16x16x128_f8f6f4 v[120:123], v[132:139], v[178:185], 0
	v_mfma_f32_16x16x128_f8f6f4 v[148:151], v[132:139], v[202:209], 0
	v_mfma_f32_16x16x128_f8f6f4 v[186:189], v[140:147], v[202:209], 0
	v_mfma_f32_16x16x128_f8f6f4 v[218:221], v[132:139], v[210:217], 0
	v_mfma_f32_16x16x128_f8f6f4 v[226:229], v[140:147], v[210:217], 0
	v_mfma_f32_16x16x128_f8f6f4 v[116:119], v[162:169], v[178:185], 0
	v_mfma_f32_16x16x128_f8f6f4 v[112:115], v[170:177], v[178:185], 0
	v_mfma_f32_16x16x128_f8f6f4 v[100:103], v[162:169], v[194:201], 0
	v_mfma_f32_16x16x128_f8f6f4 v[96:99], v[170:177], v[194:201], 0
	v_mfma_f32_16x16x128_f8f6f4 v[178:181], v[162:169], v[202:209], 0
	v_mfma_f32_16x16x128_f8f6f4 v[182:185], v[170:177], v[202:209], 0
	v_mfma_f32_16x16x128_f8f6f4 v[194:197], v[162:169], v[210:217], 0
	v_mfma_f32_16x16x128_f8f6f4 v[198:201], v[170:177], v[210:217], 0
	s_setprio 0
	s_barrier
	s_mov_b32 m0, s33
	s_mov_b32 s14, s38
	s_mov_b32 s15, s39
	s_nop 1
	ds_read_b128 v[64:67], v161 offset:16384
	ds_read_b128 v[68:71], v161 offset:17408
	ds_read_b128 v[72:75], v161 offset:18432
	ds_read_b128 v[76:79], v161 offset:19456
	ds_read_b128 v[80:83], v161 offset:20480
	ds_read_b128 v[84:87], v161 offset:21504
	ds_read_b128 v[88:91], v161 offset:22528
	ds_read_b128 v[92:95], v161 offset:23552
	buffer_load_dwordx4 v223, s[12:15], s55 offen lds
	s_mov_b32 m0, s34
	s_add_i32 s67, s55, s30
	buffer_load_dwordx4 v157, s[12:15], s55 offen lds
	s_mov_b32 m0, s35
	s_nop 0
	buffer_load_dwordx4 v223, s[12:15], s67 offen lds
	s_mov_b32 m0, s41
	s_nop 0
	buffer_load_dwordx4 v157, s[12:15], s67 offen lds
	s_mov_b32 m0, s31
	s_nop 0
	buffer_load_dwordx4 v222, s[36:39], s66 offen lds
	s_mov_b32 m0, s42
	s_nop 0
	buffer_load_dwordx4 v156, s[36:39], s66 offen lds
	s_waitcnt vmcnt(8)
	s_waitcnt lgkmcnt(0)
	s_barrier
	s_setprio 1
	v_mfma_f32_16x16x128_f8f6f4 v[60:63], v[132:139], v[64:71], 0
	v_mfma_f32_16x16x128_f8f6f4 v[56:59], v[140:147], v[64:71], 0
	v_mfma_f32_16x16x128_f8f6f4 v[202:205], v[132:139], v[72:79], 0
	v_mfma_f32_16x16x128_f8f6f4 v[206:209], v[140:147], v[72:79], 0
	v_mfma_f32_16x16x128_f8f6f4 v[210:213], v[132:139], v[80:87], 0
	v_mfma_f32_16x16x128_f8f6f4 v[214:217], v[140:147], v[80:87], 0
	v_mfma_f32_16x16x128_f8f6f4 v[230:233], v[132:139], v[88:95], 0
	v_mfma_f32_16x16x128_f8f6f4 v[234:237], v[140:147], v[88:95], 0
	v_mfma_f32_16x16x128_f8f6f4 v[52:55], v[162:169], v[64:71], 0
	v_mfma_f32_16x16x128_f8f6f4 v[48:51], v[170:177], v[64:71], 0
	v_mfma_f32_16x16x128_f8f6f4 v[238:241], v[162:169], v[72:79], 0
	v_mfma_f32_16x16x128_f8f6f4 v[242:245], v[170:177], v[72:79], 0
	v_mfma_f32_16x16x128_f8f6f4 v[246:249], v[162:169], v[80:87], 0
	v_mfma_f32_16x16x128_f8f6f4 v[250:253], v[170:177], v[80:87], 0
	v_mfma_f32_16x16x128_f8f6f4 v[190:193], v[162:169], v[88:95], 0
	v_mfma_f32_16x16x128_f8f6f4 v[152:155], v[170:177], v[88:95], 0
	s_setprio 0
	s_barrier
; #define PG8_STAGE(bufoff, rs_, soff_, voff) do { _Pragma("unroll") for (int _i = 0; _i < 2; ++_i) \
;         __builtin_amdgcn_raw_ptr_buffer_load_lds(rs_, (LAS void*)(lds + (bufoff) + ldsw + _i * 8192), 16, (int)(voff)[_i], (int)(soff_), 0, 0); } while (0)
; #define PG8_LDA(dst, b, h) do { _Pragma("unroll") for (int m = 0; m < 4; ++m) dst[m] = PG8_LD2(lds + PG8_SA(b, h) + aoff + m * 2048); } while (0)
; #define PG8_LDB(dst, b, h) do { _Pragma("unroll") for (int n = 0; n < 2; ++n) dst[n] = PG8_LD2(lds + PG8_SB(b, h) + boff + n * 2048); } while (0)
; #define PG8_WAIT_V(n) asm volatile("s_waitcnt vmcnt(" #n ")" ::: "memory")
; #define PG8_WAIT_L(n) asm volatile("s_waitcnt lgkmcnt(" #n ")" ::: "memory")
; #define PG8_BAR __builtin_amdgcn_s_barrier()
; #define PG8_SCHED __builtin_amdgcn_sched_barrier(0)
; template <class Epi, class Sched, bool ALIGN_EPI = false, bool SP2 = false, bool FP8 = false>
; __device__ __forceinline__ void gemm_phase(LAS unsigned char* lds, const Gemm g, const Sched& S, const Epi& E, int wbase) {
;     ...
;         for (int t = 0; t < nt; t += 2) {
;     ...
;             PG8_LDB(B0, 1, 0); PG8_LDB(B1, 1, 1); PG8_SCHED; PG8_LDA(At, 1, 0); PG8_STAGE(PG8_SA(0, 1), rA2, a2 + hstep, voffA);
;             PG8_WAIT_V(8); PG8_WAIT_L(0); PG8_BAR; PG8_MMA(0, 0, At, B0); PG8_MMA(0, 1, At, B1); PG8_BAR; PG8_SCHED;
;             PG8_LDA(At, 1, 1); PG8_STAGE(PG8_SB(1, 0), rB2, b3, voffB); PG8_STAGE(PG8_SB(1, 1), rB2, b3 + hstep, voffB); PG8_STAGE(PG8_SA(1, 0), rA2, a3, voffA);
;             PG8_WAIT_V(8); PG8_WAIT_L(0); PG8_BAR; PG8_MMA(1, 0, At, B0); PG8_MMA(1, 1, At, B1); PG8_BAR; PG8_SCHED;
	v_add_u32_e32 v8, 0x18000, v160
	s_nop 3
	ds_read_b128 v[0:3], v8
	ds_read_b128 v[4:7], v8 offset:1024
	ds_read_b128 v[16:19], v8 offset:2048
	ds_read_b128 v[20:23], v8 offset:3072
	v_add_u32_e32 v8, 0x1c000, v160
	ds_read_b128 v[132:135], v8
	ds_read_b128 v[136:139], v8 offset:1024
	ds_read_b128 v[140:143], v8 offset:2048
	ds_read_b128 v[144:147], v8 offset:3072
	s_add_i32 s66, s66, s30
	s_mov_b32 m0, s43
	ds_read_b128 v[8:11], v161 offset:32768
	ds_read_b128 v[12:15], v161 offset:33792
	ds_read_b128 v[24:27], v161 offset:34816
	ds_read_b128 v[28:31], v161 offset:35840
	ds_read_b128 v[32:35], v161 offset:36864
	ds_read_b128 v[36:39], v161 offset:37888
	ds_read_b128 v[40:43], v161 offset:38912
	ds_read_b128 v[44:47], v161 offset:39936
	buffer_load_dwordx4 v222, s[36:39], s66 offen lds
	s_mov_b32 m0, s44
	s_nop 0
	buffer_load_dwordx4 v156, s[36:39], s66 offen lds
	s_waitcnt vmcnt(8)
	s_waitcnt lgkmcnt(0)
	s_barrier
	s_setprio 1
	v_mfma_f32_16x16x128_f8f6f4 v[128:131], v[0:7], v[8:15], v[120:123]
	v_mfma_f32_16x16x128_f8f6f4 v[124:127], v[16:23], v[8:15], v[124:127]
	v_mfma_f32_16x16x128_f8f6f4 v[108:111], v[0:7], v[24:31], v[108:111]
	v_mfma_f32_16x16x128_f8f6f4 v[104:107], v[16:23], v[24:31], v[104:107]
	v_mfma_f32_16x16x128_f8f6f4 v[92:95], v[0:7], v[32:39], v[148:151]
	v_mfma_f32_16x16x128_f8f6f4 v[88:91], v[16:23], v[32:39], v[186:189]
	v_mfma_f32_16x16x128_f8f6f4 v[76:79], v[0:7], v[40:47], v[218:221]
	v_mfma_f32_16x16x128_f8f6f4 v[72:75], v[16:23], v[40:47], v[226:229]
	v_mfma_f32_16x16x128_f8f6f4 v[116:119], v[132:139], v[8:15], v[116:119]
	v_mfma_f32_16x16x128_f8f6f4 v[112:115], v[140:147], v[8:15], v[112:115]
	v_mfma_f32_16x16x128_f8f6f4 v[100:103], v[132:139], v[24:31], v[100:103]
	v_mfma_f32_16x16x128_f8f6f4 v[96:99], v[140:147], v[24:31], v[96:99]
	v_mfma_f32_16x16x128_f8f6f4 v[84:87], v[132:139], v[32:39], v[178:181]
	v_mfma_f32_16x16x128_f8f6f4 v[80:83], v[140:147], v[32:39], v[182:185]
	v_mfma_f32_16x16x128_f8f6f4 v[68:71], v[132:139], v[40:47], v[194:197]
	v_mfma_f32_16x16x128_f8f6f4 v[64:67], v[140:147], v[40:47], v[198:201]
	s_setprio 0
	s_barrier
	s_mov_b32 m0, s45
	s_bitset1_b32 s55, 7
	ds_read_b128 v[32:35], v161 offset:49152
	ds_read_b128 v[36:39], v161 offset:50176
	ds_read_b128 v[162:165], v161 offset:51200
	ds_read_b128 v[166:169], v161 offset:52224
	ds_read_b128 v[170:173], v161 offset:53248
	ds_read_b128 v[174:177], v161 offset:54272
	ds_read_b128 v[178:181], v161 offset:55296
	ds_read_b128 v[182:185], v161 offset:56320
	buffer_load_dwordx4 v223, s[12:15], s55 offen lds
	s_mov_b32 m0, s46
	s_nop 0
	buffer_load_dwordx4 v157, s[12:15], s55 offen lds
	s_add_i32 s55, s55, s30
	s_mov_b32 m0, s52
	s_nop 0
	buffer_load_dwordx4 v223, s[12:15], s55 offen lds
	s_mov_b32 m0, s53
	s_nop 0
	buffer_load_dwordx4 v157, s[12:15], s55 offen lds
	s_mov_b32 m0, s47
	s_nop 0
	buffer_load_dwordx4 v222, s[36:39], s54 offen lds
	s_mov_b32 m0, s48
	s_nop 0
	buffer_load_dwordx4 v156, s[36:39], s54 offen lds
	s_waitcnt vmcnt(8)
	s_waitcnt lgkmcnt(0)
	s_barrier
	s_setprio 1
	v_mfma_f32_16x16x128_f8f6f4 v[60:63], v[0:7], v[32:39], v[60:63]
	v_mfma_f32_16x16x128_f8f6f4 v[56:59], v[16:23], v[32:39], v[56:59]
	v_mfma_f32_16x16x128_f8f6f4 v[44:47], v[0:7], v[162:169], v[202:205]
	v_mfma_f32_16x16x128_f8f6f4 v[40:43], v[16:23], v[162:169], v[206:209]
	v_mfma_f32_16x16x128_f8f6f4 v[28:31], v[0:7], v[170:177], v[210:213]
	v_mfma_f32_16x16x128_f8f6f4 v[24:27], v[16:23], v[170:177], v[214:217]
	v_mfma_f32_16x16x128_f8f6f4 v[12:15], v[0:7], v[178:185], v[230:233]
	v_mfma_f32_16x16x128_f8f6f4 v[8:11], v[16:23], v[178:185], v[234:237]
	v_mfma_f32_16x16x128_f8f6f4 v[52:55], v[132:139], v[32:39], v[52:55]
	v_mfma_f32_16x16x128_f8f6f4 v[48:51], v[140:147], v[32:39], v[48:51]
	v_mfma_f32_16x16x128_f8f6f4 v[36:39], v[132:139], v[162:169], v[238:241]
	v_mfma_f32_16x16x128_f8f6f4 v[32:35], v[140:147], v[162:169], v[242:245]
	v_mfma_f32_16x16x128_f8f6f4 v[20:23], v[132:139], v[170:177], v[246:249]
	v_mfma_f32_16x16x128_f8f6f4 v[16:19], v[140:147], v[170:177], v[250:253]
	v_mfma_f32_16x16x128_f8f6f4 v[4:7], v[132:139], v[178:185], v[190:193]
	v_mfma_f32_16x16x128_f8f6f4 v[0:3], v[140:147], v[178:185], v[152:155]
	s_setprio 0
	s_barrier
	s_add_i32 s11, s11, 2
	s_addk_i32 s4, 0x100
	s_addk_i32 s5, 0x100
	s_cmp_ge_i32 s11, s58
	s_cbranch_scc0 .LBB0_926
	s_branch .Lzp_after_926

; #define PG8_BAR __builtin_amdgcn_s_barrier()
; template <class Epi, class Sched, bool ALIGN_EPI = false, bool SP2 = false, bool FP8 = false>
; __device__ __forceinline__ void gemm_phase(LAS unsigned char* lds, const Gemm g, const Sched& S, const Epi& E, int wbase) {
;     ...
;         if constexpr (ALIGN_EPI) { if (wr == 0) PG8_BAR; }
;         { int fr_ = fr, fq_ = fq; asm volatile("" : "+v"(fr_), "+v"(fq_));
;           if constexpr (Epi::HAS_PRE) E(acc, cur, wr, wc, fr_, fq_, pre_); else E(acc, cur, wr, wc, fr_, fq_); } S.done(cur);
.Lzp_after_926:
	v_mov_b32_e32 v230, 0x358637bd
	v_mov_b32_e32 v233, v159
	v_mov_b32_e32 v231, 1
	v_mov_b32_e32 v234, 0xff61b1e6
	s_and_b64 vcc, exec, s[24:25]
	s_cbranch_vccnz .LBB0_929
	s_branch .LBB0_930

; #define PG8_STAGE(bufoff, rs_, soff_, voff) do { _Pragma("unroll") for (int _i = 0; _i < 2; ++_i) \
;         __builtin_amdgcn_raw_ptr_buffer_load_lds(rs_, (LAS void*)(lds + (bufoff) + ldsw + _i * 8192), 16, (int)(voff)[_i], (int)(soff_), 0, 0); } while (0)
; #define PG8_LDA(dst, b, h) do { _Pragma("unroll") for (int m = 0; m < 4; ++m) dst[m] = PG8_LD2(lds + PG8_SA(b, h) + aoff + m * 2048); } while (0)
; #define PG8_LDB(dst, b, h) do { _Pragma("unroll") for (int n = 0; n < 2; ++n) dst[n] = PG8_LD2(lds + PG8_SB(b, h) + boff + n * 2048); } while (0)
; #define PG8_WAIT_V(n) asm volatile("s_waitcnt vmcnt(" #n ")" ::: "memory")
; #define PG8_WAIT_L(n) asm volatile("s_waitcnt lgkmcnt(" #n ")" ::: "memory")
; #define PG8_BAR __builtin_amdgcn_s_barrier()
; #define PG8_SCHED __builtin_amdgcn_sched_barrier(0)
; template <class Epi, class Sched, bool ALIGN_EPI = false, bool SP2 = false, bool FP8 = false>
; __device__ __forceinline__ void gemm_phase(LAS unsigned char* lds, const Gemm g, const Sched& S, const Epi& E, int wbase) {
;     ...
;             const unsigned a2 = last ? nA : cA + (unsigned)(t + 2) * kstep, b2 = last ? nB : cB + (unsigned)(t + 2) * kstep; const rsrc_t rA2 = (Sched::TWO && last) ? rAn : rAc, rB2 = (Sched::TWO && last) ? rBn : rBc;
;             const unsigned a3 = a2 + kstep, b3 = b2 + kstep;
;             if (last && has_next) S.a_ready(nxt);
;             if constexpr (SP2) {
;             PG8_LDB(B0, 0, 0); PG8_LDB(B1, 0, 1); PG8_SCHED; PG8_LDA(At, 0, 0); PG8_STAGE(PG8_SA(1, 1), rAc, a1 + hstep, voffA);
;             PG8_WAIT_V(8); PG8_WAIT_L(0); PG8_BAR; PG8_MMA(0, 0, At, B0); PG8_MMA(0, 1, At, B1); PG8_BAR; PG8_SCHED;
;             PG8_LDA(At, 0, 1); PG8_STAGE(PG8_SB(0, 0), rB2, b2, voffB); PG8_STAGE(PG8_SB(0, 1), rB2, b2 + hstep, voffB); PG8_STAGE(PG8_SA(0, 0), rA2, a2, voffA);
;             PG8_WAIT_V(8); PG8_WAIT_L(0); PG8_BAR; PG8_MMA(1, 0, At, B0); PG8_MMA(1, 1, At, B1); PG8_BAR; PG8_SCHED;
.LBB0_1002:
	s_lshl_b32 s81, s80, 19
	s_andn2_b64 vcc, exec, s[24:25]
	s_lshl_b32 s82, s79, 19
	s_cbranch_vccnz .LBB0_1058
	s_and_b64 s[2:3], s[28:29], exec
	s_waitcnt vmcnt(37)
	s_waitcnt vmcnt(36)
	s_waitcnt vmcnt(35)
	s_waitcnt vmcnt(32)
	s_waitcnt vmcnt(31)
	s_waitcnt vmcnt(27)
	s_waitcnt vmcnt(26)
	s_waitcnt vmcnt(24)
	s_waitcnt vmcnt(23)
	s_cselect_b32 s2, s81, s4
	s_cselect_b32 s3, s82, s5
	s_addk_i32 s4, 0x80
	s_addk_i32 s5, 0x100
	s_mov_b32 s11, 0
	s_waitcnt vmcnt(0)
	v_add_u32_e32 v132, 0x10000, v180
	v_add_u32_e32 v156, 0x14000, v180
	ds_read_b128 v[96:99], v132
	ds_read_b128 v[108:111], v132 offset:1024
	ds_read_b128 v[120:123], v132 offset:2048
	ds_read_b128 v[132:135], v132 offset:3072
	ds_read_b128 v[136:139], v156
	ds_read_b128 v[144:147], v156 offset:1024
	ds_read_b128 v[152:155], v156 offset:2048
	ds_read_b128 v[156:159], v156 offset:3072
	s_add_i32 s14, s4, 0x80
	s_cmp_eq_u32 s62, s11
	s_cselect_b32 s66, s2, s14
	s_cselect_b32 s55, s3, s5
	s_or_b32 s54, s66, 0x80
	s_add_i32 s14, s33, s4
	s_mov_b32 m0, s63
	ds_read_b128 v[160:163], v181
	ds_read_b128 v[164:167], v181 offset:1024
	ds_read_b128 v[168:171], v181 offset:2048
	ds_read_b128 v[182:185], v181 offset:3072
	ds_read_b128 v[186:189], v181 offset:4096
	ds_read_b128 v[190:193], v181 offset:5120
	ds_read_b128 v[194:197], v181 offset:6144
	ds_read_b128 v[198:201], v181 offset:7168
	buffer_load_dwordx4 v174, s[36:39], s14 offen lds
	s_mov_b32 m0, s65
	s_nop 0
	buffer_load_dwordx4 v176, s[36:39], s14 offen lds
	s_waitcnt vmcnt(8)
	s_waitcnt lgkmcnt(0)
	s_barrier
	s_setprio 1
	v_mfma_f32_16x16x32_bf16 v[148:151], v[96:99], v[160:163], 0
	v_mfma_f32_16x16x32_bf16 v[140:143], v[120:123], v[160:163], 0
	v_mfma_f32_16x16x32_bf16 v[116:119], v[96:99], v[168:171], 0
	v_mfma_f32_16x16x32_bf16 v[112:115], v[120:123], v[168:171], 0
	v_mfma_f32_16x16x32_bf16 v[92:95], v[96:99], v[186:189], 0
	v_mfma_f32_16x16x32_bf16 v[88:91], v[120:123], v[186:189], 0
	v_mfma_f32_16x16x32_bf16 v[76:79], v[96:99], v[194:197], 0
	v_mfma_f32_16x16x32_bf16 v[72:75], v[120:123], v[194:197], 0
	v_mfma_f32_16x16x32_bf16 v[148:151], v[108:111], v[164:167], v[148:151]
	v_mfma_f32_16x16x32_bf16 v[140:143], v[132:135], v[164:167], v[140:143]
	v_mfma_f32_16x16x32_bf16 v[116:119], v[108:111], v[182:185], v[116:119]
	v_mfma_f32_16x16x32_bf16 v[112:115], v[132:135], v[182:185], v[112:115]
	v_mfma_f32_16x16x32_bf16 v[92:95], v[108:111], v[190:193], v[92:95]
	v_mfma_f32_16x16x32_bf16 v[88:91], v[132:135], v[190:193], v[88:91]
	v_mfma_f32_16x16x32_bf16 v[76:79], v[108:111], v[198:201], v[76:79]
	v_mfma_f32_16x16x32_bf16 v[72:75], v[132:135], v[198:201], v[72:75]
	v_mfma_f32_16x16x32_bf16 v[128:131], v[136:139], v[160:163], 0
	v_mfma_f32_16x16x32_bf16 v[124:127], v[152:155], v[160:163], 0
	v_mfma_f32_16x16x32_bf16 v[104:107], v[136:139], v[168:171], 0
	v_mfma_f32_16x16x32_bf16 v[100:103], v[152:155], v[168:171], 0
	v_mfma_f32_16x16x32_bf16 v[84:87], v[136:139], v[186:189], 0
	v_mfma_f32_16x16x32_bf16 v[80:83], v[152:155], v[186:189], 0
	v_mfma_f32_16x16x32_bf16 v[68:71], v[136:139], v[194:197], 0
	v_mfma_f32_16x16x32_bf16 v[64:67], v[152:155], v[194:197], 0
	v_mfma_f32_16x16x32_bf16 v[128:131], v[144:147], v[164:167], v[128:131]
	v_mfma_f32_16x16x32_bf16 v[124:127], v[156:159], v[164:167], v[124:127]
	v_mfma_f32_16x16x32_bf16 v[104:107], v[144:147], v[182:185], v[104:107]
	v_mfma_f32_16x16x32_bf16 v[100:103], v[156:159], v[182:185], v[100:103]
	v_mfma_f32_16x16x32_bf16 v[84:87], v[144:147], v[190:193], v[84:87]
	v_mfma_f32_16x16x32_bf16 v[80:83], v[156:159], v[190:193], v[80:83]
	v_mfma_f32_16x16x32_bf16 v[68:71], v[144:147], v[198:201], v[68:71]
	v_mfma_f32_16x16x32_bf16 v[64:67], v[156:159], v[198:201], v[64:67]
	s_setprio 0
	s_barrier
	s_mov_b32 m0, s35
	s_mov_b32 s14, s38
	s_mov_b32 s15, s39
	ds_read_b128 v[160:163], v181 offset:16384
	ds_read_b128 v[164:167], v181 offset:17408
	ds_read_b128 v[168:171], v181 offset:18432
	ds_read_b128 v[182:185], v181 offset:19456
	ds_read_b128 v[186:189], v181 offset:20480
	ds_read_b128 v[190:193], v181 offset:21504
	ds_read_b128 v[194:197], v181 offset:22528
	ds_read_b128 v[198:201], v181 offset:23552
	buffer_load_dwordx4 v175, s[12:15], s55 offen lds
	s_mov_b32 m0, s41
	s_add_i32 s67, s55, s33
	buffer_load_dwordx4 v177, s[12:15], s55 offen lds
	s_mov_b32 m0, s42
	s_nop 0
	buffer_load_dwordx4 v175, s[12:15], s67 offen lds
	s_mov_b32 m0, s43
	s_nop 0
	buffer_load_dwordx4 v177, s[12:15], s67 offen lds
	s_mov_b32 m0, s34
	s_nop 0
	buffer_load_dwordx4 v174, s[36:39], s66 offen lds
	s_mov_b32 m0, s44
	s_nop 0
	buffer_load_dwordx4 v176, s[36:39], s66 offen lds
	s_waitcnt vmcnt(8)
	s_waitcnt lgkmcnt(0)
	s_barrier
; #define PG8_STAGE(bufoff, rs_, soff_, voff) do { _Pragma("unroll") for (int _i = 0; _i < 2; ++_i) \
;         __builtin_amdgcn_raw_ptr_buffer_load_lds(rs_, (LAS void*)(lds + (bufoff) + ldsw + _i * 8192), 16, (int)(voff)[_i], (int)(soff_), 0, 0); } while (0)
; #define PG8_LDA(dst, b, h) do { _Pragma("unroll") for (int m = 0; m < 4; ++m) dst[m] = PG8_LD2(lds + PG8_SA(b, h) + aoff + m * 2048); } while (0)
; #define PG8_LDB(dst, b, h) do { _Pragma("unroll") for (int n = 0; n < 2; ++n) dst[n] = PG8_LD2(lds + PG8_SB(b, h) + boff + n * 2048); } while (0)
; #define PG8_WAIT_V(n) asm volatile("s_waitcnt vmcnt(" #n ")" ::: "memory")
; #define PG8_WAIT_L(n) asm volatile("s_waitcnt lgkmcnt(" #n ")" ::: "memory")
; #define PG8_BAR __builtin_amdgcn_s_barrier()
; #define PG8_SCHED __builtin_amdgcn_sched_barrier(0)
; template <class Epi, class Sched, bool ALIGN_EPI = false, bool SP2 = false, bool FP8 = false>
; __device__ __forceinline__ void gemm_phase(LAS unsigned char* lds, const Gemm g, const Sched& S, const Epi& E, int wbase) {
;     ...
;             PG8_WAIT_V(8); PG8_WAIT_L(0); PG8_BAR; PG8_MMA(1, 0, At, B0); PG8_MMA(1, 1, At, B1); PG8_BAR; PG8_SCHED;
;             PG8_LDB(B0, 1, 0); PG8_LDB(B1, 1, 1); PG8_SCHED; PG8_LDA(At, 1, 0); PG8_STAGE(PG8_SA(0, 1), rA2, a2 + hstep, voffA);
;             PG8_WAIT_V(8); PG8_WAIT_L(0); PG8_BAR; PG8_MMA(0, 0, At, B0); PG8_MMA(0, 1, At, B1); PG8_BAR; PG8_SCHED;
	s_setprio 1
	v_mfma_f32_16x16x32_bf16 v[60:63], v[96:99], v[160:163], 0
	v_mfma_f32_16x16x32_bf16 v[56:59], v[120:123], v[160:163], 0
	v_mfma_f32_16x16x32_bf16 v[44:47], v[96:99], v[168:171], 0
	v_mfma_f32_16x16x32_bf16 v[40:43], v[120:123], v[168:171], 0
	v_mfma_f32_16x16x32_bf16 v[28:31], v[96:99], v[186:189], 0
	v_mfma_f32_16x16x32_bf16 v[24:27], v[120:123], v[186:189], 0
	v_mfma_f32_16x16x32_bf16 v[12:15], v[96:99], v[194:197], 0
	v_mfma_f32_16x16x32_bf16 v[8:11], v[120:123], v[194:197], 0
	v_mfma_f32_16x16x32_bf16 v[60:63], v[108:111], v[164:167], v[60:63]
	v_mfma_f32_16x16x32_bf16 v[56:59], v[132:135], v[164:167], v[56:59]
	v_mfma_f32_16x16x32_bf16 v[44:47], v[108:111], v[182:185], v[44:47]
	v_mfma_f32_16x16x32_bf16 v[40:43], v[132:135], v[182:185], v[40:43]
	v_mfma_f32_16x16x32_bf16 v[28:31], v[108:111], v[190:193], v[28:31]
	v_mfma_f32_16x16x32_bf16 v[24:27], v[132:135], v[190:193], v[24:27]
	v_mfma_f32_16x16x32_bf16 v[12:15], v[108:111], v[198:201], v[12:15]
	v_mfma_f32_16x16x32_bf16 v[8:11], v[132:135], v[198:201], v[8:11]
	v_mfma_f32_16x16x32_bf16 v[52:55], v[136:139], v[160:163], 0
	v_mfma_f32_16x16x32_bf16 v[48:51], v[152:155], v[160:163], 0
	v_mfma_f32_16x16x32_bf16 v[36:39], v[136:139], v[168:171], 0
	v_mfma_f32_16x16x32_bf16 v[32:35], v[152:155], v[168:171], 0
	v_mfma_f32_16x16x32_bf16 v[20:23], v[136:139], v[186:189], 0
	v_mfma_f32_16x16x32_bf16 v[16:19], v[152:155], v[186:189], 0
	v_mfma_f32_16x16x32_bf16 v[4:7], v[136:139], v[194:197], 0
	v_mfma_f32_16x16x32_bf16 v[0:3], v[152:155], v[194:197], 0
	v_mfma_f32_16x16x32_bf16 v[52:55], v[144:147], v[164:167], v[52:55]
	v_mfma_f32_16x16x32_bf16 v[48:51], v[156:159], v[164:167], v[48:51]
	v_mfma_f32_16x16x32_bf16 v[36:39], v[144:147], v[182:185], v[36:39]
	v_mfma_f32_16x16x32_bf16 v[32:35], v[156:159], v[182:185], v[32:35]
	v_mfma_f32_16x16x32_bf16 v[20:23], v[144:147], v[190:193], v[20:23]
	v_mfma_f32_16x16x32_bf16 v[16:19], v[156:159], v[190:193], v[16:19]
	v_mfma_f32_16x16x32_bf16 v[4:7], v[144:147], v[198:201], v[4:7]
	v_mfma_f32_16x16x32_bf16 v[0:3], v[156:159], v[198:201], v[0:3]
	s_setprio 0
	s_barrier
	v_add_u32_e32 v132, 0x18000, v180
	v_add_u32_e32 v156, 0x1c000, v180
	ds_read_b128 v[96:99], v132
	ds_read_b128 v[108:111], v132 offset:1024
	ds_read_b128 v[120:123], v132 offset:2048
	ds_read_b128 v[132:135], v132 offset:3072
	ds_read_b128 v[136:139], v156
	ds_read_b128 v[144:147], v156 offset:1024
	ds_read_b128 v[152:155], v156 offset:2048
	ds_read_b128 v[156:159], v156 offset:3072
	s_add_i32 s66, s66, s33
	s_mov_b32 m0, s45
	ds_read_b128 v[160:163], v181 offset:32768
	ds_read_b128 v[164:167], v181 offset:33792
	ds_read_b128 v[168:171], v181 offset:34816
	ds_read_b128 v[182:185], v181 offset:35840
	ds_read_b128 v[186:189], v181 offset:36864
	ds_read_b128 v[190:193], v181 offset:37888
	ds_read_b128 v[194:197], v181 offset:38912
	ds_read_b128 v[198:201], v181 offset:39936
	buffer_load_dwordx4 v174, s[36:39], s66 offen lds
	s_mov_b32 m0, s46
	s_nop 0
	buffer_load_dwordx4 v176, s[36:39], s66 offen lds
	s_waitcnt vmcnt(8)
	s_waitcnt lgkmcnt(0)
	s_barrier
	s_setprio 1
	v_mfma_f32_16x16x32_bf16 v[148:151], v[96:99], v[160:163], v[148:151]
	v_mfma_f32_16x16x32_bf16 v[140:143], v[120:123], v[160:163], v[140:143]
	v_mfma_f32_16x16x32_bf16 v[116:119], v[96:99], v[168:171], v[116:119]
	v_mfma_f32_16x16x32_bf16 v[112:115], v[120:123], v[168:171], v[112:115]
	v_mfma_f32_16x16x32_bf16 v[92:95], v[96:99], v[186:189], v[92:95]
	v_mfma_f32_16x16x32_bf16 v[88:91], v[120:123], v[186:189], v[88:91]
	v_mfma_f32_16x16x32_bf16 v[76:79], v[96:99], v[194:197], v[76:79]
	v_mfma_f32_16x16x32_bf16 v[72:75], v[120:123], v[194:197], v[72:75]
	v_mfma_f32_16x16x32_bf16 v[148:151], v[108:111], v[164:167], v[148:151]
	v_mfma_f32_16x16x32_bf16 v[140:143], v[132:135], v[164:167], v[140:143]
	v_mfma_f32_16x16x32_bf16 v[116:119], v[108:111], v[182:185], v[116:119]
	v_mfma_f32_16x16x32_bf16 v[112:115], v[132:135], v[182:185], v[112:115]
	v_mfma_f32_16x16x32_bf16 v[92:95], v[108:111], v[190:193], v[92:95]
	v_mfma_f32_16x16x32_bf16 v[88:91], v[132:135], v[190:193], v[88:91]
	v_mfma_f32_16x16x32_bf16 v[76:79], v[108:111], v[198:201], v[76:79]
	v_mfma_f32_16x16x32_bf16 v[72:75], v[132:135], v[198:201], v[72:75]
	v_mfma_f32_16x16x32_bf16 v[128:131], v[136:139], v[160:163], v[128:131]
	v_mfma_f32_16x16x32_bf16 v[124:127], v[152:155], v[160:163], v[124:127]
	v_mfma_f32_16x16x32_bf16 v[104:107], v[136:139], v[168:171], v[104:107]
	v_mfma_f32_16x16x32_bf16 v[100:103], v[152:155], v[168:171], v[100:103]
	v_mfma_f32_16x16x32_bf16 v[84:87], v[136:139], v[186:189], v[84:87]
	v_mfma_f32_16x16x32_bf16 v[80:83], v[152:155], v[186:189], v[80:83]
	v_mfma_f32_16x16x32_bf16 v[68:71], v[136:139], v[194:197], v[68:71]
	v_mfma_f32_16x16x32_bf16 v[64:67], v[152:155], v[194:197], v[64:67]
	v_mfma_f32_16x16x32_bf16 v[128:131], v[144:147], v[164:167], v[128:131]
	v_mfma_f32_16x16x32_bf16 v[124:127], v[156:159], v[164:167], v[124:127]
	v_mfma_f32_16x16x32_bf16 v[104:107], v[144:147], v[182:185], v[104:107]
	v_mfma_f32_16x16x32_bf16 v[100:103], v[156:159], v[182:185], v[100:103]
	v_mfma_f32_16x16x32_bf16 v[84:87], v[144:147], v[190:193], v[84:87]
	v_mfma_f32_16x16x32_bf16 v[80:83], v[156:159], v[190:193], v[80:83]
	v_mfma_f32_16x16x32_bf16 v[68:71], v[144:147], v[198:201], v[68:71]
	v_mfma_f32_16x16x32_bf16 v[64:67], v[156:159], v[198:201], v[64:67]
	s_setprio 0
	s_barrier
; #define PG8_STAGE(bufoff, rs_, soff_, voff) do { _Pragma("unroll") for (int _i = 0; _i < 2; ++_i) \
;         __builtin_amdgcn_raw_ptr_buffer_load_lds(rs_, (LAS void*)(lds + (bufoff) + ldsw + _i * 8192), 16, (int)(voff)[_i], (int)(soff_), 0, 0); } while (0)
; #define PG8_LDA(dst, b, h) do { _Pragma("unroll") for (int m = 0; m < 4; ++m) dst[m] = PG8_LD2(lds + PG8_SA(b, h) + aoff + m * 2048); } while (0)
; #define PG8_LDB(dst, b, h) do { _Pragma("unroll") for (int n = 0; n < 2; ++n) dst[n] = PG8_LD2(lds + PG8_SB(b, h) + boff + n * 2048); } while (0)
; #define PG8_WAIT_V(n) asm volatile("s_waitcnt vmcnt(" #n ")" ::: "memory")
; #define PG8_WAIT_L(n) asm volatile("s_waitcnt lgkmcnt(" #n ")" ::: "memory")
; #define PG8_BAR __builtin_amdgcn_s_barrier()
; #define PG8_SCHED __builtin_amdgcn_sched_barrier(0)
; template <class Epi, class Sched, bool ALIGN_EPI = false, bool SP2 = false, bool FP8 = false>
; __device__ __forceinline__ void gemm_phase(LAS unsigned char* lds, const Gemm g, const Sched& S, const Epi& E, int wbase) {
;     ...
;             PG8_LDB(B0, 0, 0); PG8_LDB(B1, 0, 1); PG8_SCHED; PG8_LDA(At, 0, 0); PG8_STAGE(PG8_SA(1, 1), rAc, a1 + hstep, voffA);
;             PG8_WAIT_V(8); PG8_WAIT_L(0); PG8_BAR; PG8_MMA(0, 0, At, B0); PG8_MMA(0, 1, At, B1); PG8_BAR; PG8_SCHED;
;     ...
;             PG8_WAIT_V(8); PG8_WAIT_L(0); PG8_BAR; PG8_MMA(0, 0, At, B0); PG8_MMA(0, 1, At, B1); PG8_BAR; PG8_SCHED;
;             PG8_LDA(At, 1, 1); PG8_STAGE(PG8_SB(1, 0), rB2, b3, voffB); PG8_STAGE(PG8_SB(1, 1), rB2, b3 + hstep, voffB); PG8_STAGE(PG8_SA(1, 0), rA2, a3, voffA);
;             PG8_WAIT_V(8); PG8_WAIT_L(0); PG8_BAR; PG8_MMA(1, 0, At, B0); PG8_MMA(1, 1, At, B1); PG8_BAR; PG8_SCHED;
	s_mov_b32 m0, s47
	s_bitset1_b32 s55, 7
	ds_read_b128 v[160:163], v181 offset:49152
	ds_read_b128 v[164:167], v181 offset:50176
	ds_read_b128 v[168:171], v181 offset:51200
	ds_read_b128 v[182:185], v181 offset:52224
	ds_read_b128 v[186:189], v181 offset:53248
	ds_read_b128 v[190:193], v181 offset:54272
	ds_read_b128 v[194:197], v181 offset:55296
	ds_read_b128 v[198:201], v181 offset:56320
	buffer_load_dwordx4 v175, s[12:15], s55 offen lds
	s_mov_b32 m0, s48
	s_nop 0
	buffer_load_dwordx4 v177, s[12:15], s55 offen lds
	s_add_i32 s55, s55, s33
	s_mov_b32 m0, s56
	s_nop 0
	buffer_load_dwordx4 v175, s[12:15], s55 offen lds
	s_mov_b32 m0, s57
	s_nop 0
	buffer_load_dwordx4 v177, s[12:15], s55 offen lds
	s_mov_b32 m0, s52
	s_nop 0
	buffer_load_dwordx4 v174, s[36:39], s54 offen lds
	s_mov_b32 m0, s53
	s_nop 0
	buffer_load_dwordx4 v176, s[36:39], s54 offen lds
	s_waitcnt vmcnt(8)
	s_waitcnt lgkmcnt(0)
	s_barrier
	s_setprio 1
	v_mfma_f32_16x16x32_bf16 v[60:63], v[96:99], v[160:163], v[60:63]
	v_mfma_f32_16x16x32_bf16 v[56:59], v[120:123], v[160:163], v[56:59]
	v_mfma_f32_16x16x32_bf16 v[44:47], v[96:99], v[168:171], v[44:47]
	v_mfma_f32_16x16x32_bf16 v[40:43], v[120:123], v[168:171], v[40:43]
	v_mfma_f32_16x16x32_bf16 v[28:31], v[96:99], v[186:189], v[28:31]
	v_mfma_f32_16x16x32_bf16 v[24:27], v[120:123], v[186:189], v[24:27]
	v_mfma_f32_16x16x32_bf16 v[12:15], v[96:99], v[194:197], v[12:15]
	v_mfma_f32_16x16x32_bf16 v[8:11], v[120:123], v[194:197], v[8:11]
	v_mfma_f32_16x16x32_bf16 v[60:63], v[108:111], v[164:167], v[60:63]
	v_mfma_f32_16x16x32_bf16 v[56:59], v[132:135], v[164:167], v[56:59]
	v_mfma_f32_16x16x32_bf16 v[44:47], v[108:111], v[182:185], v[44:47]
	v_mfma_f32_16x16x32_bf16 v[40:43], v[132:135], v[182:185], v[40:43]
	v_mfma_f32_16x16x32_bf16 v[28:31], v[108:111], v[190:193], v[28:31]
	v_mfma_f32_16x16x32_bf16 v[24:27], v[132:135], v[190:193], v[24:27]
	v_mfma_f32_16x16x32_bf16 v[12:15], v[108:111], v[198:201], v[12:15]
	v_mfma_f32_16x16x32_bf16 v[8:11], v[132:135], v[198:201], v[8:11]
	v_mfma_f32_16x16x32_bf16 v[52:55], v[136:139], v[160:163], v[52:55]
	v_mfma_f32_16x16x32_bf16 v[48:51], v[152:155], v[160:163], v[48:51]
	v_mfma_f32_16x16x32_bf16 v[36:39], v[136:139], v[168:171], v[36:39]
	v_mfma_f32_16x16x32_bf16 v[32:35], v[152:155], v[168:171], v[32:35]
	v_mfma_f32_16x16x32_bf16 v[20:23], v[136:139], v[186:189], v[20:23]
	v_mfma_f32_16x16x32_bf16 v[16:19], v[152:155], v[186:189], v[16:19]
	v_mfma_f32_16x16x32_bf16 v[4:7], v[136:139], v[194:197], v[4:7]
	v_mfma_f32_16x16x32_bf16 v[0:3], v[152:155], v[194:197], v[0:3]
	v_mfma_f32_16x16x32_bf16 v[52:55], v[144:147], v[164:167], v[52:55]
	v_mfma_f32_16x16x32_bf16 v[48:51], v[156:159], v[164:167], v[48:51]
	v_mfma_f32_16x16x32_bf16 v[36:39], v[144:147], v[182:185], v[36:39]
	v_mfma_f32_16x16x32_bf16 v[32:35], v[156:159], v[182:185], v[32:35]
	v_mfma_f32_16x16x32_bf16 v[20:23], v[144:147], v[190:193], v[20:23]
	v_mfma_f32_16x16x32_bf16 v[16:19], v[156:159], v[190:193], v[16:19]
	v_mfma_f32_16x16x32_bf16 v[4:7], v[144:147], v[198:201], v[4:7]
	v_mfma_f32_16x16x32_bf16 v[0:3], v[156:159], v[198:201], v[0:3]
	s_setprio 0
	s_barrier
	s_add_i32 s11, s11, 2
	s_addk_i32 s4, 0x100
	s_addk_i32 s5, 0x100
	s_cmp_ge_i32 s11, s60
	s_cbranch_scc0 .LBB0_1004
	s_branch .Lzp_after_1004
.LBB0_1004:
	v_add_u32_e32 v132, 0x10000, v180
	v_add_u32_e32 v156, 0x14000, v180
	ds_read_b128 v[96:99], v132
	ds_read_b128 v[108:111], v132 offset:1024
	ds_read_b128 v[120:123], v132 offset:2048
	ds_read_b128 v[132:135], v132 offset:3072
	ds_read_b128 v[136:139], v156
	ds_read_b128 v[144:147], v156 offset:1024
	ds_read_b128 v[152:155], v156 offset:2048
	ds_read_b128 v[156:159], v156 offset:3072
	s_add_i32 s14, s4, 0x80
	s_cmp_eq_u32 s62, s11
	s_cselect_b32 s66, s2, s14
	s_cselect_b32 s55, s3, s5
	s_or_b32 s54, s66, 0x80
	s_add_i32 s14, s33, s4
	s_mov_b32 m0, s63
	ds_read_b128 v[160:163], v181
	ds_read_b128 v[164:167], v181 offset:1024
	ds_read_b128 v[168:171], v181 offset:2048
	ds_read_b128 v[182:185], v181 offset:3072
	ds_read_b128 v[186:189], v181 offset:4096
	ds_read_b128 v[190:193], v181 offset:5120
	ds_read_b128 v[194:197], v181 offset:6144
	ds_read_b128 v[198:201], v181 offset:7168
	buffer_load_dwordx4 v174, s[36:39], s14 offen lds
	s_mov_b32 m0, s65
	s_nop 0
	buffer_load_dwordx4 v176, s[36:39], s14 offen lds
	s_waitcnt vmcnt(8)
	s_waitcnt lgkmcnt(0)
	s_barrier
	s_setprio 1
	v_mfma_f32_16x16x32_bf16 v[148:151], v[96:99], v[160:163], v[148:151]
	v_mfma_f32_16x16x32_bf16 v[140:143], v[120:123], v[160:163], v[140:143]
	v_mfma_f32_16x16x32_bf16 v[116:119], v[96:99], v[168:171], v[116:119]
	v_mfma_f32_16x16x32_bf16 v[112:115], v[120:123], v[168:171], v[112:115]
	v_mfma_f32_16x16x32_bf16 v[92:95], v[96:99], v[186:189], v[92:95]
	v_mfma_f32_16x16x32_bf16 v[88:91], v[120:123], v[186:189], v[88:91]
	v_mfma_f32_16x16x32_bf16 v[76:79], v[96:99], v[194:197], v[76:79]
	v_mfma_f32_16x16x32_bf16 v[72:75], v[120:123], v[194:197], v[72:75]
	v_mfma_f32_16x16x32_bf16 v[148:151], v[108:111], v[164:167], v[148:151]
	v_mfma_f32_16x16x32_bf16 v[140:143], v[132:135], v[164:167], v[140:143]
	v_mfma_f32_16x16x32_bf16 v[116:119], v[108:111], v[182:185], v[116:119]
	v_mfma_f32_16x16x32_bf16 v[112:115], v[132:135], v[182:185], v[112:115]
	v_mfma_f32_16x16x32_bf16 v[92:95], v[108:111], v[190:193], v[92:95]
	v_mfma_f32_16x16x32_bf16 v[88:91], v[132:135], v[190:193], v[88:91]
	v_mfma_f32_16x16x32_bf16 v[76:79], v[108:111], v[198:201], v[76:79]
	v_mfma_f32_16x16x32_bf16 v[72:75], v[132:135], v[198:201], v[72:75]
	v_mfma_f32_16x16x32_bf16 v[128:131], v[136:139], v[160:163], v[128:131]
	v_mfma_f32_16x16x32_bf16 v[124:127], v[152:155], v[160:163], v[124:127]
	v_mfma_f32_16x16x32_bf16 v[104:107], v[136:139], v[168:171], v[104:107]
	v_mfma_f32_16x16x32_bf16 v[100:103], v[152:155], v[168:171], v[100:103]
	v_mfma_f32_16x16x32_bf16 v[84:87], v[136:139], v[186:189], v[84:87]
	v_mfma_f32_16x16x32_bf16 v[80:83], v[152:155], v[186:189], v[80:83]
	v_mfma_f32_16x16x32_bf16 v[68:71], v[136:139], v[194:197], v[68:71]
	v_mfma_f32_16x16x32_bf16 v[64:67], v[152:155], v[194:197], v[64:67]
	v_mfma_f32_16x16x32_bf16 v[128:131], v[144:147], v[164:167], v[128:131]
	v_mfma_f32_16x16x32_bf16 v[124:127], v[156:159], v[164:167], v[124:127]
	v_mfma_f32_16x16x32_bf16 v[104:107], v[144:147], v[182:185], v[104:107]
	v_mfma_f32_16x16x32_bf16 v[100:103], v[156:159], v[182:185], v[100:103]
	v_mfma_f32_16x16x32_bf16 v[84:87], v[144:147], v[190:193], v[84:87]
	v_mfma_f32_16x16x32_bf16 v[80:83], v[156:159], v[190:193], v[80:83]
	v_mfma_f32_16x16x32_bf16 v[68:71], v[144:147], v[198:201], v[68:71]
	v_mfma_f32_16x16x32_bf16 v[64:67], v[156:159], v[198:201], v[64:67]
	s_setprio 0
	s_barrier
; #define PG8_STAGE(bufoff, rs_, soff_, voff) do { _Pragma("unroll") for (int _i = 0; _i < 2; ++_i) \
;         __builtin_amdgcn_raw_ptr_buffer_load_lds(rs_, (LAS void*)(lds + (bufoff) + ldsw + _i * 8192), 16, (int)(voff)[_i], (int)(soff_), 0, 0); } while (0)
; #define PG8_LDA(dst, b, h) do { _Pragma("unroll") for (int m = 0; m < 4; ++m) dst[m] = PG8_LD2(lds + PG8_SA(b, h) + aoff + m * 2048); } while (0)
; #define PG8_LDB(dst, b, h) do { _Pragma("unroll") for (int n = 0; n < 2; ++n) dst[n] = PG8_LD2(lds + PG8_SB(b, h) + boff + n * 2048); } while (0)
; #define PG8_WAIT_V(n) asm volatile("s_waitcnt vmcnt(" #n ")" ::: "memory")
; #define PG8_WAIT_L(n) asm volatile("s_waitcnt lgkmcnt(" #n ")" ::: "memory")
; #define PG8_BAR __builtin_amdgcn_s_barrier()
; #define PG8_SCHED __builtin_amdgcn_sched_barrier(0)
; template <class Epi, class Sched, bool ALIGN_EPI = false, bool SP2 = false, bool FP8 = false>
; __device__ __forceinline__ void gemm_phase(LAS unsigned char* lds, const Gemm g, const Sched& S, const Epi& E, int wbase) {
;     ...
;             PG8_LDA(At, 0, 1); PG8_STAGE(PG8_SB(0, 0), rB2, b2, voffB); PG8_STAGE(PG8_SB(0, 1), rB2, b2 + hstep, voffB); PG8_STAGE(PG8_SA(0, 0), rA2, a2, voffA);
;             PG8_WAIT_V(8); PG8_WAIT_L(0); PG8_BAR; PG8_MMA(1, 0, At, B0); PG8_MMA(1, 1, At, B1); PG8_BAR; PG8_SCHED;
;             PG8_LDB(B0, 1, 0); PG8_LDB(B1, 1, 1); PG8_SCHED; PG8_LDA(At, 1, 0); PG8_STAGE(PG8_SA(0, 1), rA2, a2 + hstep, voffA);
;             PG8_WAIT_V(8); PG8_WAIT_L(0); PG8_BAR; PG8_MMA(0, 0, At, B0); PG8_MMA(0, 1, At, B1); PG8_BAR; PG8_SCHED;
	s_mov_b32 m0, s35
	s_mov_b32 s14, s38
	s_mov_b32 s15, s39
	ds_read_b128 v[160:163], v181 offset:16384
	ds_read_b128 v[164:167], v181 offset:17408
	ds_read_b128 v[168:171], v181 offset:18432
	ds_read_b128 v[182:185], v181 offset:19456
	ds_read_b128 v[186:189], v181 offset:20480
	ds_read_b128 v[190:193], v181 offset:21504
	ds_read_b128 v[194:197], v181 offset:22528
	ds_read_b128 v[198:201], v181 offset:23552
	buffer_load_dwordx4 v175, s[12:15], s55 offen lds
	s_mov_b32 m0, s41
	s_add_i32 s67, s55, s33
	buffer_load_dwordx4 v177, s[12:15], s55 offen lds
	s_mov_b32 m0, s42
	s_nop 0
	buffer_load_dwordx4 v175, s[12:15], s67 offen lds
	s_mov_b32 m0, s43
	s_nop 0
	buffer_load_dwordx4 v177, s[12:15], s67 offen lds
	s_mov_b32 m0, s34
	s_nop 0
	buffer_load_dwordx4 v174, s[36:39], s66 offen lds
	s_mov_b32 m0, s44
	s_nop 0
	buffer_load_dwordx4 v176, s[36:39], s66 offen lds
	s_waitcnt vmcnt(8)
	s_waitcnt lgkmcnt(0)
	s_barrier
	s_setprio 1
	v_mfma_f32_16x16x32_bf16 v[60:63], v[96:99], v[160:163], v[60:63]
	v_mfma_f32_16x16x32_bf16 v[56:59], v[120:123], v[160:163], v[56:59]
	v_mfma_f32_16x16x32_bf16 v[44:47], v[96:99], v[168:171], v[44:47]
	v_mfma_f32_16x16x32_bf16 v[40:43], v[120:123], v[168:171], v[40:43]
	v_mfma_f32_16x16x32_bf16 v[28:31], v[96:99], v[186:189], v[28:31]
	v_mfma_f32_16x16x32_bf16 v[24:27], v[120:123], v[186:189], v[24:27]
	v_mfma_f32_16x16x32_bf16 v[12:15], v[96:99], v[194:197], v[12:15]
	v_mfma_f32_16x16x32_bf16 v[8:11], v[120:123], v[194:197], v[8:11]
	v_mfma_f32_16x16x32_bf16 v[60:63], v[108:111], v[164:167], v[60:63]
	v_mfma_f32_16x16x32_bf16 v[56:59], v[132:135], v[164:167], v[56:59]
	v_mfma_f32_16x16x32_bf16 v[44:47], v[108:111], v[182:185], v[44:47]
	v_mfma_f32_16x16x32_bf16 v[40:43], v[132:135], v[182:185], v[40:43]
	v_mfma_f32_16x16x32_bf16 v[28:31], v[108:111], v[190:193], v[28:31]
	v_mfma_f32_16x16x32_bf16 v[24:27], v[132:135], v[190:193], v[24:27]
	v_mfma_f32_16x16x32_bf16 v[12:15], v[108:111], v[198:201], v[12:15]
	v_mfma_f32_16x16x32_bf16 v[8:11], v[132:135], v[198:201], v[8:11]
	v_mfma_f32_16x16x32_bf16 v[52:55], v[136:139], v[160:163], v[52:55]
	v_mfma_f32_16x16x32_bf16 v[48:51], v[152:155], v[160:163], v[48:51]
	v_mfma_f32_16x16x32_bf16 v[36:39], v[136:139], v[168:171], v[36:39]
	v_mfma_f32_16x16x32_bf16 v[32:35], v[152:155], v[168:171], v[32:35]
	v_mfma_f32_16x16x32_bf16 v[20:23], v[136:139], v[186:189], v[20:23]
	v_mfma_f32_16x16x32_bf16 v[16:19], v[152:155], v[186:189], v[16:19]
	v_mfma_f32_16x16x32_bf16 v[4:7], v[136:139], v[194:197], v[4:7]
	v_mfma_f32_16x16x32_bf16 v[0:3], v[152:155], v[194:197], v[0:3]
	v_mfma_f32_16x16x32_bf16 v[52:55], v[144:147], v[164:167], v[52:55]
	v_mfma_f32_16x16x32_bf16 v[48:51], v[156:159], v[164:167], v[48:51]
	v_mfma_f32_16x16x32_bf16 v[36:39], v[144:147], v[182:185], v[36:39]
	v_mfma_f32_16x16x32_bf16 v[32:35], v[156:159], v[182:185], v[32:35]
	v_mfma_f32_16x16x32_bf16 v[20:23], v[144:147], v[190:193], v[20:23]
	v_mfma_f32_16x16x32_bf16 v[16:19], v[156:159], v[190:193], v[16:19]
	v_mfma_f32_16x16x32_bf16 v[4:7], v[144:147], v[198:201], v[4:7]
	v_mfma_f32_16x16x32_bf16 v[0:3], v[156:159], v[198:201], v[0:3]
	s_setprio 0
	s_barrier
	v_add_u32_e32 v132, 0x18000, v180
	v_add_u32_e32 v156, 0x1c000, v180
	ds_read_b128 v[96:99], v132
	ds_read_b128 v[108:111], v132 offset:1024
	ds_read_b128 v[120:123], v132 offset:2048
	ds_read_b128 v[132:135], v132 offset:3072
	ds_read_b128 v[136:139], v156
	ds_read_b128 v[144:147], v156 offset:1024
	ds_read_b128 v[152:155], v156 offset:2048
	ds_read_b128 v[156:159], v156 offset:3072
	s_add_i32 s66, s66, s33
	s_mov_b32 m0, s45
	ds_read_b128 v[160:163], v181 offset:32768
	ds_read_b128 v[164:167], v181 offset:33792
	ds_read_b128 v[168:171], v181 offset:34816
	ds_read_b128 v[182:185], v181 offset:35840
	ds_read_b128 v[186:189], v181 offset:36864
	ds_read_b128 v[190:193], v181 offset:37888
	ds_read_b128 v[194:197], v181 offset:38912
	ds_read_b128 v[198:201], v181 offset:39936
	buffer_load_dwordx4 v174, s[36:39], s66 offen lds
	s_mov_b32 m0, s46
	s_nop 0
	buffer_load_dwordx4 v176, s[36:39], s66 offen lds
	s_waitcnt vmcnt(8)
	s_waitcnt lgkmcnt(0)
	s_barrier
; #define PG8_STAGE(bufoff, rs_, soff_, voff) do { _Pragma("unroll") for (int _i = 0; _i < 2; ++_i) \
;         __builtin_amdgcn_raw_ptr_buffer_load_lds(rs_, (LAS void*)(lds + (bufoff) + ldsw + _i * 8192), 16, (int)(voff)[_i], (int)(soff_), 0, 0); } while (0)
; #define PG8_LDA(dst, b, h) do { _Pragma("unroll") for (int m = 0; m < 4; ++m) dst[m] = PG8_LD2(lds + PG8_SA(b, h) + aoff + m * 2048); } while (0)
; #define PG8_WAIT_V(n) asm volatile("s_waitcnt vmcnt(" #n ")" ::: "memory")
; #define PG8_WAIT_L(n) asm volatile("s_waitcnt lgkmcnt(" #n ")" ::: "memory")
; #define PG8_BAR __builtin_amdgcn_s_barrier()
; #define PG8_SCHED __builtin_amdgcn_sched_barrier(0)
; template <class Epi, class Sched, bool ALIGN_EPI = false, bool SP2 = false, bool FP8 = false>
; __device__ __forceinline__ void gemm_phase(LAS unsigned char* lds, const Gemm g, const Sched& S, const Epi& E, int wbase) {
;     ...
;             PG8_LDA(At, 1, 1); PG8_STAGE(PG8_SB(1, 0), rB2, b3, voffB); PG8_STAGE(PG8_SB(1, 1), rB2, b3 + hstep, voffB); PG8_STAGE(PG8_SA(1, 0), rA2, a3, voffA);
;             PG8_WAIT_V(8); PG8_WAIT_L(0); PG8_BAR; PG8_MMA(1, 0, At, B0); PG8_MMA(1, 1, At, B1); PG8_BAR; PG8_SCHED;
;     ...
;         if constexpr (ALIGN_EPI) { if (wr == 0) PG8_BAR; }
	s_setprio 1
	v_mfma_f32_16x16x32_bf16 v[148:151], v[96:99], v[160:163], v[148:151]
	v_mfma_f32_16x16x32_bf16 v[140:143], v[120:123], v[160:163], v[140:143]
	v_mfma_f32_16x16x32_bf16 v[116:119], v[96:99], v[168:171], v[116:119]
	v_mfma_f32_16x16x32_bf16 v[112:115], v[120:123], v[168:171], v[112:115]
	v_mfma_f32_16x16x32_bf16 v[92:95], v[96:99], v[186:189], v[92:95]
	v_mfma_f32_16x16x32_bf16 v[88:91], v[120:123], v[186:189], v[88:91]
	v_mfma_f32_16x16x32_bf16 v[76:79], v[96:99], v[194:197], v[76:79]
	v_mfma_f32_16x16x32_bf16 v[72:75], v[120:123], v[194:197], v[72:75]
	v_mfma_f32_16x16x32_bf16 v[148:151], v[108:111], v[164:167], v[148:151]
	v_mfma_f32_16x16x32_bf16 v[140:143], v[132:135], v[164:167], v[140:143]
	v_mfma_f32_16x16x32_bf16 v[116:119], v[108:111], v[182:185], v[116:119]
	v_mfma_f32_16x16x32_bf16 v[112:115], v[132:135], v[182:185], v[112:115]
	v_mfma_f32_16x16x32_bf16 v[92:95], v[108:111], v[190:193], v[92:95]
	v_mfma_f32_16x16x32_bf16 v[88:91], v[132:135], v[190:193], v[88:91]
	v_mfma_f32_16x16x32_bf16 v[76:79], v[108:111], v[198:201], v[76:79]
	v_mfma_f32_16x16x32_bf16 v[72:75], v[132:135], v[198:201], v[72:75]
	v_mfma_f32_16x16x32_bf16 v[128:131], v[136:139], v[160:163], v[128:131]
	v_mfma_f32_16x16x32_bf16 v[124:127], v[152:155], v[160:163], v[124:127]
	v_mfma_f32_16x16x32_bf16 v[104:107], v[136:139], v[168:171], v[104:107]
	v_mfma_f32_16x16x32_bf16 v[100:103], v[152:155], v[168:171], v[100:103]
	v_mfma_f32_16x16x32_bf16 v[84:87], v[136:139], v[186:189], v[84:87]
	v_mfma_f32_16x16x32_bf16 v[80:83], v[152:155], v[186:189], v[80:83]
	v_mfma_f32_16x16x32_bf16 v[68:71], v[136:139], v[194:197], v[68:71]
	v_mfma_f32_16x16x32_bf16 v[64:67], v[152:155], v[194:197], v[64:67]
	v_mfma_f32_16x16x32_bf16 v[128:131], v[144:147], v[164:167], v[128:131]
	v_mfma_f32_16x16x32_bf16 v[124:127], v[156:159], v[164:167], v[124:127]
	v_mfma_f32_16x16x32_bf16 v[104:107], v[144:147], v[182:185], v[104:107]
	v_mfma_f32_16x16x32_bf16 v[100:103], v[156:159], v[182:185], v[100:103]
	v_mfma_f32_16x16x32_bf16 v[84:87], v[144:147], v[190:193], v[84:87]
	v_mfma_f32_16x16x32_bf16 v[80:83], v[156:159], v[190:193], v[80:83]
	v_mfma_f32_16x16x32_bf16 v[68:71], v[144:147], v[198:201], v[68:71]
	v_mfma_f32_16x16x32_bf16 v[64:67], v[156:159], v[198:201], v[64:67]
	s_setprio 0
	s_barrier
	s_mov_b32 m0, s47
	s_bitset1_b32 s55, 7
	ds_read_b128 v[160:163], v181 offset:49152
	ds_read_b128 v[164:167], v181 offset:50176
	ds_read_b128 v[168:171], v181 offset:51200
	ds_read_b128 v[182:185], v181 offset:52224
	ds_read_b128 v[186:189], v181 offset:53248
	ds_read_b128 v[190:193], v181 offset:54272
	ds_read_b128 v[194:197], v181 offset:55296
	ds_read_b128 v[198:201], v181 offset:56320
	buffer_load_dwordx4 v175, s[12:15], s55 offen lds
	s_mov_b32 m0, s48
	s_nop 0
	buffer_load_dwordx4 v177, s[12:15], s55 offen lds
	s_add_i32 s55, s55, s33
	s_mov_b32 m0, s56
	s_nop 0
	buffer_load_dwordx4 v175, s[12:15], s55 offen lds
	s_mov_b32 m0, s57
	s_nop 0
	buffer_load_dwordx4 v177, s[12:15], s55 offen lds
	s_mov_b32 m0, s52
	s_nop 0
	buffer_load_dwordx4 v174, s[36:39], s54 offen lds
	s_mov_b32 m0, s53
	s_nop 0
	buffer_load_dwordx4 v176, s[36:39], s54 offen lds
	s_waitcnt vmcnt(8)
	s_waitcnt lgkmcnt(0)
	s_barrier
	s_setprio 1
	v_mfma_f32_16x16x32_bf16 v[60:63], v[96:99], v[160:163], v[60:63]
	v_mfma_f32_16x16x32_bf16 v[56:59], v[120:123], v[160:163], v[56:59]
	v_mfma_f32_16x16x32_bf16 v[44:47], v[96:99], v[168:171], v[44:47]
	v_mfma_f32_16x16x32_bf16 v[40:43], v[120:123], v[168:171], v[40:43]
	v_mfma_f32_16x16x32_bf16 v[28:31], v[96:99], v[186:189], v[28:31]
	v_mfma_f32_16x16x32_bf16 v[24:27], v[120:123], v[186:189], v[24:27]
	v_mfma_f32_16x16x32_bf16 v[12:15], v[96:99], v[194:197], v[12:15]
	v_mfma_f32_16x16x32_bf16 v[8:11], v[120:123], v[194:197], v[8:11]
	v_mfma_f32_16x16x32_bf16 v[60:63], v[108:111], v[164:167], v[60:63]
	v_mfma_f32_16x16x32_bf16 v[56:59], v[132:135], v[164:167], v[56:59]
	v_mfma_f32_16x16x32_bf16 v[44:47], v[108:111], v[182:185], v[44:47]
	v_mfma_f32_16x16x32_bf16 v[40:43], v[132:135], v[182:185], v[40:43]
	v_mfma_f32_16x16x32_bf16 v[28:31], v[108:111], v[190:193], v[28:31]
	v_mfma_f32_16x16x32_bf16 v[24:27], v[132:135], v[190:193], v[24:27]
	v_mfma_f32_16x16x32_bf16 v[12:15], v[108:111], v[198:201], v[12:15]
	v_mfma_f32_16x16x32_bf16 v[8:11], v[132:135], v[198:201], v[8:11]
	v_mfma_f32_16x16x32_bf16 v[52:55], v[136:139], v[160:163], v[52:55]
	v_mfma_f32_16x16x32_bf16 v[48:51], v[152:155], v[160:163], v[48:51]
	v_mfma_f32_16x16x32_bf16 v[36:39], v[136:139], v[168:171], v[36:39]
	v_mfma_f32_16x16x32_bf16 v[32:35], v[152:155], v[168:171], v[32:35]
	v_mfma_f32_16x16x32_bf16 v[20:23], v[136:139], v[186:189], v[20:23]
	v_mfma_f32_16x16x32_bf16 v[16:19], v[152:155], v[186:189], v[16:19]
	v_mfma_f32_16x16x32_bf16 v[4:7], v[136:139], v[194:197], v[4:7]
	v_mfma_f32_16x16x32_bf16 v[0:3], v[152:155], v[194:197], v[0:3]
	v_mfma_f32_16x16x32_bf16 v[52:55], v[144:147], v[164:167], v[52:55]
	v_mfma_f32_16x16x32_bf16 v[48:51], v[156:159], v[164:167], v[48:51]
	v_mfma_f32_16x16x32_bf16 v[36:39], v[144:147], v[182:185], v[36:39]
	v_mfma_f32_16x16x32_bf16 v[32:35], v[156:159], v[182:185], v[32:35]
	v_mfma_f32_16x16x32_bf16 v[20:23], v[144:147], v[190:193], v[20:23]
	v_mfma_f32_16x16x32_bf16 v[16:19], v[156:159], v[190:193], v[16:19]
	v_mfma_f32_16x16x32_bf16 v[4:7], v[144:147], v[198:201], v[4:7]
	v_mfma_f32_16x16x32_bf16 v[0:3], v[156:159], v[198:201], v[0:3]
	s_setprio 0
	s_barrier
	s_add_i32 s11, s11, 2
	s_addk_i32 s4, 0x100
	s_addk_i32 s5, 0x100
	s_cmp_ge_i32 s11, s60
	s_cbranch_scc0 .LBB0_1004
.Lzp_after_1004:
	s_and_b64 vcc, exec, s[26:27]
	s_cbranch_vccz .LBB0_1007
.LBB0_1006:
	s_barrier

; #define PG8_STAGE(bufoff, rs_, soff_, voff) do { _Pragma("unroll") for (int _i = 0; _i < 2; ++_i) \
;         __builtin_amdgcn_raw_ptr_buffer_load_lds(rs_, (LAS void*)(lds + (bufoff) + ldsw + _i * 8192), 16, (int)(voff)[_i], (int)(soff_), 0, 0); } while (0)
; #define PG8_LDA(dst, b, h) do { _Pragma("unroll") for (int m = 0; m < 4; ++m) dst[m] = PG8_LD2(lds + PG8_SA(b, h) + aoff + m * 2048); } while (0)
; #define PG8_LDB(dst, b, h) do { _Pragma("unroll") for (int n = 0; n < 2; ++n) dst[n] = PG8_LD2(lds + PG8_SB(b, h) + boff + n * 2048); } while (0)
; #define PG8_WAIT_V(n) asm volatile("s_waitcnt vmcnt(" #n ")" ::: "memory")
; #define PG8_WAIT_L(n) asm volatile("s_waitcnt lgkmcnt(" #n ")" ::: "memory")
; #define PG8_BAR __builtin_amdgcn_s_barrier()
; #define PG8_SCHED __builtin_amdgcn_sched_barrier(0)
; template <class Epi, class Sched, bool ALIGN_EPI = false, bool SP2 = false, bool FP8 = false>
; __device__ __forceinline__ void gemm_phase(LAS unsigned char* lds, const Gemm g, const Sched& S, const Epi& E, int wbase) {
;     ...
;             const unsigned a2 = last ? nA : cA + (unsigned)(t + 2) * kstep, b2 = last ? nB : cB + (unsigned)(t + 2) * kstep; const rsrc_t rA2 = (Sched::TWO && last) ? rAn : rAc, rB2 = (Sched::TWO && last) ? rBn : rBc;
;             const unsigned a3 = a2 + kstep, b3 = b2 + kstep;
;             if (last && has_next) S.a_ready(nxt);
;             if constexpr (SP2) {
;             PG8_LDB(B0, 0, 0); PG8_LDB(B1, 0, 1); PG8_SCHED; PG8_LDA(At, 0, 0); PG8_STAGE(PG8_SA(1, 1), rAc, a1 + hstep, voffA);
;             PG8_WAIT_V(8); PG8_WAIT_L(0); PG8_BAR; PG8_MMA(0, 0, At, B0); PG8_MMA(0, 1, At, B1); PG8_BAR; PG8_SCHED;
;             PG8_LDA(At, 0, 1); PG8_STAGE(PG8_SB(0, 0), rB2, b2, voffB); PG8_STAGE(PG8_SB(0, 1), rB2, b2 + hstep, voffB); PG8_STAGE(PG8_SA(0, 0), rA2, a2, voffA);
;             PG8_WAIT_V(8); PG8_WAIT_L(0); PG8_BAR; PG8_MMA(1, 0, At, B0); PG8_MMA(1, 1, At, B1); PG8_BAR; PG8_SCHED;
.LBB0_1626:
	s_lshl_b32 s56, s53, 19
	s_andn2_b64 vcc, exec, s[12:13]
	s_lshl_b32 s57, s52, 19
	s_cbranch_vccnz .LBB0_1634
	s_and_b64 s[6:7], s[18:19], exec
	s_waitcnt vmcnt(37)
	s_waitcnt vmcnt(35)
	s_waitcnt vmcnt(31)
	s_waitcnt vmcnt(27)
	s_waitcnt vmcnt(23)
	s_waitcnt vmcnt(22)
	s_cselect_b32 s59, s56, s55
	s_cselect_b32 s60, s57, s54
	s_add_i32 s61, s55, 0x80
	s_add_i32 s62, s54, 0x100
	s_mov_b32 s63, 0
	v_add_u32_e32 v136, 0x10000, v161
	ds_read_b128 v[128:131], v136
	ds_read_b128 v[132:135], v136 offset:1024
	ds_read_b128 v[164:167], v136 offset:2048
	ds_read_b128 v[168:171], v136 offset:3072
	v_add_u32_e32 v136, 0x14000, v161
	ds_read_b128 v[172:175], v136
	ds_read_b128 v[176:179], v136 offset:1024
	ds_read_b128 v[180:183], v136 offset:2048
	ds_read_b128 v[184:187], v136 offset:3072
	s_add_i32 s6, s61, 0x80
	s_cmp_eq_u32 s46, s63
	s_cselect_b32 s65, s59, s6
	s_cselect_b32 s55, s60, s62
	s_or_b32 s54, s65, 0x80
	s_add_i32 s6, s22, s61
	s_mov_b32 m0, s47
	ds_read_b128 v[188:191], v162
	ds_read_b128 v[192:195], v162 offset:1024
	ds_read_b128 v[196:199], v162 offset:2048
	ds_read_b128 v[200:203], v162 offset:3072
	ds_read_b128 v[204:207], v162 offset:4096
	ds_read_b128 v[208:211], v162 offset:5120
	ds_read_b128 v[212:215], v162 offset:6144
	ds_read_b128 v[216:219], v162 offset:7168
	buffer_load_dwordx4 v137, s[36:39], s6 offen lds
	s_mov_b32 m0, s48
	s_nop 0
	buffer_load_dwordx4 v145, s[36:39], s6 offen lds
	s_waitcnt vmcnt(8)
	s_waitcnt lgkmcnt(0)
	s_barrier
	s_setprio 1
	v_mfma_f32_16x16x32_bf16 v[120:123], v[128:131], v[188:191], 0
	v_mfma_f32_16x16x32_bf16 v[124:127], v[164:167], v[188:191], 0
	v_mfma_f32_16x16x32_bf16 v[104:107], v[128:131], v[196:199], 0
	v_mfma_f32_16x16x32_bf16 v[108:111], v[164:167], v[196:199], 0
	v_mfma_f32_16x16x32_bf16 v[88:91], v[128:131], v[204:207], 0
	v_mfma_f32_16x16x32_bf16 v[92:95], v[164:167], v[204:207], 0
	v_mfma_f32_16x16x32_bf16 v[72:75], v[128:131], v[212:215], 0
	v_mfma_f32_16x16x32_bf16 v[76:79], v[164:167], v[212:215], 0
	v_mfma_f32_16x16x32_bf16 v[120:123], v[132:135], v[192:195], v[120:123]
	v_mfma_f32_16x16x32_bf16 v[124:127], v[168:171], v[192:195], v[124:127]
	v_mfma_f32_16x16x32_bf16 v[104:107], v[132:135], v[200:203], v[104:107]
	v_mfma_f32_16x16x32_bf16 v[108:111], v[168:171], v[200:203], v[108:111]
	v_mfma_f32_16x16x32_bf16 v[88:91], v[132:135], v[208:211], v[88:91]
	v_mfma_f32_16x16x32_bf16 v[92:95], v[168:171], v[208:211], v[92:95]
	v_mfma_f32_16x16x32_bf16 v[72:75], v[132:135], v[216:219], v[72:75]
	v_mfma_f32_16x16x32_bf16 v[76:79], v[168:171], v[216:219], v[76:79]
	v_mfma_f32_16x16x32_bf16 v[112:115], v[172:175], v[188:191], 0
	v_mfma_f32_16x16x32_bf16 v[116:119], v[180:183], v[188:191], 0
	v_mfma_f32_16x16x32_bf16 v[96:99], v[172:175], v[196:199], 0
	v_mfma_f32_16x16x32_bf16 v[100:103], v[180:183], v[196:199], 0
	v_mfma_f32_16x16x32_bf16 v[80:83], v[172:175], v[204:207], 0
	v_mfma_f32_16x16x32_bf16 v[84:87], v[180:183], v[204:207], 0
	v_mfma_f32_16x16x32_bf16 v[64:67], v[172:175], v[212:215], 0
	v_mfma_f32_16x16x32_bf16 v[68:71], v[180:183], v[212:215], 0
	v_mfma_f32_16x16x32_bf16 v[112:115], v[176:179], v[192:195], v[112:115]
	v_mfma_f32_16x16x32_bf16 v[116:119], v[184:187], v[192:195], v[116:119]
	v_mfma_f32_16x16x32_bf16 v[96:99], v[176:179], v[200:203], v[96:99]
	v_mfma_f32_16x16x32_bf16 v[100:103], v[184:187], v[200:203], v[100:103]
	v_mfma_f32_16x16x32_bf16 v[80:83], v[176:179], v[208:211], v[80:83]
	v_mfma_f32_16x16x32_bf16 v[84:87], v[184:187], v[208:211], v[84:87]
	v_mfma_f32_16x16x32_bf16 v[64:67], v[176:179], v[216:219], v[64:67]
	v_mfma_f32_16x16x32_bf16 v[68:71], v[184:187], v[216:219], v[68:71]
	s_setprio 0
	s_barrier
	s_mov_b32 m0, s24
	s_mov_b32 s6, s38
	s_mov_b32 s7, s39
	ds_read_b128 v[188:191], v162 offset:16384
	ds_read_b128 v[192:195], v162 offset:17408
	ds_read_b128 v[196:199], v162 offset:18432
	ds_read_b128 v[200:203], v162 offset:19456
	ds_read_b128 v[204:207], v162 offset:20480
	ds_read_b128 v[208:211], v162 offset:21504
	ds_read_b128 v[212:215], v162 offset:22528
	ds_read_b128 v[216:219], v162 offset:23552
	buffer_load_dwordx4 v141, s[4:7], s55 offen lds
	s_mov_b32 m0, s25
	s_add_i32 s66, s55, s22
	buffer_load_dwordx4 v149, s[4:7], s55 offen lds
	s_mov_b32 m0, s26
	s_nop 0
	buffer_load_dwordx4 v141, s[4:7], s66 offen lds
	s_mov_b32 m0, s27
	s_nop 0
	buffer_load_dwordx4 v149, s[4:7], s66 offen lds
	s_mov_b32 m0, s23
	s_nop 0
	buffer_load_dwordx4 v137, s[36:39], s65 offen lds
	s_mov_b32 m0, s28
	s_nop 0
	buffer_load_dwordx4 v145, s[36:39], s65 offen lds
	s_waitcnt vmcnt(8)
	s_waitcnt lgkmcnt(0)
	s_barrier
	s_setprio 1
	v_mfma_f32_16x16x32_bf16 v[56:59], v[128:131], v[188:191], 0
	v_mfma_f32_16x16x32_bf16 v[60:63], v[164:167], v[188:191], 0
	v_mfma_f32_16x16x32_bf16 v[40:43], v[128:131], v[196:199], 0
	v_mfma_f32_16x16x32_bf16 v[44:47], v[164:167], v[196:199], 0
	v_mfma_f32_16x16x32_bf16 v[24:27], v[128:131], v[204:207], 0
	v_mfma_f32_16x16x32_bf16 v[28:31], v[164:167], v[204:207], 0
	v_mfma_f32_16x16x32_bf16 v[8:11], v[128:131], v[212:215], 0
	v_mfma_f32_16x16x32_bf16 v[12:15], v[164:167], v[212:215], 0
	v_mfma_f32_16x16x32_bf16 v[56:59], v[132:135], v[192:195], v[56:59]
	v_mfma_f32_16x16x32_bf16 v[60:63], v[168:171], v[192:195], v[60:63]
	v_mfma_f32_16x16x32_bf16 v[40:43], v[132:135], v[200:203], v[40:43]
	v_mfma_f32_16x16x32_bf16 v[44:47], v[168:171], v[200:203], v[44:47]
	v_mfma_f32_16x16x32_bf16 v[24:27], v[132:135], v[208:211], v[24:27]
	v_mfma_f32_16x16x32_bf16 v[28:31], v[168:171], v[208:211], v[28:31]
	v_mfma_f32_16x16x32_bf16 v[8:11], v[132:135], v[216:219], v[8:11]
	v_mfma_f32_16x16x32_bf16 v[12:15], v[168:171], v[216:219], v[12:15]
	v_mfma_f32_16x16x32_bf16 v[48:51], v[172:175], v[188:191], 0
	v_mfma_f32_16x16x32_bf16 v[52:55], v[180:183], v[188:191], 0
	v_mfma_f32_16x16x32_bf16 v[32:35], v[172:175], v[196:199], 0
	v_mfma_f32_16x16x32_bf16 v[36:39], v[180:183], v[196:199], 0
	v_mfma_f32_16x16x32_bf16 v[16:19], v[172:175], v[204:207], 0
	v_mfma_f32_16x16x32_bf16 v[20:23], v[180:183], v[204:207], 0
	v_mfma_f32_16x16x32_bf16 v[4:7], v[172:175], v[212:215], 0
	v_mfma_f32_16x16x32_bf16 v[0:3], v[180:183], v[212:215], 0
	v_mfma_f32_16x16x32_bf16 v[48:51], v[176:179], v[192:195], v[48:51]
	v_mfma_f32_16x16x32_bf16 v[52:55], v[184:187], v[192:195], v[52:55]
	v_mfma_f32_16x16x32_bf16 v[32:35], v[176:179], v[200:203], v[32:35]
	v_mfma_f32_16x16x32_bf16 v[36:39], v[184:187], v[200:203], v[36:39]
	v_mfma_f32_16x16x32_bf16 v[16:19], v[176:179], v[208:211], v[16:19]
	v_mfma_f32_16x16x32_bf16 v[20:23], v[184:187], v[208:211], v[20:23]
	v_mfma_f32_16x16x32_bf16 v[4:7], v[176:179], v[216:219], v[4:7]
	v_mfma_f32_16x16x32_bf16 v[0:3], v[184:187], v[216:219], v[0:3]
	s_setprio 0
	s_barrier
; #define PG8_STAGE(bufoff, rs_, soff_, voff) do { _Pragma("unroll") for (int _i = 0; _i < 2; ++_i) \
;         __builtin_amdgcn_raw_ptr_buffer_load_lds(rs_, (LAS void*)(lds + (bufoff) + ldsw + _i * 8192), 16, (int)(voff)[_i], (int)(soff_), 0, 0); } while (0)
; #define PG8_LDA(dst, b, h) do { _Pragma("unroll") for (int m = 0; m < 4; ++m) dst[m] = PG8_LD2(lds + PG8_SA(b, h) + aoff + m * 2048); } while (0)
; #define PG8_LDB(dst, b, h) do { _Pragma("unroll") for (int n = 0; n < 2; ++n) dst[n] = PG8_LD2(lds + PG8_SB(b, h) + boff + n * 2048); } while (0)
; #define PG8_WAIT_V(n) asm volatile("s_waitcnt vmcnt(" #n ")" ::: "memory")
; #define PG8_WAIT_L(n) asm volatile("s_waitcnt lgkmcnt(" #n ")" ::: "memory")
; #define PG8_BAR __builtin_amdgcn_s_barrier()
; #define PG8_SCHED __builtin_amdgcn_sched_barrier(0)
; template <class Epi, class Sched, bool ALIGN_EPI = false, bool SP2 = false, bool FP8 = false>
; __device__ __forceinline__ void gemm_phase(LAS unsigned char* lds, const Gemm g, const Sched& S, const Epi& E, int wbase) {
;     ...
;             PG8_LDB(B0, 1, 0); PG8_LDB(B1, 1, 1); PG8_SCHED; PG8_LDA(At, 1, 0); PG8_STAGE(PG8_SA(0, 1), rA2, a2 + hstep, voffA);
;             PG8_WAIT_V(8); PG8_WAIT_L(0); PG8_BAR; PG8_MMA(0, 0, At, B0); PG8_MMA(0, 1, At, B1); PG8_BAR; PG8_SCHED;
;             PG8_LDA(At, 1, 1); PG8_STAGE(PG8_SB(1, 0), rB2, b3, voffB); PG8_STAGE(PG8_SB(1, 1), rB2, b3 + hstep, voffB); PG8_STAGE(PG8_SA(1, 0), rA2, a3, voffA);
;             PG8_WAIT_V(8); PG8_WAIT_L(0); PG8_BAR; PG8_MMA(1, 0, At, B0); PG8_MMA(1, 1, At, B1); PG8_BAR; PG8_SCHED;
	v_add_u32_e32 v136, 0x18000, v161
	ds_read_b128 v[128:131], v136
	ds_read_b128 v[132:135], v136 offset:1024
	ds_read_b128 v[164:167], v136 offset:2048
	ds_read_b128 v[168:171], v136 offset:3072
	v_add_u32_e32 v136, 0x1c000, v161
	ds_read_b128 v[172:175], v136
	ds_read_b128 v[176:179], v136 offset:1024
	ds_read_b128 v[180:183], v136 offset:2048
	ds_read_b128 v[184:187], v136 offset:3072
	s_add_i32 s65, s65, s22
	s_mov_b32 m0, s29
	ds_read_b128 v[188:191], v162 offset:32768
	ds_read_b128 v[192:195], v162 offset:33792
	ds_read_b128 v[196:199], v162 offset:34816
	ds_read_b128 v[200:203], v162 offset:35840
	ds_read_b128 v[204:207], v162 offset:36864
	ds_read_b128 v[208:211], v162 offset:37888
	ds_read_b128 v[212:215], v162 offset:38912
	ds_read_b128 v[216:219], v162 offset:39936
	buffer_load_dwordx4 v137, s[36:39], s65 offen lds
	s_mov_b32 m0, s30
	s_nop 0
	buffer_load_dwordx4 v145, s[36:39], s65 offen lds
	s_waitcnt vmcnt(8)
	s_waitcnt lgkmcnt(0)
	s_barrier
	s_setprio 1
	v_mfma_f32_16x16x32_bf16 v[120:123], v[128:131], v[188:191], v[120:123]
	v_mfma_f32_16x16x32_bf16 v[124:127], v[164:167], v[188:191], v[124:127]
	v_mfma_f32_16x16x32_bf16 v[104:107], v[128:131], v[196:199], v[104:107]
	v_mfma_f32_16x16x32_bf16 v[108:111], v[164:167], v[196:199], v[108:111]
	v_mfma_f32_16x16x32_bf16 v[88:91], v[128:131], v[204:207], v[88:91]
	v_mfma_f32_16x16x32_bf16 v[92:95], v[164:167], v[204:207], v[92:95]
	v_mfma_f32_16x16x32_bf16 v[72:75], v[128:131], v[212:215], v[72:75]
	v_mfma_f32_16x16x32_bf16 v[76:79], v[164:167], v[212:215], v[76:79]
	v_mfma_f32_16x16x32_bf16 v[120:123], v[132:135], v[192:195], v[120:123]
	v_mfma_f32_16x16x32_bf16 v[124:127], v[168:171], v[192:195], v[124:127]
	v_mfma_f32_16x16x32_bf16 v[104:107], v[132:135], v[200:203], v[104:107]
	v_mfma_f32_16x16x32_bf16 v[108:111], v[168:171], v[200:203], v[108:111]
	v_mfma_f32_16x16x32_bf16 v[88:91], v[132:135], v[208:211], v[88:91]
	v_mfma_f32_16x16x32_bf16 v[92:95], v[168:171], v[208:211], v[92:95]
	v_mfma_f32_16x16x32_bf16 v[72:75], v[132:135], v[216:219], v[72:75]
	v_mfma_f32_16x16x32_bf16 v[76:79], v[168:171], v[216:219], v[76:79]
	v_mfma_f32_16x16x32_bf16 v[112:115], v[172:175], v[188:191], v[112:115]
	v_mfma_f32_16x16x32_bf16 v[116:119], v[180:183], v[188:191], v[116:119]
	v_mfma_f32_16x16x32_bf16 v[96:99], v[172:175], v[196:199], v[96:99]
	v_mfma_f32_16x16x32_bf16 v[100:103], v[180:183], v[196:199], v[100:103]
	v_mfma_f32_16x16x32_bf16 v[80:83], v[172:175], v[204:207], v[80:83]
	v_mfma_f32_16x16x32_bf16 v[84:87], v[180:183], v[204:207], v[84:87]
	v_mfma_f32_16x16x32_bf16 v[64:67], v[172:175], v[212:215], v[64:67]
	v_mfma_f32_16x16x32_bf16 v[68:71], v[180:183], v[212:215], v[68:71]
	v_mfma_f32_16x16x32_bf16 v[112:115], v[176:179], v[192:195], v[112:115]
	v_mfma_f32_16x16x32_bf16 v[116:119], v[184:187], v[192:195], v[116:119]
	v_mfma_f32_16x16x32_bf16 v[96:99], v[176:179], v[200:203], v[96:99]
	v_mfma_f32_16x16x32_bf16 v[100:103], v[184:187], v[200:203], v[100:103]
	v_mfma_f32_16x16x32_bf16 v[80:83], v[176:179], v[208:211], v[80:83]
	v_mfma_f32_16x16x32_bf16 v[84:87], v[184:187], v[208:211], v[84:87]
	v_mfma_f32_16x16x32_bf16 v[64:67], v[176:179], v[216:219], v[64:67]
	v_mfma_f32_16x16x32_bf16 v[68:71], v[184:187], v[216:219], v[68:71]
	s_setprio 0
	s_barrier
	s_mov_b32 m0, s31
	s_bitset1_b32 s55, 7
	ds_read_b128 v[188:191], v162 offset:49152
	ds_read_b128 v[192:195], v162 offset:50176
	ds_read_b128 v[196:199], v162 offset:51200
	ds_read_b128 v[200:203], v162 offset:52224
	ds_read_b128 v[204:207], v162 offset:53248
	ds_read_b128 v[208:211], v162 offset:54272
	ds_read_b128 v[212:215], v162 offset:55296
	ds_read_b128 v[216:219], v162 offset:56320
	buffer_load_dwordx4 v141, s[4:7], s55 offen lds
	s_mov_b32 m0, s33
	s_nop 0
	buffer_load_dwordx4 v149, s[4:7], s55 offen lds
	s_add_i32 s55, s55, s22
	s_mov_b32 m0, s41
	s_nop 0
	buffer_load_dwordx4 v141, s[4:7], s55 offen lds
	s_mov_b32 m0, s42
	s_nop 0
	buffer_load_dwordx4 v149, s[4:7], s55 offen lds
	s_mov_b32 m0, s34
	s_nop 0
	buffer_load_dwordx4 v137, s[36:39], s54 offen lds
	s_mov_b32 m0, s35
	s_nop 0
	buffer_load_dwordx4 v145, s[36:39], s54 offen lds
	s_waitcnt vmcnt(8)
	s_waitcnt lgkmcnt(0)
	s_barrier
	s_setprio 1
	v_mfma_f32_16x16x32_bf16 v[56:59], v[128:131], v[188:191], v[56:59]
	v_mfma_f32_16x16x32_bf16 v[60:63], v[164:167], v[188:191], v[60:63]
	v_mfma_f32_16x16x32_bf16 v[40:43], v[128:131], v[196:199], v[40:43]
	v_mfma_f32_16x16x32_bf16 v[44:47], v[164:167], v[196:199], v[44:47]
	v_mfma_f32_16x16x32_bf16 v[24:27], v[128:131], v[204:207], v[24:27]
	v_mfma_f32_16x16x32_bf16 v[28:31], v[164:167], v[204:207], v[28:31]
	v_mfma_f32_16x16x32_bf16 v[8:11], v[128:131], v[212:215], v[8:11]
	v_mfma_f32_16x16x32_bf16 v[12:15], v[164:167], v[212:215], v[12:15]
	v_mfma_f32_16x16x32_bf16 v[56:59], v[132:135], v[192:195], v[56:59]
	v_mfma_f32_16x16x32_bf16 v[60:63], v[168:171], v[192:195], v[60:63]
	v_mfma_f32_16x16x32_bf16 v[40:43], v[132:135], v[200:203], v[40:43]
	v_mfma_f32_16x16x32_bf16 v[44:47], v[168:171], v[200:203], v[44:47]
	v_mfma_f32_16x16x32_bf16 v[24:27], v[132:135], v[208:211], v[24:27]
	v_mfma_f32_16x16x32_bf16 v[28:31], v[168:171], v[208:211], v[28:31]
	v_mfma_f32_16x16x32_bf16 v[8:11], v[132:135], v[216:219], v[8:11]
	v_mfma_f32_16x16x32_bf16 v[12:15], v[168:171], v[216:219], v[12:15]
	v_mfma_f32_16x16x32_bf16 v[48:51], v[172:175], v[188:191], v[48:51]
	v_mfma_f32_16x16x32_bf16 v[52:55], v[180:183], v[188:191], v[52:55]
	v_mfma_f32_16x16x32_bf16 v[32:35], v[172:175], v[196:199], v[32:35]
	v_mfma_f32_16x16x32_bf16 v[36:39], v[180:183], v[196:199], v[36:39]
	v_mfma_f32_16x16x32_bf16 v[16:19], v[172:175], v[204:207], v[16:19]
	v_mfma_f32_16x16x32_bf16 v[20:23], v[180:183], v[204:207], v[20:23]
	v_mfma_f32_16x16x32_bf16 v[4:7], v[172:175], v[212:215], v[4:7]
	v_mfma_f32_16x16x32_bf16 v[0:3], v[180:183], v[212:215], v[0:3]
	v_mfma_f32_16x16x32_bf16 v[48:51], v[176:179], v[192:195], v[48:51]
	v_mfma_f32_16x16x32_bf16 v[52:55], v[184:187], v[192:195], v[52:55]
	v_mfma_f32_16x16x32_bf16 v[32:35], v[176:179], v[200:203], v[32:35]
	v_mfma_f32_16x16x32_bf16 v[36:39], v[184:187], v[200:203], v[36:39]
	v_mfma_f32_16x16x32_bf16 v[16:19], v[176:179], v[208:211], v[16:19]
	v_mfma_f32_16x16x32_bf16 v[20:23], v[184:187], v[208:211], v[20:23]
	v_mfma_f32_16x16x32_bf16 v[4:7], v[176:179], v[216:219], v[4:7]
	v_mfma_f32_16x16x32_bf16 v[0:3], v[184:187], v[216:219], v[0:3]
	s_setprio 0
	s_barrier
	s_add_i32 s63, s63, 2
	s_addk_i32 s61, 0x100
	s_addk_i32 s62, 0x100
	s_cmp_ge_i32 s63, s44
	s_cbranch_scc0 .LBB0_1628
	s_branch .Lzp_after_1628

; #define PG8_BAR __builtin_amdgcn_s_barrier()
; template <class Epi, class Sched, bool ALIGN_EPI = false, bool SP2 = false, bool FP8 = false>
; __device__ __forceinline__ void gemm_phase(LAS unsigned char* lds, const Gemm g, const Sched& S, const Epi& E, int wbase) {
;     ...
;         if constexpr (ALIGN_EPI) { if (wr == 0) PG8_BAR; }
;         { int fr_ = fr, fq_ = fq; asm volatile("" : "+v"(fr_), "+v"(fq_));
;           if constexpr (Epi::HAS_PRE) E(acc, cur, wr, wc, fr_, fq_, pre_); else E(acc, cur, wr, wc, fr_, fq_); } S.done(cur);
.Lzp_after_1628:
	s_and_b64 vcc, exec, s[14:15]
	s_cbranch_vccz .LBB0_1631

; #define PG8_STAGE(bufoff, rs_, soff_, voff) do { _Pragma("unroll") for (int _i = 0; _i < 2; ++_i) \
;         __builtin_amdgcn_raw_ptr_buffer_load_lds(rs_, (LAS void*)(lds + (bufoff) + ldsw + _i * 8192), 16, (int)(voff)[_i], (int)(soff_), 0, 0); } while (0)
; #define PG8_LDA(dst, b, h) do { _Pragma("unroll") for (int m = 0; m < 4; ++m) dst[m] = PG8_LD2(lds + PG8_SA(b, h) + aoff + m * 2048); } while (0)
; #define PG8_LDB(dst, b, h) do { _Pragma("unroll") for (int n = 0; n < 2; ++n) dst[n] = PG8_LD2(lds + PG8_SB(b, h) + boff + n * 2048); } while (0)
; #define PG8_WAIT_V(n) asm volatile("s_waitcnt vmcnt(" #n ")" ::: "memory")
; #define PG8_WAIT_L(n) asm volatile("s_waitcnt lgkmcnt(" #n ")" ::: "memory")
; #define PG8_BAR __builtin_amdgcn_s_barrier()
; #define PG8_SCHED __builtin_amdgcn_sched_barrier(0)
; template <class Epi, class Sched, bool ALIGN_EPI = false, bool SP2 = false, bool FP8 = false>
; __device__ __forceinline__ void gemm_phase(LAS unsigned char* lds, const Gemm g, const Sched& S, const Epi& E, int wbase) {
;     ...
;             const unsigned a2 = last ? nA : cA + (unsigned)(t + 2) * kstep, b2 = last ? nB : cB + (unsigned)(t + 2) * kstep; const rsrc_t rA2 = (Sched::TWO && last) ? rAn : rAc, rB2 = (Sched::TWO && last) ? rBn : rBc;
;             const unsigned a3 = a2 + kstep, b3 = b2 + kstep;
;             if (last && has_next) S.a_ready(nxt);
;             if constexpr (SP2) {
;             PG8_LDB(B0, 0, 0); PG8_LDB(B1, 0, 1); PG8_SCHED; PG8_LDA(At, 0, 0); PG8_STAGE(PG8_SA(1, 1), rAc, a1 + hstep, voffA);
;             PG8_WAIT_V(8); PG8_WAIT_L(0); PG8_BAR; PG8_MMA(0, 0, At, B0); PG8_MMA(0, 1, At, B1); PG8_BAR; PG8_SCHED;
;             PG8_LDA(At, 0, 1); PG8_STAGE(PG8_SB(0, 0), rB2, b2, voffB); PG8_STAGE(PG8_SB(0, 1), rB2, b2 + hstep, voffB); PG8_STAGE(PG8_SA(0, 0), rA2, a2, voffA);
;             PG8_WAIT_V(8); PG8_WAIT_L(0); PG8_BAR; PG8_MMA(1, 0, At, B0); PG8_MMA(1, 1, At, B1); PG8_BAR; PG8_SCHED;
.LBB0_1699:
	s_mul_i32 s61, s60, 0x1c0000
	s_andn2_b64 vcc, exec, s[14:15]
	s_mul_i32 s62, s59, 0x1c0000
	s_cbranch_vccnz .LBB0_1703
	s_and_b64 s[6:7], s[18:19], exec
	s_waitcnt vmcnt(37)
	s_waitcnt vmcnt(36)
	s_waitcnt vmcnt(35)
	s_waitcnt vmcnt(32)
	s_waitcnt vmcnt(31)
	s_waitcnt vmcnt(28)
	s_waitcnt vmcnt(27)
	s_waitcnt vmcnt(23)
	s_waitcnt vmcnt(22)
	s_cselect_b32 s21, s61, s55
	s_cselect_b32 s63, s62, s54
	s_add_i32 s65, s55, 0x80
	s_add_i32 s66, s54, 0x100
	s_mov_b32 s67, 0
	v_add_u32_e32 v140, 0x10000, v176
	v_add_u32_e32 v156, 0x14000, v176
	ds_read_b128 v[112:115], v140
	ds_read_b128 v[124:127], v140 offset:1024
	ds_read_b128 v[136:139], v140 offset:2048
	ds_read_b128 v[140:143], v140 offset:3072
	ds_read_b128 v[144:147], v156
	ds_read_b128 v[148:151], v156 offset:1024
	ds_read_b128 v[152:155], v156 offset:2048
	ds_read_b128 v[156:159], v156 offset:3072
	s_add_i32 s6, s65, 0x80
	s_cmp_eq_u32 s52, s67
	s_cselect_b32 s68, s21, s6
	s_cselect_b32 s55, s63, s66
	s_or_b32 s54, s68, 0x80
	s_add_i32 s6, s25, s65
	s_mov_b32 m0, s53
	ds_read_b128 v[160:163], v177
	ds_read_b128 v[164:167], v177 offset:1024
	ds_read_b128 v[178:181], v177 offset:2048
	ds_read_b128 v[182:185], v177 offset:3072
	ds_read_b128 v[186:189], v177 offset:4096
	ds_read_b128 v[190:193], v177 offset:5120
	ds_read_b128 v[194:197], v177 offset:6144
	ds_read_b128 v[198:201], v177 offset:7168
	buffer_load_dwordx4 v170, s[36:39], s6 offen lds
	s_mov_b32 m0, s56
	s_nop 0
	buffer_load_dwordx4 v172, s[36:39], s6 offen lds
	s_waitcnt vmcnt(8)
	s_waitcnt lgkmcnt(0)
	s_barrier
	s_setprio 1
	v_mfma_f32_16x16x32_bf16 v[132:135], v[112:115], v[160:163], 0
	v_mfma_f32_16x16x32_bf16 v[128:131], v[136:139], v[160:163], 0
	v_mfma_f32_16x16x32_bf16 v[108:111], v[112:115], v[178:181], 0
	v_mfma_f32_16x16x32_bf16 v[104:107], v[136:139], v[178:181], 0
	v_mfma_f32_16x16x32_bf16 v[92:95], v[112:115], v[186:189], 0
	v_mfma_f32_16x16x32_bf16 v[88:91], v[136:139], v[186:189], 0
	v_mfma_f32_16x16x32_bf16 v[76:79], v[112:115], v[194:197], 0
	v_mfma_f32_16x16x32_bf16 v[72:75], v[136:139], v[194:197], 0
	v_mfma_f32_16x16x32_bf16 v[132:135], v[124:127], v[164:167], v[132:135]
	v_mfma_f32_16x16x32_bf16 v[128:131], v[140:143], v[164:167], v[128:131]
	v_mfma_f32_16x16x32_bf16 v[108:111], v[124:127], v[182:185], v[108:111]
	v_mfma_f32_16x16x32_bf16 v[104:107], v[140:143], v[182:185], v[104:107]
	v_mfma_f32_16x16x32_bf16 v[92:95], v[124:127], v[190:193], v[92:95]
	v_mfma_f32_16x16x32_bf16 v[88:91], v[140:143], v[190:193], v[88:91]
	v_mfma_f32_16x16x32_bf16 v[76:79], v[124:127], v[198:201], v[76:79]
	v_mfma_f32_16x16x32_bf16 v[72:75], v[140:143], v[198:201], v[72:75]
	v_mfma_f32_16x16x32_bf16 v[120:123], v[144:147], v[160:163], 0
	v_mfma_f32_16x16x32_bf16 v[116:119], v[152:155], v[160:163], 0
	v_mfma_f32_16x16x32_bf16 v[100:103], v[144:147], v[178:181], 0
	v_mfma_f32_16x16x32_bf16 v[96:99], v[152:155], v[178:181], 0
	v_mfma_f32_16x16x32_bf16 v[84:87], v[144:147], v[186:189], 0
	v_mfma_f32_16x16x32_bf16 v[80:83], v[152:155], v[186:189], 0
	v_mfma_f32_16x16x32_bf16 v[68:71], v[144:147], v[194:197], 0
	v_mfma_f32_16x16x32_bf16 v[64:67], v[152:155], v[194:197], 0
	v_mfma_f32_16x16x32_bf16 v[120:123], v[148:151], v[164:167], v[120:123]
	v_mfma_f32_16x16x32_bf16 v[116:119], v[156:159], v[164:167], v[116:119]
	v_mfma_f32_16x16x32_bf16 v[100:103], v[148:151], v[182:185], v[100:103]
	v_mfma_f32_16x16x32_bf16 v[96:99], v[156:159], v[182:185], v[96:99]
	v_mfma_f32_16x16x32_bf16 v[84:87], v[148:151], v[190:193], v[84:87]
	v_mfma_f32_16x16x32_bf16 v[80:83], v[156:159], v[190:193], v[80:83]
	v_mfma_f32_16x16x32_bf16 v[68:71], v[148:151], v[198:201], v[68:71]
	v_mfma_f32_16x16x32_bf16 v[64:67], v[156:159], v[198:201], v[64:67]
	s_setprio 0
	s_barrier
	s_mov_b32 m0, s27
	s_mov_b32 s6, s38
	s_mov_b32 s7, s39
	ds_read_b128 v[160:163], v177 offset:16384
	ds_read_b128 v[164:167], v177 offset:17408
	ds_read_b128 v[178:181], v177 offset:18432
	ds_read_b128 v[182:185], v177 offset:19456
	ds_read_b128 v[186:189], v177 offset:20480
	ds_read_b128 v[190:193], v177 offset:21504
	ds_read_b128 v[194:197], v177 offset:22528
	ds_read_b128 v[198:201], v177 offset:23552
	buffer_load_dwordx4 v171, s[4:7], s55 offen lds
	s_mov_b32 m0, s28
	s_add_i32 s69, s55, s25
	buffer_load_dwordx4 v173, s[4:7], s55 offen lds
	s_mov_b32 m0, s29
	s_nop 0
	buffer_load_dwordx4 v171, s[4:7], s69 offen lds
	s_mov_b32 m0, s30
	s_nop 0
	buffer_load_dwordx4 v173, s[4:7], s69 offen lds
	s_mov_b32 m0, s26
	s_nop 0
	buffer_load_dwordx4 v170, s[36:39], s68 offen lds
	s_mov_b32 m0, s31
	s_nop 0
	buffer_load_dwordx4 v172, s[36:39], s68 offen lds
	s_waitcnt vmcnt(8)
	s_waitcnt lgkmcnt(0)
	s_barrier
; #define PG8_STAGE(bufoff, rs_, soff_, voff) do { _Pragma("unroll") for (int _i = 0; _i < 2; ++_i) \
;         __builtin_amdgcn_raw_ptr_buffer_load_lds(rs_, (LAS void*)(lds + (bufoff) + ldsw + _i * 8192), 16, (int)(voff)[_i], (int)(soff_), 0, 0); } while (0)
; #define PG8_LDA(dst, b, h) do { _Pragma("unroll") for (int m = 0; m < 4; ++m) dst[m] = PG8_LD2(lds + PG8_SA(b, h) + aoff + m * 2048); } while (0)
; #define PG8_LDB(dst, b, h) do { _Pragma("unroll") for (int n = 0; n < 2; ++n) dst[n] = PG8_LD2(lds + PG8_SB(b, h) + boff + n * 2048); } while (0)
; #define PG8_WAIT_V(n) asm volatile("s_waitcnt vmcnt(" #n ")" ::: "memory")
; #define PG8_WAIT_L(n) asm volatile("s_waitcnt lgkmcnt(" #n ")" ::: "memory")
; #define PG8_BAR __builtin_amdgcn_s_barrier()
; #define PG8_SCHED __builtin_amdgcn_sched_barrier(0)
; template <class Epi, class Sched, bool ALIGN_EPI = false, bool SP2 = false, bool FP8 = false>
; __device__ __forceinline__ void gemm_phase(LAS unsigned char* lds, const Gemm g, const Sched& S, const Epi& E, int wbase) {
;     ...
;             PG8_WAIT_V(8); PG8_WAIT_L(0); PG8_BAR; PG8_MMA(1, 0, At, B0); PG8_MMA(1, 1, At, B1); PG8_BAR; PG8_SCHED;
;             PG8_LDB(B0, 1, 0); PG8_LDB(B1, 1, 1); PG8_SCHED; PG8_LDA(At, 1, 0); PG8_STAGE(PG8_SA(0, 1), rA2, a2 + hstep, voffA);
;             PG8_WAIT_V(8); PG8_WAIT_L(0); PG8_BAR; PG8_MMA(0, 0, At, B0); PG8_MMA(0, 1, At, B1); PG8_BAR; PG8_SCHED;
	s_setprio 1
	v_mfma_f32_16x16x32_bf16 v[60:63], v[112:115], v[160:163], 0
	v_mfma_f32_16x16x32_bf16 v[56:59], v[136:139], v[160:163], 0
	v_mfma_f32_16x16x32_bf16 v[44:47], v[112:115], v[178:181], 0
	v_mfma_f32_16x16x32_bf16 v[40:43], v[136:139], v[178:181], 0
	v_mfma_f32_16x16x32_bf16 v[28:31], v[112:115], v[186:189], 0
	v_mfma_f32_16x16x32_bf16 v[24:27], v[136:139], v[186:189], 0
	v_mfma_f32_16x16x32_bf16 v[12:15], v[112:115], v[194:197], 0
	v_mfma_f32_16x16x32_bf16 v[8:11], v[136:139], v[194:197], 0
	v_mfma_f32_16x16x32_bf16 v[60:63], v[124:127], v[164:167], v[60:63]
	v_mfma_f32_16x16x32_bf16 v[56:59], v[140:143], v[164:167], v[56:59]
	v_mfma_f32_16x16x32_bf16 v[44:47], v[124:127], v[182:185], v[44:47]
	v_mfma_f32_16x16x32_bf16 v[40:43], v[140:143], v[182:185], v[40:43]
	v_mfma_f32_16x16x32_bf16 v[28:31], v[124:127], v[190:193], v[28:31]
	v_mfma_f32_16x16x32_bf16 v[24:27], v[140:143], v[190:193], v[24:27]
	v_mfma_f32_16x16x32_bf16 v[12:15], v[124:127], v[198:201], v[12:15]
	v_mfma_f32_16x16x32_bf16 v[8:11], v[140:143], v[198:201], v[8:11]
	v_mfma_f32_16x16x32_bf16 v[52:55], v[144:147], v[160:163], 0
	v_mfma_f32_16x16x32_bf16 v[48:51], v[152:155], v[160:163], 0
	v_mfma_f32_16x16x32_bf16 v[36:39], v[144:147], v[178:181], 0
	v_mfma_f32_16x16x32_bf16 v[32:35], v[152:155], v[178:181], 0
	v_mfma_f32_16x16x32_bf16 v[20:23], v[144:147], v[186:189], 0
	v_mfma_f32_16x16x32_bf16 v[16:19], v[152:155], v[186:189], 0
	v_mfma_f32_16x16x32_bf16 v[4:7], v[144:147], v[194:197], 0
	v_mfma_f32_16x16x32_bf16 v[0:3], v[152:155], v[194:197], 0
	v_mfma_f32_16x16x32_bf16 v[52:55], v[148:151], v[164:167], v[52:55]
	v_mfma_f32_16x16x32_bf16 v[48:51], v[156:159], v[164:167], v[48:51]
	v_mfma_f32_16x16x32_bf16 v[36:39], v[148:151], v[182:185], v[36:39]
	v_mfma_f32_16x16x32_bf16 v[32:35], v[156:159], v[182:185], v[32:35]
	v_mfma_f32_16x16x32_bf16 v[20:23], v[148:151], v[190:193], v[20:23]
	v_mfma_f32_16x16x32_bf16 v[16:19], v[156:159], v[190:193], v[16:19]
	v_mfma_f32_16x16x32_bf16 v[4:7], v[148:151], v[198:201], v[4:7]
	v_mfma_f32_16x16x32_bf16 v[0:3], v[156:159], v[198:201], v[0:3]
	s_setprio 0
	s_barrier
	v_add_u32_e32 v140, 0x18000, v176
	v_add_u32_e32 v156, 0x1c000, v176
	ds_read_b128 v[112:115], v140
	ds_read_b128 v[124:127], v140 offset:1024
	ds_read_b128 v[136:139], v140 offset:2048
	ds_read_b128 v[140:143], v140 offset:3072
	ds_read_b128 v[144:147], v156
	ds_read_b128 v[148:151], v156 offset:1024
	ds_read_b128 v[152:155], v156 offset:2048
	ds_read_b128 v[156:159], v156 offset:3072
	s_add_i32 s68, s68, s25
	s_mov_b32 m0, s33
	ds_read_b128 v[160:163], v177 offset:32768
	ds_read_b128 v[164:167], v177 offset:33792
	ds_read_b128 v[178:181], v177 offset:34816
	ds_read_b128 v[182:185], v177 offset:35840
	ds_read_b128 v[186:189], v177 offset:36864
	ds_read_b128 v[190:193], v177 offset:37888
	ds_read_b128 v[194:197], v177 offset:38912
	ds_read_b128 v[198:201], v177 offset:39936
	buffer_load_dwordx4 v170, s[36:39], s68 offen lds
	s_mov_b32 m0, s34
	s_nop 0
	buffer_load_dwordx4 v172, s[36:39], s68 offen lds
	s_waitcnt vmcnt(8)
	s_waitcnt lgkmcnt(0)
	s_barrier
	s_setprio 1
	v_mfma_f32_16x16x32_bf16 v[132:135], v[112:115], v[160:163], v[132:135]
	v_mfma_f32_16x16x32_bf16 v[128:131], v[136:139], v[160:163], v[128:131]
	v_mfma_f32_16x16x32_bf16 v[108:111], v[112:115], v[178:181], v[108:111]
	v_mfma_f32_16x16x32_bf16 v[104:107], v[136:139], v[178:181], v[104:107]
	v_mfma_f32_16x16x32_bf16 v[92:95], v[112:115], v[186:189], v[92:95]
	v_mfma_f32_16x16x32_bf16 v[88:91], v[136:139], v[186:189], v[88:91]
	v_mfma_f32_16x16x32_bf16 v[76:79], v[112:115], v[194:197], v[76:79]
	v_mfma_f32_16x16x32_bf16 v[72:75], v[136:139], v[194:197], v[72:75]
	v_mfma_f32_16x16x32_bf16 v[132:135], v[124:127], v[164:167], v[132:135]
	v_mfma_f32_16x16x32_bf16 v[128:131], v[140:143], v[164:167], v[128:131]
	v_mfma_f32_16x16x32_bf16 v[108:111], v[124:127], v[182:185], v[108:111]
	v_mfma_f32_16x16x32_bf16 v[104:107], v[140:143], v[182:185], v[104:107]
	v_mfma_f32_16x16x32_bf16 v[92:95], v[124:127], v[190:193], v[92:95]
	v_mfma_f32_16x16x32_bf16 v[88:91], v[140:143], v[190:193], v[88:91]
	v_mfma_f32_16x16x32_bf16 v[76:79], v[124:127], v[198:201], v[76:79]
	v_mfma_f32_16x16x32_bf16 v[72:75], v[140:143], v[198:201], v[72:75]
	v_mfma_f32_16x16x32_bf16 v[120:123], v[144:147], v[160:163], v[120:123]
	v_mfma_f32_16x16x32_bf16 v[116:119], v[152:155], v[160:163], v[116:119]
	v_mfma_f32_16x16x32_bf16 v[100:103], v[144:147], v[178:181], v[100:103]
	v_mfma_f32_16x16x32_bf16 v[96:99], v[152:155], v[178:181], v[96:99]
	v_mfma_f32_16x16x32_bf16 v[84:87], v[144:147], v[186:189], v[84:87]
	v_mfma_f32_16x16x32_bf16 v[80:83], v[152:155], v[186:189], v[80:83]
	v_mfma_f32_16x16x32_bf16 v[68:71], v[144:147], v[194:197], v[68:71]
	v_mfma_f32_16x16x32_bf16 v[64:67], v[152:155], v[194:197], v[64:67]
	v_mfma_f32_16x16x32_bf16 v[120:123], v[148:151], v[164:167], v[120:123]
	v_mfma_f32_16x16x32_bf16 v[116:119], v[156:159], v[164:167], v[116:119]
	v_mfma_f32_16x16x32_bf16 v[100:103], v[148:151], v[182:185], v[100:103]
	v_mfma_f32_16x16x32_bf16 v[96:99], v[156:159], v[182:185], v[96:99]
	v_mfma_f32_16x16x32_bf16 v[84:87], v[148:151], v[190:193], v[84:87]
	v_mfma_f32_16x16x32_bf16 v[80:83], v[156:159], v[190:193], v[80:83]
	v_mfma_f32_16x16x32_bf16 v[68:71], v[148:151], v[198:201], v[68:71]
	v_mfma_f32_16x16x32_bf16 v[64:67], v[156:159], v[198:201], v[64:67]
	s_setprio 0
	s_barrier
; #define PG8_STAGE(bufoff, rs_, soff_, voff) do { _Pragma("unroll") for (int _i = 0; _i < 2; ++_i) \
;         __builtin_amdgcn_raw_ptr_buffer_load_lds(rs_, (LAS void*)(lds + (bufoff) + ldsw + _i * 8192), 16, (int)(voff)[_i], (int)(soff_), 0, 0); } while (0)
; #define PG8_LDA(dst, b, h) do { _Pragma("unroll") for (int m = 0; m < 4; ++m) dst[m] = PG8_LD2(lds + PG8_SA(b, h) + aoff + m * 2048); } while (0)
; #define PG8_WAIT_V(n) asm volatile("s_waitcnt vmcnt(" #n ")" ::: "memory")
; #define PG8_WAIT_L(n) asm volatile("s_waitcnt lgkmcnt(" #n ")" ::: "memory")
; #define PG8_BAR __builtin_amdgcn_s_barrier()
; #define PG8_SCHED __builtin_amdgcn_sched_barrier(0)
; template <class Epi, class Sched, bool ALIGN_EPI = false, bool SP2 = false, bool FP8 = false>
; __device__ __forceinline__ void gemm_phase(LAS unsigned char* lds, const Gemm g, const Sched& S, const Epi& E, int wbase) {
;     ...
;             PG8_LDA(At, 1, 1); PG8_STAGE(PG8_SB(1, 0), rB2, b3, voffB); PG8_STAGE(PG8_SB(1, 1), rB2, b3 + hstep, voffB); PG8_STAGE(PG8_SA(1, 0), rA2, a3, voffA);
;             PG8_WAIT_V(8); PG8_WAIT_L(0); PG8_BAR; PG8_MMA(1, 0, At, B0); PG8_MMA(1, 1, At, B1); PG8_BAR; PG8_SCHED;
	s_mov_b32 m0, s1
	s_bitset1_b32 s55, 7
	ds_read_b128 v[160:163], v177 offset:49152
	ds_read_b128 v[164:167], v177 offset:50176
	ds_read_b128 v[178:181], v177 offset:51200
	ds_read_b128 v[182:185], v177 offset:52224
	ds_read_b128 v[186:189], v177 offset:53248
	ds_read_b128 v[190:193], v177 offset:54272
	ds_read_b128 v[194:197], v177 offset:55296
	ds_read_b128 v[198:201], v177 offset:56320
	buffer_load_dwordx4 v171, s[4:7], s55 offen lds
	s_mov_b32 m0, s35
	s_nop 0
	buffer_load_dwordx4 v173, s[4:7], s55 offen lds
	s_add_i32 s55, s55, s25
	s_mov_b32 m0, s43
	s_nop 0
	buffer_load_dwordx4 v171, s[4:7], s55 offen lds
	s_mov_b32 m0, s44
	s_nop 0
	buffer_load_dwordx4 v173, s[4:7], s55 offen lds
	s_mov_b32 m0, s41
	s_nop 0
	buffer_load_dwordx4 v170, s[36:39], s54 offen lds
	s_mov_b32 m0, s42
	s_nop 0
	buffer_load_dwordx4 v172, s[36:39], s54 offen lds
	s_waitcnt vmcnt(8)
	s_waitcnt lgkmcnt(0)
	s_barrier
	s_setprio 1
	v_mfma_f32_16x16x32_bf16 v[60:63], v[112:115], v[160:163], v[60:63]
	v_mfma_f32_16x16x32_bf16 v[56:59], v[136:139], v[160:163], v[56:59]
	v_mfma_f32_16x16x32_bf16 v[44:47], v[112:115], v[178:181], v[44:47]
	v_mfma_f32_16x16x32_bf16 v[40:43], v[136:139], v[178:181], v[40:43]
	v_mfma_f32_16x16x32_bf16 v[28:31], v[112:115], v[186:189], v[28:31]
	v_mfma_f32_16x16x32_bf16 v[24:27], v[136:139], v[186:189], v[24:27]
	v_mfma_f32_16x16x32_bf16 v[12:15], v[112:115], v[194:197], v[12:15]
	v_mfma_f32_16x16x32_bf16 v[8:11], v[136:139], v[194:197], v[8:11]
	v_mfma_f32_16x16x32_bf16 v[60:63], v[124:127], v[164:167], v[60:63]
	v_mfma_f32_16x16x32_bf16 v[56:59], v[140:143], v[164:167], v[56:59]
	v_mfma_f32_16x16x32_bf16 v[44:47], v[124:127], v[182:185], v[44:47]
	v_mfma_f32_16x16x32_bf16 v[40:43], v[140:143], v[182:185], v[40:43]
	v_mfma_f32_16x16x32_bf16 v[28:31], v[124:127], v[190:193], v[28:31]
	v_mfma_f32_16x16x32_bf16 v[24:27], v[140:143], v[190:193], v[24:27]
	v_mfma_f32_16x16x32_bf16 v[12:15], v[124:127], v[198:201], v[12:15]
	v_mfma_f32_16x16x32_bf16 v[8:11], v[140:143], v[198:201], v[8:11]
	v_mfma_f32_16x16x32_bf16 v[52:55], v[144:147], v[160:163], v[52:55]
	v_mfma_f32_16x16x32_bf16 v[48:51], v[152:155], v[160:163], v[48:51]
	v_mfma_f32_16x16x32_bf16 v[36:39], v[144:147], v[178:181], v[36:39]
	v_mfma_f32_16x16x32_bf16 v[32:35], v[152:155], v[178:181], v[32:35]
	v_mfma_f32_16x16x32_bf16 v[20:23], v[144:147], v[186:189], v[20:23]
	v_mfma_f32_16x16x32_bf16 v[16:19], v[152:155], v[186:189], v[16:19]
	v_mfma_f32_16x16x32_bf16 v[4:7], v[144:147], v[194:197], v[4:7]
	v_mfma_f32_16x16x32_bf16 v[0:3], v[152:155], v[194:197], v[0:3]
	v_mfma_f32_16x16x32_bf16 v[52:55], v[148:151], v[164:167], v[52:55]
	v_mfma_f32_16x16x32_bf16 v[48:51], v[156:159], v[164:167], v[48:51]
	v_mfma_f32_16x16x32_bf16 v[36:39], v[148:151], v[182:185], v[36:39]
	v_mfma_f32_16x16x32_bf16 v[32:35], v[156:159], v[182:185], v[32:35]
	v_mfma_f32_16x16x32_bf16 v[20:23], v[148:151], v[190:193], v[20:23]
	v_mfma_f32_16x16x32_bf16 v[16:19], v[156:159], v[190:193], v[16:19]
	v_mfma_f32_16x16x32_bf16 v[4:7], v[148:151], v[198:201], v[4:7]
	v_mfma_f32_16x16x32_bf16 v[0:3], v[156:159], v[198:201], v[0:3]
	s_setprio 0
	s_barrier
	s_add_i32 s67, s67, 2
	s_addk_i32 s65, 0x100
	s_addk_i32 s66, 0x100
	s_cmp_ge_i32 s67, s47
	s_cbranch_scc0 .LBB0_1701
	s_branch .Lzp_after_1701

; #define PG8_BAR __builtin_amdgcn_s_barrier()
; template <class Epi, class Sched, bool ALIGN_EPI = false, bool SP2 = false, bool FP8 = false>
; __device__ __forceinline__ void gemm_phase(LAS unsigned char* lds, const Gemm g, const Sched& S, const Epi& E, int wbase) {
;     ...
;         if constexpr (ALIGN_EPI) { if (wr == 0) PG8_BAR; }
;         { int fr_ = fr, fq_ = fq; asm volatile("" : "+v"(fr_), "+v"(fq_));
;           if constexpr (Epi::HAS_PRE) E(acc, cur, wr, wc, fr_, fq_, pre_); else E(acc, cur, wr, wc, fr_, fq_); } S.done(cur);
.Lzp_after_1701:
	v_readlane_b32 s68, v255, 22
	v_readlane_b32 s69, v255, 23
	s_and_b64 vcc, exec, s[16:17]
	s_cbranch_vccnz .LBB0_1704
	s_branch .LBB0_1705

; #define PG8_STAGE(bufoff, rs_, soff_, voff) do { _Pragma("unroll") for (int _i = 0; _i < 2; ++_i) \
;         __builtin_amdgcn_raw_ptr_buffer_load_lds(rs_, (LAS void*)(lds + (bufoff) + ldsw + _i * 8192), 16, (int)(voff)[_i], (int)(soff_), 0, 0); } while (0)
; #define PG8_LDA(dst, b, h) do { _Pragma("unroll") for (int m = 0; m < 4; ++m) dst[m] = PG8_LD2(lds + PG8_SA(b, h) + aoff + m * 2048); } while (0)
; #define PG8_LDB(dst, b, h) do { _Pragma("unroll") for (int n = 0; n < 2; ++n) dst[n] = PG8_LD2(lds + PG8_SB(b, h) + boff + n * 2048); } while (0)
; #define PG8_WAIT_V(n) asm volatile("s_waitcnt vmcnt(" #n ")" ::: "memory")
; #define PG8_WAIT_L(n) asm volatile("s_waitcnt lgkmcnt(" #n ")" ::: "memory")
; #define PG8_BAR __builtin_amdgcn_s_barrier()
; #define PG8_SCHED __builtin_amdgcn_sched_barrier(0)
; template <class Epi, class Sched, bool ALIGN_EPI = false, bool SP2 = false, bool FP8 = false>
; __device__ __forceinline__ void gemm_phase(LAS unsigned char* lds, const Gemm g, const Sched& S, const Epi& E, int wbase) {
;     ...
;             const unsigned a2 = last ? nA : cA + (unsigned)(t + 2) * kstep, b2 = last ? nB : cB + (unsigned)(t + 2) * kstep; const rsrc_t rA2 = (Sched::TWO && last) ? rAn : rAc, rB2 = (Sched::TWO && last) ? rBn : rBc;
;             const unsigned a3 = a2 + kstep, b3 = b2 + kstep;
;             if (last && has_next) S.a_ready(nxt);
;             if constexpr (SP2) {
;             PG8_LDB(B0, 0, 0); PG8_LDB(B1, 0, 1); PG8_SCHED; PG8_LDA(At, 0, 0); PG8_STAGE(PG8_SA(1, 1), rAc, a1 + hstep, voffA);
;             PG8_WAIT_V(8); PG8_WAIT_L(0); PG8_BAR; PG8_MMA(0, 0, At, B0); PG8_MMA(0, 1, At, B1); PG8_BAR; PG8_SCHED;
;             PG8_LDA(At, 0, 1); PG8_STAGE(PG8_SB(0, 0), rB2, b2, voffB); PG8_STAGE(PG8_SB(0, 1), rB2, b2 + hstep, voffB); PG8_STAGE(PG8_SA(0, 0), rA2, a2, voffA);
;             PG8_WAIT_V(8); PG8_WAIT_L(0); PG8_BAR; PG8_MMA(1, 0, At, B0); PG8_MMA(1, 1, At, B1); PG8_BAR; PG8_SCHED;
.LBB0_1779:
	s_lshl_b32 s53, s52, 18
	s_andn2_b64 vcc, exec, s[14:15]
	s_lshl_b32 s56, s48, 18
	s_cbranch_vccnz .LBB0_1783
	s_and_b64 s[6:7], s[18:19], exec
	s_waitcnt vmcnt(37)
	s_waitcnt vmcnt(35)
	s_waitcnt vmcnt(31)
	s_waitcnt vmcnt(27)
	s_waitcnt vmcnt(23)
	s_waitcnt vmcnt(22)
	v_mov_b32_e32 v225, 1
	v_mov_b32_e32 v223, v233
	v_mov_b32_e32 v222, 0x358637bd
	s_cselect_b32 s59, s53, s55
	s_cselect_b32 s60, s56, s54
	s_add_i32 s61, s55, 0x80
	s_add_i32 s62, s54, 0x100
	s_mov_b32 s63, 0
	v_add_u32_e32 v140, 0x10000, v154
	v_add_u32_e32 v144, 0x14000, v154
	ds_read_b128 v[128:131], v140
	ds_read_b128 v[132:135], v140 offset:1024
	ds_read_b128 v[136:139], v140 offset:2048
	ds_read_b128 v[140:143], v140 offset:3072
	ds_read_b128 v[156:159], v144
	ds_read_b128 v[160:163], v144 offset:1024
	ds_read_b128 v[164:167], v144 offset:2048
	ds_read_b128 v[168:171], v144 offset:3072
	s_add_i32 s6, s61, 0x80
	s_cmp_eq_u32 s45, s63
	s_cselect_b32 s65, s59, s6
	s_cselect_b32 s55, s60, s62
	s_or_b32 s54, s65, 0x80
	s_add_i32 s6, s21, s61
	s_mov_b32 m0, s46
	ds_read_b128 v[172:175], v155
	ds_read_b128 v[176:179], v155 offset:1024
	ds_read_b128 v[180:183], v155 offset:2048
	ds_read_b128 v[184:187], v155 offset:3072
	ds_read_b128 v[194:197], v155 offset:4096
	ds_read_b128 v[198:201], v155 offset:5120
	ds_read_b128 v[202:205], v155 offset:6144
	ds_read_b128 v[206:209], v155 offset:7168
	buffer_load_dwordx4 v148, s[36:39], s6 offen lds
	s_mov_b32 m0, s47
	s_nop 0
	buffer_load_dwordx4 v150, s[36:39], s6 offen lds
	s_waitcnt vmcnt(8)
	s_waitcnt lgkmcnt(0)
	s_barrier
	s_setprio 1
	v_mfma_f32_16x16x128_f8f6f4 v[120:123], v[128:135], v[172:179], 0
	v_mfma_f32_16x16x128_f8f6f4 v[124:127], v[136:143], v[172:179], 0
	v_mfma_f32_16x16x128_f8f6f4 v[104:107], v[128:135], v[180:187], 0
	v_mfma_f32_16x16x128_f8f6f4 v[108:111], v[136:143], v[180:187], 0
	v_mfma_f32_16x16x128_f8f6f4 v[144:147], v[128:135], v[194:201], 0
	v_mfma_f32_16x16x128_f8f6f4 v[188:191], v[136:143], v[194:201], 0
	v_mfma_f32_16x16x128_f8f6f4 v[210:213], v[128:135], v[202:209], 0
	v_mfma_f32_16x16x128_f8f6f4 v[214:217], v[136:143], v[202:209], 0
	v_mfma_f32_16x16x128_f8f6f4 v[112:115], v[156:163], v[172:179], 0
	v_mfma_f32_16x16x128_f8f6f4 v[116:119], v[164:171], v[172:179], 0
	v_mfma_f32_16x16x128_f8f6f4 v[96:99], v[156:163], v[180:187], 0
	v_mfma_f32_16x16x128_f8f6f4 v[100:103], v[164:171], v[180:187], 0
	v_mfma_f32_16x16x128_f8f6f4 v[172:175], v[156:163], v[194:201], 0
	v_mfma_f32_16x16x128_f8f6f4 v[176:179], v[164:171], v[194:201], 0
	v_mfma_f32_16x16x128_f8f6f4 v[180:183], v[156:163], v[202:209], 0
	v_mfma_f32_16x16x128_f8f6f4 v[184:187], v[164:171], v[202:209], 0
	s_setprio 0
	s_barrier
	s_mov_b32 m0, s23
	s_mov_b32 s6, s38
	s_mov_b32 s7, s39
	s_nop 0
	ds_read_b128 v[64:67], v155 offset:16384
	ds_read_b128 v[68:71], v155 offset:17408
	ds_read_b128 v[72:75], v155 offset:18432
	ds_read_b128 v[76:79], v155 offset:19456
	ds_read_b128 v[80:83], v155 offset:20480
	ds_read_b128 v[84:87], v155 offset:21504
	ds_read_b128 v[88:91], v155 offset:22528
	ds_read_b128 v[92:95], v155 offset:23552
	buffer_load_dwordx4 v149, s[4:7], s55 offen lds
	s_mov_b32 m0, s24
	s_add_i32 s66, s55, s21
	buffer_load_dwordx4 v151, s[4:7], s55 offen lds
	s_mov_b32 m0, s25
	s_nop 0
	buffer_load_dwordx4 v149, s[4:7], s66 offen lds
	s_mov_b32 m0, s26
	s_nop 0
	buffer_load_dwordx4 v151, s[4:7], s66 offen lds
	s_mov_b32 m0, s22
	s_nop 0
	buffer_load_dwordx4 v148, s[36:39], s65 offen lds
	s_mov_b32 m0, s27
	s_nop 0
	buffer_load_dwordx4 v150, s[36:39], s65 offen lds
	s_waitcnt vmcnt(8)
	s_waitcnt lgkmcnt(0)
	s_barrier
	s_setprio 1
	v_mfma_f32_16x16x128_f8f6f4 v[56:59], v[128:135], v[64:71], 0
	v_mfma_f32_16x16x128_f8f6f4 v[60:63], v[136:143], v[64:71], 0
	v_mfma_f32_16x16x128_f8f6f4 v[8:11], v[128:135], v[88:95], 0
	v_mfma_f32_16x16x128_f8f6f4 v[192:195], v[128:135], v[72:79], 0
	v_mfma_f32_16x16x128_f8f6f4 v[196:199], v[136:143], v[72:79], 0
	v_mfma_f32_16x16x128_f8f6f4 v[200:203], v[128:135], v[80:87], 0
	v_mfma_f32_16x16x128_f8f6f4 v[204:207], v[136:143], v[80:87], 0
	v_mfma_f32_16x16x128_f8f6f4 v[218:221], v[136:143], v[88:95], 0
	v_mfma_f32_16x16x128_f8f6f4 v[52:55], v[164:171], v[64:71], 0
	v_mfma_f32_16x16x128_f8f6f4 v[226:229], v[156:163], v[64:71], 0
	v_mfma_f32_16x16x128_f8f6f4 v[230:233], v[156:163], v[72:79], 0
	v_mfma_f32_16x16x128_f8f6f4 v[234:237], v[164:171], v[72:79], 0
	v_mfma_f32_16x16x128_f8f6f4 v[238:241], v[156:163], v[80:87], 0
	v_mfma_f32_16x16x128_f8f6f4 v[242:245], v[164:171], v[80:87], 0
	v_mfma_f32_16x16x128_f8f6f4 v[246:249], v[156:163], v[88:95], 0
	v_mfma_f32_16x16x128_f8f6f4 v[250:253], v[164:171], v[88:95], 0
	s_setprio 0
	s_barrier
; #define PG8_STAGE(bufoff, rs_, soff_, voff) do { _Pragma("unroll") for (int _i = 0; _i < 2; ++_i) \
;         __builtin_amdgcn_raw_ptr_buffer_load_lds(rs_, (LAS void*)(lds + (bufoff) + ldsw + _i * 8192), 16, (int)(voff)[_i], (int)(soff_), 0, 0); } while (0)
; #define PG8_LDA(dst, b, h) do { _Pragma("unroll") for (int m = 0; m < 4; ++m) dst[m] = PG8_LD2(lds + PG8_SA(b, h) + aoff + m * 2048); } while (0)
; #define PG8_LDB(dst, b, h) do { _Pragma("unroll") for (int n = 0; n < 2; ++n) dst[n] = PG8_LD2(lds + PG8_SB(b, h) + boff + n * 2048); } while (0)
; #define PG8_WAIT_V(n) asm volatile("s_waitcnt vmcnt(" #n ")" ::: "memory")
; #define PG8_WAIT_L(n) asm volatile("s_waitcnt lgkmcnt(" #n ")" ::: "memory")
; #define PG8_BAR __builtin_amdgcn_s_barrier()
; #define PG8_SCHED __builtin_amdgcn_sched_barrier(0)
; template <class Epi, class Sched, bool ALIGN_EPI = false, bool SP2 = false, bool FP8 = false>
; __device__ __forceinline__ void gemm_phase(LAS unsigned char* lds, const Gemm g, const Sched& S, const Epi& E, int wbase) {
;     ...
;             PG8_LDB(B0, 1, 0); PG8_LDB(B1, 1, 1); PG8_SCHED; PG8_LDA(At, 1, 0); PG8_STAGE(PG8_SA(0, 1), rA2, a2 + hstep, voffA);
;             PG8_WAIT_V(8); PG8_WAIT_L(0); PG8_BAR; PG8_MMA(0, 0, At, B0); PG8_MMA(0, 1, At, B1); PG8_BAR; PG8_SCHED;
;             PG8_LDA(At, 1, 1); PG8_STAGE(PG8_SB(1, 0), rB2, b3, voffB); PG8_STAGE(PG8_SB(1, 1), rB2, b3 + hstep, voffB); PG8_STAGE(PG8_SA(1, 0), rA2, a3, voffA);
;             PG8_WAIT_V(8); PG8_WAIT_L(0); PG8_BAR; PG8_MMA(1, 0, At, B0); PG8_MMA(1, 1, At, B1); PG8_BAR; PG8_SCHED;
	s_nop 1
	v_add_u32_e32 v16, 0x18000, v154
	v_add_u32_e32 v20, 0x1c000, v154
	s_nop 0
	ds_read_b128 v[0:3], v16
	ds_read_b128 v[4:7], v16 offset:1024
	ds_read_b128 v[12:15], v16 offset:2048
	ds_read_b128 v[16:19], v16 offset:3072
	ds_read_b128 v[128:131], v20
	ds_read_b128 v[132:135], v20 offset:1024
	ds_read_b128 v[136:139], v20 offset:2048
	ds_read_b128 v[140:143], v20 offset:3072
	s_add_i32 s65, s65, s21
	s_mov_b32 m0, s28
	ds_read_b128 v[20:23], v155 offset:32768
	ds_read_b128 v[24:27], v155 offset:33792
	ds_read_b128 v[28:31], v155 offset:34816
	ds_read_b128 v[32:35], v155 offset:35840
	ds_read_b128 v[36:39], v155 offset:36864
	ds_read_b128 v[40:43], v155 offset:37888
	ds_read_b128 v[44:47], v155 offset:38912
	ds_read_b128 v[48:51], v155 offset:39936
	buffer_load_dwordx4 v148, s[36:39], s65 offen lds
	s_mov_b32 m0, s29
	s_nop 0
	buffer_load_dwordx4 v150, s[36:39], s65 offen lds
	s_waitcnt vmcnt(8)
	s_waitcnt lgkmcnt(0)
	s_barrier
	s_setprio 1
	v_mfma_f32_16x16x128_f8f6f4 v[120:123], v[0:7], v[20:27], v[120:123]
	v_mfma_f32_16x16x128_f8f6f4 v[124:127], v[12:19], v[20:27], v[124:127]
	v_mfma_f32_16x16x128_f8f6f4 v[104:107], v[0:7], v[28:35], v[104:107]
	v_mfma_f32_16x16x128_f8f6f4 v[108:111], v[12:19], v[28:35], v[108:111]
	v_mfma_f32_16x16x128_f8f6f4 v[88:91], v[0:7], v[36:43], v[144:147]
	v_mfma_f32_16x16x128_f8f6f4 v[92:95], v[12:19], v[36:43], v[188:191]
	v_mfma_f32_16x16x128_f8f6f4 v[72:75], v[0:7], v[44:51], v[210:213]
	v_mfma_f32_16x16x128_f8f6f4 v[76:79], v[12:19], v[44:51], v[214:217]
	v_mfma_f32_16x16x128_f8f6f4 v[112:115], v[128:135], v[20:27], v[112:115]
	v_mfma_f32_16x16x128_f8f6f4 v[116:119], v[136:143], v[20:27], v[116:119]
	v_mfma_f32_16x16x128_f8f6f4 v[96:99], v[128:135], v[28:35], v[96:99]
	v_mfma_f32_16x16x128_f8f6f4 v[100:103], v[136:143], v[28:35], v[100:103]
	v_mfma_f32_16x16x128_f8f6f4 v[80:83], v[128:135], v[36:43], v[172:175]
	v_mfma_f32_16x16x128_f8f6f4 v[84:87], v[136:143], v[36:43], v[176:179]
	v_mfma_f32_16x16x128_f8f6f4 v[64:67], v[128:135], v[44:51], v[180:183]
	v_mfma_f32_16x16x128_f8f6f4 v[68:71], v[136:143], v[44:51], v[184:187]
	s_setprio 0
	s_barrier
	s_mov_b32 m0, s30
	s_bitset1_b32 s55, 7
	ds_read_b128 v[32:35], v155 offset:49152
	ds_read_b128 v[36:39], v155 offset:50176
	ds_read_b128 v[156:159], v155 offset:51200
	ds_read_b128 v[160:163], v155 offset:52224
	ds_read_b128 v[164:167], v155 offset:53248
	ds_read_b128 v[168:171], v155 offset:54272
	ds_read_b128 v[172:175], v155 offset:55296
	ds_read_b128 v[176:179], v155 offset:56320
	buffer_load_dwordx4 v149, s[4:7], s55 offen lds
	s_mov_b32 m0, s31
	s_nop 0
	buffer_load_dwordx4 v151, s[4:7], s55 offen lds
	s_add_i32 s55, s55, s21
	s_mov_b32 m0, s35
	s_nop 0
	buffer_load_dwordx4 v149, s[4:7], s55 offen lds
	s_mov_b32 m0, s41
	s_nop 0
	buffer_load_dwordx4 v151, s[4:7], s55 offen lds
	s_mov_b32 m0, s33
	s_nop 0
	buffer_load_dwordx4 v148, s[36:39], s54 offen lds
	s_mov_b32 m0, s34
	s_nop 0
	buffer_load_dwordx4 v150, s[36:39], s54 offen lds
	s_waitcnt vmcnt(8)
	s_waitcnt lgkmcnt(0)
	s_barrier
	s_setprio 1
	v_mfma_f32_16x16x128_f8f6f4 v[56:59], v[0:7], v[32:39], v[56:59]
	v_mfma_f32_16x16x128_f8f6f4 v[60:63], v[12:19], v[32:39], v[60:63]
	v_mfma_f32_16x16x128_f8f6f4 v[40:43], v[0:7], v[156:163], v[192:195]
	v_mfma_f32_16x16x128_f8f6f4 v[44:47], v[12:19], v[156:163], v[196:199]
	v_mfma_f32_16x16x128_f8f6f4 v[24:27], v[0:7], v[164:171], v[200:203]
	v_mfma_f32_16x16x128_f8f6f4 v[28:31], v[12:19], v[164:171], v[204:207]
	v_mfma_f32_16x16x128_f8f6f4 v[8:11], v[0:7], v[172:179], v[8:11]
	v_mfma_f32_16x16x128_f8f6f4 v[12:15], v[12:19], v[172:179], v[218:221]
	v_mfma_f32_16x16x128_f8f6f4 v[48:51], v[128:135], v[32:39], v[226:229]
	v_mfma_f32_16x16x128_f8f6f4 v[52:55], v[136:143], v[32:39], v[52:55]
	v_mfma_f32_16x16x128_f8f6f4 v[32:35], v[128:135], v[156:163], v[230:233]
	v_mfma_f32_16x16x128_f8f6f4 v[36:39], v[136:143], v[156:163], v[234:237]
	v_mfma_f32_16x16x128_f8f6f4 v[16:19], v[128:135], v[164:171], v[238:241]
	v_mfma_f32_16x16x128_f8f6f4 v[20:23], v[136:143], v[164:171], v[242:245]
	v_mfma_f32_16x16x128_f8f6f4 v[4:7], v[128:135], v[172:179], v[246:249]
	v_mfma_f32_16x16x128_f8f6f4 v[0:3], v[136:143], v[172:179], v[250:253]
	s_setprio 0
	s_barrier
	s_add_i32 s63, s63, 2
	s_addk_i32 s61, 0x100
	s_addk_i32 s62, 0x100
	s_cmp_ge_i32 s63, s43
	s_cbranch_scc0 .LBB0_1781
	s_branch .Lzp_after_1781

; #define PG8_BAR __builtin_amdgcn_s_barrier()
; template <class Epi, class Sched, bool ALIGN_EPI = false, bool SP2 = false, bool FP8 = false>
; __device__ __forceinline__ void gemm_phase(LAS unsigned char* lds, const Gemm g, const Sched& S, const Epi& E, int wbase) {
;     ...
;         if constexpr (ALIGN_EPI) { if (wr == 0) PG8_BAR; }
;         { int fr_ = fr, fq_ = fq; asm volatile("" : "+v"(fr_), "+v"(fq_));
;           if constexpr (Epi::HAS_PRE) E(acc, cur, wr, wc, fr_, fq_, pre_); else E(acc, cur, wr, wc, fr_, fq_); } S.done(cur);
.Lzp_after_1781:
	v_mov_b32_e32 v230, v222
	v_mov_b32_e32 v233, v223
	v_mov_b32_e32 v231, v225
	v_mov_b32_e32 v234, 0xff61b1e6
	s_and_b64 vcc, exec, s[16:17]
	s_cbranch_vccnz .LBB0_1784
	s_branch .LBB0_1785

; #define PG8_STAGE(bufoff, rs_, soff_, voff) do { _Pragma("unroll") for (int _i = 0; _i < 2; ++_i) \
;         __builtin_amdgcn_raw_ptr_buffer_load_lds(rs_, (LAS void*)(lds + (bufoff) + ldsw + _i * 8192), 16, (int)(voff)[_i], (int)(soff_), 0, 0); } while (0)
; #define PG8_LDA(dst, b, h) do { _Pragma("unroll") for (int m = 0; m < 4; ++m) dst[m] = PG8_LD2(lds + PG8_SA(b, h) + aoff + m * 2048); } while (0)
; #define PG8_LDB(dst, b, h) do { _Pragma("unroll") for (int n = 0; n < 2; ++n) dst[n] = PG8_LD2(lds + PG8_SB(b, h) + boff + n * 2048); } while (0)
; #define PG8_WAIT_V(n) asm volatile("s_waitcnt vmcnt(" #n ")" ::: "memory")
; #define PG8_WAIT_L(n) asm volatile("s_waitcnt lgkmcnt(" #n ")" ::: "memory")
; #define PG8_BAR __builtin_amdgcn_s_barrier()
; #define PG8_SCHED __builtin_amdgcn_sched_barrier(0)
; template <class Epi, class Sched, bool ALIGN_EPI = false, bool SP2 = false, bool FP8 = false>
; __device__ __forceinline__ void gemm_phase(LAS unsigned char* lds, const Gemm g, const Sched& S, const Epi& E, int wbase) {
;     ...
;             const unsigned a2 = last ? nA : cA + (unsigned)(t + 2) * kstep, b2 = last ? nB : cB + (unsigned)(t + 2) * kstep; const rsrc_t rA2 = (Sched::TWO && last) ? rAn : rAc, rB2 = (Sched::TWO && last) ? rBn : rBc;
;             const unsigned a3 = a2 + kstep, b3 = b2 + kstep;
;             if (last && has_next) S.a_ready(nxt);
;             if constexpr (SP2) {
;             PG8_LDB(B0, 0, 0); PG8_LDB(B1, 0, 1); PG8_SCHED; PG8_LDA(At, 0, 0); PG8_STAGE(PG8_SA(1, 1), rAc, a1 + hstep, voffA);
;             PG8_WAIT_V(8); PG8_WAIT_L(0); PG8_BAR; PG8_MMA(0, 0, At, B0); PG8_MMA(0, 1, At, B1); PG8_BAR; PG8_SCHED;
;             PG8_LDA(At, 0, 1); PG8_STAGE(PG8_SB(0, 0), rB2, b2, voffB); PG8_STAGE(PG8_SB(0, 1), rB2, b2 + hstep, voffB); PG8_STAGE(PG8_SA(0, 0), rA2, a2, voffA);
;             PG8_WAIT_V(8); PG8_WAIT_L(0); PG8_BAR; PG8_MMA(1, 0, At, B0); PG8_MMA(1, 1, At, B1); PG8_BAR; PG8_SCHED;
.LBB0_1852:
	s_mul_i32 s61, s60, 0xe0000
	s_andn2_b64 vcc, exec, s[14:15]
	s_mul_i32 s62, s59, 0xe0000
	s_cbranch_vccnz .LBB0_1856
	s_and_b64 s[6:7], s[18:19], exec
	s_waitcnt vmcnt(37)
	s_waitcnt vmcnt(36)
	s_waitcnt vmcnt(35)
	s_waitcnt vmcnt(32)
	s_waitcnt vmcnt(31)
	s_waitcnt vmcnt(28)
	s_waitcnt vmcnt(27)
	s_waitcnt vmcnt(24)
	s_waitcnt vmcnt(23)
	s_waitcnt vmcnt(22)
	v_mov_b32_e32 v223, 0xff61b1e6
	v_mov_b32_e32 v222, 1
	v_mov_b32_e32 v169, v233
	v_mov_b32_e32 v168, 0x358637bd
	s_cselect_b32 s21, s61, s55
	s_cselect_b32 s63, s62, s54
	s_add_i32 s65, s55, 0x80
	s_add_i32 s66, s54, 0x100
	s_mov_b32 s67, 0
	v_add_u32_e32 v140, 0x10000, v176
	v_add_u32_e32 v156, 0x14000, v176
	ds_read_b128 v[128:131], v140
	ds_read_b128 v[132:135], v140 offset:1024
	ds_read_b128 v[136:139], v140 offset:2048
	ds_read_b128 v[140:143], v140 offset:3072
	ds_read_b128 v[144:147], v156
	ds_read_b128 v[148:151], v156 offset:1024
	ds_read_b128 v[152:155], v156 offset:2048
	ds_read_b128 v[156:159], v156 offset:3072
	s_add_i32 s6, s65, 0x80
	s_cmp_eq_u32 s52, s67
	s_cselect_b32 s68, s21, s6
	s_cselect_b32 s55, s63, s66
	s_or_b32 s54, s68, 0x80
	s_add_i32 s6, s24, s65
	s_mov_b32 m0, s53
	ds_read_b128 v[160:163], v177
	ds_read_b128 v[164:167], v177 offset:1024
	ds_read_b128 v[178:181], v177 offset:2048
	ds_read_b128 v[182:185], v177 offset:3072
	ds_read_b128 v[194:197], v177 offset:4096
	ds_read_b128 v[198:201], v177 offset:5120
	ds_read_b128 v[202:205], v177 offset:6144
	ds_read_b128 v[206:209], v177 offset:7168
	buffer_load_dwordx4 v170, s[36:39], s6 offen lds
	s_mov_b32 m0, s56
	s_nop 0
	buffer_load_dwordx4 v172, s[36:39], s6 offen lds
	s_waitcnt vmcnt(8)
	s_waitcnt lgkmcnt(0)
	s_barrier
	s_setprio 1
	v_mfma_f32_16x16x128_f8f6f4 v[124:127], v[128:135], v[160:167], 0
	v_mfma_f32_16x16x128_f8f6f4 v[120:123], v[136:143], v[160:167], 0
	v_mfma_f32_16x16x128_f8f6f4 v[108:111], v[128:135], v[178:185], 0
	v_mfma_f32_16x16x128_f8f6f4 v[104:107], v[136:143], v[178:185], 0
	v_mfma_f32_16x16x128_f8f6f4 v[186:189], v[128:135], v[194:201], 0
	v_mfma_f32_16x16x128_f8f6f4 v[190:193], v[136:143], v[194:201], 0
	v_mfma_f32_16x16x128_f8f6f4 v[210:213], v[128:135], v[202:209], 0
	v_mfma_f32_16x16x128_f8f6f4 v[214:217], v[136:143], v[202:209], 0
	v_mfma_f32_16x16x128_f8f6f4 v[116:119], v[144:151], v[160:167], 0
	v_mfma_f32_16x16x128_f8f6f4 v[112:115], v[152:159], v[160:167], 0
	v_mfma_f32_16x16x128_f8f6f4 v[100:103], v[144:151], v[178:185], 0
	v_mfma_f32_16x16x128_f8f6f4 v[96:99], v[152:159], v[178:185], 0
	v_mfma_f32_16x16x128_f8f6f4 v[160:163], v[144:151], v[194:201], 0
	v_mfma_f32_16x16x128_f8f6f4 v[164:167], v[152:159], v[194:201], 0
	v_mfma_f32_16x16x128_f8f6f4 v[178:181], v[144:151], v[202:209], 0
	v_mfma_f32_16x16x128_f8f6f4 v[182:185], v[152:159], v[202:209], 0
	s_setprio 0
	s_barrier
	s_mov_b32 m0, s26
	s_mov_b32 s6, s38
	s_mov_b32 s7, s39
	s_nop 1
	ds_read_b128 v[64:67], v177 offset:16384
	ds_read_b128 v[68:71], v177 offset:17408
	ds_read_b128 v[72:75], v177 offset:18432
	ds_read_b128 v[76:79], v177 offset:19456
	ds_read_b128 v[80:83], v177 offset:20480
	ds_read_b128 v[84:87], v177 offset:21504
	ds_read_b128 v[88:91], v177 offset:22528
	ds_read_b128 v[92:95], v177 offset:23552
	buffer_load_dwordx4 v171, s[4:7], s55 offen lds
	s_mov_b32 m0, s27
	s_add_i32 s69, s55, s24
	buffer_load_dwordx4 v173, s[4:7], s55 offen lds
	s_mov_b32 m0, s28
	s_nop 0
	buffer_load_dwordx4 v171, s[4:7], s69 offen lds
	s_mov_b32 m0, s29
	s_nop 0
	buffer_load_dwordx4 v173, s[4:7], s69 offen lds
	s_mov_b32 m0, s25
	s_nop 0
	buffer_load_dwordx4 v170, s[36:39], s68 offen lds
	s_mov_b32 m0, s30
	s_nop 0
	buffer_load_dwordx4 v172, s[36:39], s68 offen lds
	s_waitcnt vmcnt(8)
	s_waitcnt lgkmcnt(0)
	s_barrier
	s_setprio 1
	v_mfma_f32_16x16x128_f8f6f4 v[60:63], v[128:135], v[64:71], 0
	v_mfma_f32_16x16x128_f8f6f4 v[56:59], v[136:143], v[64:71], 0
	v_mfma_f32_16x16x128_f8f6f4 v[194:197], v[128:135], v[72:79], 0
	v_mfma_f32_16x16x128_f8f6f4 v[198:201], v[136:143], v[72:79], 0
	v_mfma_f32_16x16x128_f8f6f4 v[202:205], v[128:135], v[80:87], 0
	v_mfma_f32_16x16x128_f8f6f4 v[206:209], v[136:143], v[80:87], 0
	v_mfma_f32_16x16x128_f8f6f4 v[218:221], v[128:135], v[88:95], 0
	v_mfma_f32_16x16x128_f8f6f4 v[226:229], v[136:143], v[88:95], 0
	v_mfma_f32_16x16x128_f8f6f4 v[52:55], v[144:151], v[64:71], 0
	v_mfma_f32_16x16x128_f8f6f4 v[48:51], v[152:159], v[64:71], 0
	v_mfma_f32_16x16x128_f8f6f4 v[230:233], v[144:151], v[72:79], 0
	v_mfma_f32_16x16x128_f8f6f4 v[234:237], v[152:159], v[72:79], 0
	v_mfma_f32_16x16x128_f8f6f4 v[238:241], v[144:151], v[80:87], 0
	v_mfma_f32_16x16x128_f8f6f4 v[242:245], v[152:159], v[80:87], 0
	v_mfma_f32_16x16x128_f8f6f4 v[246:249], v[144:151], v[88:95], 0
	v_mfma_f32_16x16x128_f8f6f4 v[250:253], v[152:159], v[88:95], 0
	s_setprio 0
	s_barrier
; #define PG8_STAGE(bufoff, rs_, soff_, voff) do { _Pragma("unroll") for (int _i = 0; _i < 2; ++_i) \
;         __builtin_amdgcn_raw_ptr_buffer_load_lds(rs_, (LAS void*)(lds + (bufoff) + ldsw + _i * 8192), 16, (int)(voff)[_i], (int)(soff_), 0, 0); } while (0)
; #define PG8_LDA(dst, b, h) do { _Pragma("unroll") for (int m = 0; m < 4; ++m) dst[m] = PG8_LD2(lds + PG8_SA(b, h) + aoff + m * 2048); } while (0)
; #define PG8_LDB(dst, b, h) do { _Pragma("unroll") for (int n = 0; n < 2; ++n) dst[n] = PG8_LD2(lds + PG8_SB(b, h) + boff + n * 2048); } while (0)
; #define PG8_WAIT_V(n) asm volatile("s_waitcnt vmcnt(" #n ")" ::: "memory")
; #define PG8_WAIT_L(n) asm volatile("s_waitcnt lgkmcnt(" #n ")" ::: "memory")
; #define PG8_BAR __builtin_amdgcn_s_barrier()
; #define PG8_SCHED __builtin_amdgcn_sched_barrier(0)
; template <class Epi, class Sched, bool ALIGN_EPI = false, bool SP2 = false, bool FP8 = false>
; __device__ __forceinline__ void gemm_phase(LAS unsigned char* lds, const Gemm g, const Sched& S, const Epi& E, int wbase) {
;     ...
;             PG8_LDB(B0, 1, 0); PG8_LDB(B1, 1, 1); PG8_SCHED; PG8_LDA(At, 1, 0); PG8_STAGE(PG8_SA(0, 1), rA2, a2 + hstep, voffA);
;             PG8_WAIT_V(8); PG8_WAIT_L(0); PG8_BAR; PG8_MMA(0, 0, At, B0); PG8_MMA(0, 1, At, B1); PG8_BAR; PG8_SCHED;
;             PG8_LDA(At, 1, 1); PG8_STAGE(PG8_SB(1, 0), rB2, b3, voffB); PG8_STAGE(PG8_SB(1, 1), rB2, b3 + hstep, voffB); PG8_STAGE(PG8_SA(1, 0), rA2, a3, voffA);
;             PG8_WAIT_V(8); PG8_WAIT_L(0); PG8_BAR; PG8_MMA(1, 0, At, B0); PG8_MMA(1, 1, At, B1); PG8_BAR; PG8_SCHED;
	v_add_u32_e32 v8, 0x18000, v176
	s_nop 3
	ds_read_b128 v[0:3], v8
	ds_read_b128 v[4:7], v8 offset:1024
	ds_read_b128 v[16:19], v8 offset:2048
	ds_read_b128 v[20:23], v8 offset:3072
	v_add_u32_e32 v8, 0x1c000, v176
	ds_read_b128 v[128:131], v8
	ds_read_b128 v[132:135], v8 offset:1024
	ds_read_b128 v[136:139], v8 offset:2048
	ds_read_b128 v[140:143], v8 offset:3072
	s_add_i32 s68, s68, s24
	s_mov_b32 m0, s31
	ds_read_b128 v[8:11], v177 offset:32768
	ds_read_b128 v[12:15], v177 offset:33792
	ds_read_b128 v[24:27], v177 offset:34816
	ds_read_b128 v[28:31], v177 offset:35840
	ds_read_b128 v[32:35], v177 offset:36864
	ds_read_b128 v[36:39], v177 offset:37888
	ds_read_b128 v[40:43], v177 offset:38912
	ds_read_b128 v[44:47], v177 offset:39936
	buffer_load_dwordx4 v170, s[36:39], s68 offen lds
	s_mov_b32 m0, s33
	s_nop 0
	buffer_load_dwordx4 v172, s[36:39], s68 offen lds
	s_waitcnt vmcnt(8)
	s_waitcnt lgkmcnt(0)
	s_barrier
	s_setprio 1
	v_mfma_f32_16x16x128_f8f6f4 v[124:127], v[0:7], v[8:15], v[124:127]
	v_mfma_f32_16x16x128_f8f6f4 v[120:123], v[16:23], v[8:15], v[120:123]
	v_mfma_f32_16x16x128_f8f6f4 v[108:111], v[0:7], v[24:31], v[108:111]
	v_mfma_f32_16x16x128_f8f6f4 v[104:107], v[16:23], v[24:31], v[104:107]
	v_mfma_f32_16x16x128_f8f6f4 v[92:95], v[0:7], v[32:39], v[186:189]
	v_mfma_f32_16x16x128_f8f6f4 v[88:91], v[16:23], v[32:39], v[190:193]
	v_mfma_f32_16x16x128_f8f6f4 v[76:79], v[0:7], v[40:47], v[210:213]
	v_mfma_f32_16x16x128_f8f6f4 v[72:75], v[16:23], v[40:47], v[214:217]
	v_mfma_f32_16x16x128_f8f6f4 v[116:119], v[128:135], v[8:15], v[116:119]
	v_mfma_f32_16x16x128_f8f6f4 v[112:115], v[136:143], v[8:15], v[112:115]
	v_mfma_f32_16x16x128_f8f6f4 v[100:103], v[128:135], v[24:31], v[100:103]
	v_mfma_f32_16x16x128_f8f6f4 v[96:99], v[136:143], v[24:31], v[96:99]
	v_mfma_f32_16x16x128_f8f6f4 v[84:87], v[128:135], v[32:39], v[160:163]
	v_mfma_f32_16x16x128_f8f6f4 v[80:83], v[136:143], v[32:39], v[164:167]
	v_mfma_f32_16x16x128_f8f6f4 v[68:71], v[128:135], v[40:47], v[178:181]
	v_mfma_f32_16x16x128_f8f6f4 v[64:67], v[136:143], v[40:47], v[182:185]
	s_setprio 0
	s_barrier
	s_mov_b32 m0, s34
	s_bitset1_b32 s55, 7
	ds_read_b128 v[32:35], v177 offset:49152
	ds_read_b128 v[36:39], v177 offset:50176
	ds_read_b128 v[144:147], v177 offset:51200
	ds_read_b128 v[148:151], v177 offset:52224
	ds_read_b128 v[152:155], v177 offset:53248
	ds_read_b128 v[156:159], v177 offset:54272
	ds_read_b128 v[160:163], v177 offset:55296
	ds_read_b128 v[164:167], v177 offset:56320
	buffer_load_dwordx4 v171, s[4:7], s55 offen lds
	s_mov_b32 m0, s35
	s_nop 0
	buffer_load_dwordx4 v173, s[4:7], s55 offen lds
	s_add_i32 s55, s55, s24
	s_mov_b32 m0, s43
	s_nop 0
	buffer_load_dwordx4 v171, s[4:7], s55 offen lds
	s_mov_b32 m0, s44
	s_nop 0
	buffer_load_dwordx4 v173, s[4:7], s55 offen lds
	s_mov_b32 m0, s41
	s_nop 0
	buffer_load_dwordx4 v170, s[36:39], s54 offen lds
	s_mov_b32 m0, s42
	s_nop 0
	buffer_load_dwordx4 v172, s[36:39], s54 offen lds
	s_waitcnt vmcnt(8)
	s_waitcnt lgkmcnt(0)
	s_barrier
	s_setprio 1
	v_mfma_f32_16x16x128_f8f6f4 v[60:63], v[0:7], v[32:39], v[60:63]
	v_mfma_f32_16x16x128_f8f6f4 v[56:59], v[16:23], v[32:39], v[56:59]
	v_mfma_f32_16x16x128_f8f6f4 v[44:47], v[0:7], v[144:151], v[194:197]
	v_mfma_f32_16x16x128_f8f6f4 v[40:43], v[16:23], v[144:151], v[198:201]
	v_mfma_f32_16x16x128_f8f6f4 v[28:31], v[0:7], v[152:159], v[202:205]
	v_mfma_f32_16x16x128_f8f6f4 v[24:27], v[16:23], v[152:159], v[206:209]
	v_mfma_f32_16x16x128_f8f6f4 v[12:15], v[0:7], v[160:167], v[218:221]
	v_mfma_f32_16x16x128_f8f6f4 v[8:11], v[16:23], v[160:167], v[226:229]
	v_mfma_f32_16x16x128_f8f6f4 v[52:55], v[128:135], v[32:39], v[52:55]
	v_mfma_f32_16x16x128_f8f6f4 v[48:51], v[136:143], v[32:39], v[48:51]
	v_mfma_f32_16x16x128_f8f6f4 v[36:39], v[128:135], v[144:151], v[230:233]
	v_mfma_f32_16x16x128_f8f6f4 v[32:35], v[136:143], v[144:151], v[234:237]
	v_mfma_f32_16x16x128_f8f6f4 v[20:23], v[128:135], v[152:159], v[238:241]
	v_mfma_f32_16x16x128_f8f6f4 v[16:19], v[136:143], v[152:159], v[242:245]
	v_mfma_f32_16x16x128_f8f6f4 v[4:7], v[128:135], v[160:167], v[246:249]
	v_mfma_f32_16x16x128_f8f6f4 v[0:3], v[136:143], v[160:167], v[250:253]
	s_setprio 0
	s_barrier
	s_add_i32 s67, s67, 2
	s_addk_i32 s65, 0x100
	s_addk_i32 s66, 0x100
	s_cmp_ge_i32 s67, s47
	s_cbranch_scc0 .LBB0_1854
	s_branch .Lzp_after_1854

; #define PG8_BAR __builtin_amdgcn_s_barrier()
; template <class Epi, class Sched, bool ALIGN_EPI = false, bool SP2 = false, bool FP8 = false>
; __device__ __forceinline__ void gemm_phase(LAS unsigned char* lds, const Gemm g, const Sched& S, const Epi& E, int wbase) {
;     ...
;         if constexpr (ALIGN_EPI) { if (wr == 0) PG8_BAR; }
;         { int fr_ = fr, fq_ = fq; asm volatile("" : "+v"(fr_), "+v"(fq_));
;           if constexpr (Epi::HAS_PRE) E(acc, cur, wr, wc, fr_, fq_, pre_); else E(acc, cur, wr, wc, fr_, fq_); } S.done(cur);
.Lzp_after_1854:
	v_readlane_b32 s68, v255, 22
	v_readlane_b32 s69, v255, 23
	v_mov_b32_e32 v230, v168
	v_mov_b32_e32 v233, v169
	v_mov_b32_e32 v231, v222
	v_mov_b32_e32 v234, v223
	s_and_b64 vcc, exec, s[16:17]
	s_cbranch_vccnz .LBB0_1857
	s_branch .LBB0_1858

; #define PG8_STAGE(bufoff, rs_, soff_, voff) do { _Pragma("unroll") for (int _i = 0; _i < 2; ++_i) \
;         __builtin_amdgcn_raw_ptr_buffer_load_lds(rs_, (LAS void*)(lds + (bufoff) + ldsw + _i * 8192), 16, (int)(voff)[_i], (int)(soff_), 0, 0); } while (0)
; #define PG8_LDA(dst, b, h) do { _Pragma("unroll") for (int m = 0; m < 4; ++m) dst[m] = PG8_LD2(lds + PG8_SA(b, h) + aoff + m * 2048); } while (0)
; #define PG8_LDB(dst, b, h) do { _Pragma("unroll") for (int n = 0; n < 2; ++n) dst[n] = PG8_LD2(lds + PG8_SB(b, h) + boff + n * 2048); } while (0)
; #define PG8_WAIT_V(n) asm volatile("s_waitcnt vmcnt(" #n ")" ::: "memory")
; #define PG8_WAIT_L(n) asm volatile("s_waitcnt lgkmcnt(" #n ")" ::: "memory")
; #define PG8_BAR __builtin_amdgcn_s_barrier()
; #define PG8_SCHED __builtin_amdgcn_sched_barrier(0)
; template <class Epi, class Sched, bool ALIGN_EPI = false, bool SP2 = false, bool FP8 = false>
; __device__ __forceinline__ void gemm_phase(LAS unsigned char* lds, const Gemm g, const Sched& S, const Epi& E, int wbase) {
;     ...
;             const unsigned a2 = last ? nA : cA + (unsigned)(t + 2) * kstep, b2 = last ? nB : cB + (unsigned)(t + 2) * kstep; const rsrc_t rA2 = (Sched::TWO && last) ? rAn : rAc, rB2 = (Sched::TWO && last) ? rBn : rBc;
;             const unsigned a3 = a2 + kstep, b3 = b2 + kstep;
;             if (last && has_next) S.a_ready(nxt);
;             if constexpr (SP2) {
;             PG8_LDB(B0, 0, 0); PG8_LDB(B1, 0, 1); PG8_SCHED; PG8_LDA(At, 0, 0); PG8_STAGE(PG8_SA(1, 1), rAc, a1 + hstep, voffA);
;             PG8_WAIT_V(8); PG8_WAIT_L(0); PG8_BAR; PG8_MMA(0, 0, At, B0); PG8_MMA(0, 1, At, B1); PG8_BAR; PG8_SCHED;
;             PG8_LDA(At, 0, 1); PG8_STAGE(PG8_SB(0, 0), rB2, b2, voffB); PG8_STAGE(PG8_SB(0, 1), rB2, b2 + hstep, voffB); PG8_STAGE(PG8_SA(0, 0), rA2, a2, voffA);
;             PG8_WAIT_V(8); PG8_WAIT_L(0); PG8_BAR; PG8_MMA(1, 0, At, B0); PG8_MMA(1, 1, At, B1); PG8_BAR; PG8_SCHED;
.LBB0_1942:
	s_mov_b32 s68, s94
	s_lshl_b32 s85, s84, 19
	s_andn2_b64 vcc, exec, s[22:23]
	s_lshl_b32 s94, s83, 19
	s_cbranch_vccnz .LBB0_1966
	s_and_b64 s[6:7], s[26:27], exec
	s_waitcnt vmcnt(37)
	s_waitcnt vmcnt(36)
	s_waitcnt vmcnt(35)
	s_waitcnt vmcnt(32)
	s_waitcnt vmcnt(31)
	s_waitcnt vmcnt(28)
	s_waitcnt vmcnt(27)
	s_waitcnt vmcnt(24)
	s_waitcnt vmcnt(23)
	s_cselect_b32 s29, s85, s55
	s_cselect_b32 s60, s94, s54
	s_add_i32 s61, s55, 0x80
	s_add_i32 s62, s54, 0x100
	s_mov_b32 s63, 0
	s_waitcnt vmcnt(0)
	v_add_u32_e32 v136, 0x10000, v174
	v_add_u32_e32 v156, 0x14000, v174
	ds_read_b128 v[120:123], v136
	ds_read_b128 v[124:127], v136 offset:1024
	ds_read_b128 v[132:135], v136 offset:2048
	ds_read_b128 v[136:139], v136 offset:3072
	ds_read_b128 v[144:147], v156
	ds_read_b128 v[148:151], v156 offset:1024
	ds_read_b128 v[152:155], v156 offset:2048
	ds_read_b128 v[156:159], v156 offset:3072
	s_add_i32 s6, s61, 0x80
	s_cmp_eq_u32 s77, s63
	s_cselect_b32 s66, s29, s6
	s_cselect_b32 s55, s60, s62
	s_or_b32 s54, s66, 0x80
	s_add_i32 s6, s33, s61
	s_mov_b32 m0, s79
	ds_read_b128 v[160:163], v175
	ds_read_b128 v[164:167], v175 offset:1024
	ds_read_b128 v[176:179], v175 offset:2048
	ds_read_b128 v[180:183], v175 offset:3072
	ds_read_b128 v[184:187], v175 offset:4096
	ds_read_b128 v[188:191], v175 offset:5120
	ds_read_b128 v[192:195], v175 offset:6144
	ds_read_b128 v[196:199], v175 offset:7168
	buffer_load_dwordx4 v168, s[36:39], s6 offen lds
	s_mov_b32 m0, s82
	s_nop 0
	buffer_load_dwordx4 v170, s[36:39], s6 offen lds
	s_waitcnt vmcnt(8)
	s_waitcnt lgkmcnt(0)
	s_barrier
	s_setprio 1
	v_mfma_f32_16x16x32_bf16 v[140:143], v[120:123], v[160:163], 0
	v_mfma_f32_16x16x32_bf16 v[128:131], v[132:135], v[160:163], 0
	v_mfma_f32_16x16x32_bf16 v[108:111], v[120:123], v[176:179], 0
	v_mfma_f32_16x16x32_bf16 v[104:107], v[132:135], v[176:179], 0
	v_mfma_f32_16x16x32_bf16 v[92:95], v[120:123], v[184:187], 0
	v_mfma_f32_16x16x32_bf16 v[88:91], v[132:135], v[184:187], 0
	v_mfma_f32_16x16x32_bf16 v[76:79], v[120:123], v[192:195], 0
	v_mfma_f32_16x16x32_bf16 v[72:75], v[132:135], v[192:195], 0
	v_mfma_f32_16x16x32_bf16 v[140:143], v[124:127], v[164:167], v[140:143]
	v_mfma_f32_16x16x32_bf16 v[128:131], v[136:139], v[164:167], v[128:131]
	v_mfma_f32_16x16x32_bf16 v[108:111], v[124:127], v[180:183], v[108:111]
	v_mfma_f32_16x16x32_bf16 v[104:107], v[136:139], v[180:183], v[104:107]
	v_mfma_f32_16x16x32_bf16 v[92:95], v[124:127], v[188:191], v[92:95]
	v_mfma_f32_16x16x32_bf16 v[88:91], v[136:139], v[188:191], v[88:91]
	v_mfma_f32_16x16x32_bf16 v[76:79], v[124:127], v[196:199], v[76:79]
	v_mfma_f32_16x16x32_bf16 v[72:75], v[136:139], v[196:199], v[72:75]
	v_mfma_f32_16x16x32_bf16 v[116:119], v[144:147], v[160:163], 0
	v_mfma_f32_16x16x32_bf16 v[112:115], v[152:155], v[160:163], 0
	v_mfma_f32_16x16x32_bf16 v[100:103], v[144:147], v[176:179], 0
	v_mfma_f32_16x16x32_bf16 v[96:99], v[152:155], v[176:179], 0
	v_mfma_f32_16x16x32_bf16 v[84:87], v[144:147], v[184:187], 0
	v_mfma_f32_16x16x32_bf16 v[80:83], v[152:155], v[184:187], 0
	v_mfma_f32_16x16x32_bf16 v[68:71], v[144:147], v[192:195], 0
	v_mfma_f32_16x16x32_bf16 v[64:67], v[152:155], v[192:195], 0
	v_mfma_f32_16x16x32_bf16 v[116:119], v[148:151], v[164:167], v[116:119]
	v_mfma_f32_16x16x32_bf16 v[112:115], v[156:159], v[164:167], v[112:115]
	v_mfma_f32_16x16x32_bf16 v[100:103], v[148:151], v[180:183], v[100:103]
	v_mfma_f32_16x16x32_bf16 v[96:99], v[156:159], v[180:183], v[96:99]
	v_mfma_f32_16x16x32_bf16 v[84:87], v[148:151], v[188:191], v[84:87]
	v_mfma_f32_16x16x32_bf16 v[80:83], v[156:159], v[188:191], v[80:83]
	v_mfma_f32_16x16x32_bf16 v[68:71], v[148:151], v[196:199], v[68:71]
	v_mfma_f32_16x16x32_bf16 v[64:67], v[156:159], v[196:199], v[64:67]
	s_setprio 0
	s_barrier
	s_mov_b32 m0, s35
	s_mov_b32 s6, s38
	s_mov_b32 s7, s39
	ds_read_b128 v[160:163], v175 offset:16384
	ds_read_b128 v[164:167], v175 offset:17408
	ds_read_b128 v[176:179], v175 offset:18432
	ds_read_b128 v[180:183], v175 offset:19456
	ds_read_b128 v[184:187], v175 offset:20480
	ds_read_b128 v[188:191], v175 offset:21504
	ds_read_b128 v[192:195], v175 offset:22528
	ds_read_b128 v[196:199], v175 offset:23552
	buffer_load_dwordx4 v169, s[4:7], s55 offen lds
	s_mov_b32 m0, s41
	s_add_i32 s67, s55, s33
	buffer_load_dwordx4 v171, s[4:7], s55 offen lds
	s_mov_b32 m0, s42
	s_nop 0
	buffer_load_dwordx4 v169, s[4:7], s67 offen lds
	s_mov_b32 m0, s43
	s_nop 0
	buffer_load_dwordx4 v171, s[4:7], s67 offen lds
	s_mov_b32 m0, s34
	s_nop 0
	buffer_load_dwordx4 v168, s[36:39], s66 offen lds
	s_mov_b32 m0, s44
	s_nop 0
	buffer_load_dwordx4 v170, s[36:39], s66 offen lds
	s_waitcnt vmcnt(8)
	s_waitcnt lgkmcnt(0)
	s_barrier
; #define PG8_STAGE(bufoff, rs_, soff_, voff) do { _Pragma("unroll") for (int _i = 0; _i < 2; ++_i) \
;         __builtin_amdgcn_raw_ptr_buffer_load_lds(rs_, (LAS void*)(lds + (bufoff) + ldsw + _i * 8192), 16, (int)(voff)[_i], (int)(soff_), 0, 0); } while (0)
; #define PG8_LDA(dst, b, h) do { _Pragma("unroll") for (int m = 0; m < 4; ++m) dst[m] = PG8_LD2(lds + PG8_SA(b, h) + aoff + m * 2048); } while (0)
; #define PG8_LDB(dst, b, h) do { _Pragma("unroll") for (int n = 0; n < 2; ++n) dst[n] = PG8_LD2(lds + PG8_SB(b, h) + boff + n * 2048); } while (0)
; #define PG8_WAIT_V(n) asm volatile("s_waitcnt vmcnt(" #n ")" ::: "memory")
; #define PG8_WAIT_L(n) asm volatile("s_waitcnt lgkmcnt(" #n ")" ::: "memory")
; #define PG8_BAR __builtin_amdgcn_s_barrier()
; #define PG8_SCHED __builtin_amdgcn_sched_barrier(0)
; template <class Epi, class Sched, bool ALIGN_EPI = false, bool SP2 = false, bool FP8 = false>
; __device__ __forceinline__ void gemm_phase(LAS unsigned char* lds, const Gemm g, const Sched& S, const Epi& E, int wbase) {
;     ...
;             PG8_WAIT_V(8); PG8_WAIT_L(0); PG8_BAR; PG8_MMA(1, 0, At, B0); PG8_MMA(1, 1, At, B1); PG8_BAR; PG8_SCHED;
;             PG8_LDB(B0, 1, 0); PG8_LDB(B1, 1, 1); PG8_SCHED; PG8_LDA(At, 1, 0); PG8_STAGE(PG8_SA(0, 1), rA2, a2 + hstep, voffA);
;             PG8_WAIT_V(8); PG8_WAIT_L(0); PG8_BAR; PG8_MMA(0, 0, At, B0); PG8_MMA(0, 1, At, B1); PG8_BAR; PG8_SCHED;
	s_setprio 1
	v_mfma_f32_16x16x32_bf16 v[60:63], v[120:123], v[160:163], 0
	v_mfma_f32_16x16x32_bf16 v[56:59], v[132:135], v[160:163], 0
	v_mfma_f32_16x16x32_bf16 v[44:47], v[120:123], v[176:179], 0
	v_mfma_f32_16x16x32_bf16 v[40:43], v[132:135], v[176:179], 0
	v_mfma_f32_16x16x32_bf16 v[28:31], v[120:123], v[184:187], 0
	v_mfma_f32_16x16x32_bf16 v[24:27], v[132:135], v[184:187], 0
	v_mfma_f32_16x16x32_bf16 v[12:15], v[120:123], v[192:195], 0
	v_mfma_f32_16x16x32_bf16 v[8:11], v[132:135], v[192:195], 0
	v_mfma_f32_16x16x32_bf16 v[60:63], v[124:127], v[164:167], v[60:63]
	v_mfma_f32_16x16x32_bf16 v[56:59], v[136:139], v[164:167], v[56:59]
	v_mfma_f32_16x16x32_bf16 v[44:47], v[124:127], v[180:183], v[44:47]
	v_mfma_f32_16x16x32_bf16 v[40:43], v[136:139], v[180:183], v[40:43]
	v_mfma_f32_16x16x32_bf16 v[28:31], v[124:127], v[188:191], v[28:31]
	v_mfma_f32_16x16x32_bf16 v[24:27], v[136:139], v[188:191], v[24:27]
	v_mfma_f32_16x16x32_bf16 v[12:15], v[124:127], v[196:199], v[12:15]
	v_mfma_f32_16x16x32_bf16 v[8:11], v[136:139], v[196:199], v[8:11]
	v_mfma_f32_16x16x32_bf16 v[52:55], v[144:147], v[160:163], 0
	v_mfma_f32_16x16x32_bf16 v[48:51], v[152:155], v[160:163], 0
	v_mfma_f32_16x16x32_bf16 v[36:39], v[144:147], v[176:179], 0
	v_mfma_f32_16x16x32_bf16 v[32:35], v[152:155], v[176:179], 0
	v_mfma_f32_16x16x32_bf16 v[20:23], v[144:147], v[184:187], 0
	v_mfma_f32_16x16x32_bf16 v[16:19], v[152:155], v[184:187], 0
	v_mfma_f32_16x16x32_bf16 v[4:7], v[144:147], v[192:195], 0
	v_mfma_f32_16x16x32_bf16 v[0:3], v[152:155], v[192:195], 0
	v_mfma_f32_16x16x32_bf16 v[52:55], v[148:151], v[164:167], v[52:55]
	v_mfma_f32_16x16x32_bf16 v[48:51], v[156:159], v[164:167], v[48:51]
	v_mfma_f32_16x16x32_bf16 v[36:39], v[148:151], v[180:183], v[36:39]
	v_mfma_f32_16x16x32_bf16 v[32:35], v[156:159], v[180:183], v[32:35]
	v_mfma_f32_16x16x32_bf16 v[20:23], v[148:151], v[188:191], v[20:23]
	v_mfma_f32_16x16x32_bf16 v[16:19], v[156:159], v[188:191], v[16:19]
	v_mfma_f32_16x16x32_bf16 v[4:7], v[148:151], v[196:199], v[4:7]
	v_mfma_f32_16x16x32_bf16 v[0:3], v[156:159], v[196:199], v[0:3]
	s_setprio 0
	s_barrier
	v_add_u32_e32 v136, 0x18000, v174
	v_add_u32_e32 v156, 0x1c000, v174
	ds_read_b128 v[120:123], v136
	ds_read_b128 v[124:127], v136 offset:1024
	ds_read_b128 v[132:135], v136 offset:2048
	ds_read_b128 v[136:139], v136 offset:3072
	ds_read_b128 v[144:147], v156
	ds_read_b128 v[148:151], v156 offset:1024
	ds_read_b128 v[152:155], v156 offset:2048
	ds_read_b128 v[156:159], v156 offset:3072
	s_add_i32 s66, s66, s33
	s_mov_b32 m0, s45
	ds_read_b128 v[160:163], v175 offset:32768
	ds_read_b128 v[164:167], v175 offset:33792
	ds_read_b128 v[176:179], v175 offset:34816
	ds_read_b128 v[180:183], v175 offset:35840
	ds_read_b128 v[184:187], v175 offset:36864
	ds_read_b128 v[188:191], v175 offset:37888
	ds_read_b128 v[192:195], v175 offset:38912
	ds_read_b128 v[196:199], v175 offset:39936
	buffer_load_dwordx4 v168, s[36:39], s66 offen lds
	s_mov_b32 m0, s46
	s_nop 0
	buffer_load_dwordx4 v170, s[36:39], s66 offen lds
	s_waitcnt vmcnt(8)
	s_waitcnt lgkmcnt(0)
	s_barrier
	s_setprio 1
	v_mfma_f32_16x16x32_bf16 v[140:143], v[120:123], v[160:163], v[140:143]
	v_mfma_f32_16x16x32_bf16 v[128:131], v[132:135], v[160:163], v[128:131]
	v_mfma_f32_16x16x32_bf16 v[108:111], v[120:123], v[176:179], v[108:111]
	v_mfma_f32_16x16x32_bf16 v[104:107], v[132:135], v[176:179], v[104:107]
	v_mfma_f32_16x16x32_bf16 v[92:95], v[120:123], v[184:187], v[92:95]
	v_mfma_f32_16x16x32_bf16 v[88:91], v[132:135], v[184:187], v[88:91]
	v_mfma_f32_16x16x32_bf16 v[76:79], v[120:123], v[192:195], v[76:79]
	v_mfma_f32_16x16x32_bf16 v[72:75], v[132:135], v[192:195], v[72:75]
	v_mfma_f32_16x16x32_bf16 v[140:143], v[124:127], v[164:167], v[140:143]
	v_mfma_f32_16x16x32_bf16 v[128:131], v[136:139], v[164:167], v[128:131]
	v_mfma_f32_16x16x32_bf16 v[108:111], v[124:127], v[180:183], v[108:111]
	v_mfma_f32_16x16x32_bf16 v[104:107], v[136:139], v[180:183], v[104:107]
	v_mfma_f32_16x16x32_bf16 v[92:95], v[124:127], v[188:191], v[92:95]
	v_mfma_f32_16x16x32_bf16 v[88:91], v[136:139], v[188:191], v[88:91]
	v_mfma_f32_16x16x32_bf16 v[76:79], v[124:127], v[196:199], v[76:79]
	v_mfma_f32_16x16x32_bf16 v[72:75], v[136:139], v[196:199], v[72:75]
	v_mfma_f32_16x16x32_bf16 v[116:119], v[144:147], v[160:163], v[116:119]
	v_mfma_f32_16x16x32_bf16 v[112:115], v[152:155], v[160:163], v[112:115]
	v_mfma_f32_16x16x32_bf16 v[100:103], v[144:147], v[176:179], v[100:103]
	v_mfma_f32_16x16x32_bf16 v[96:99], v[152:155], v[176:179], v[96:99]
	v_mfma_f32_16x16x32_bf16 v[84:87], v[144:147], v[184:187], v[84:87]
	v_mfma_f32_16x16x32_bf16 v[80:83], v[152:155], v[184:187], v[80:83]
	v_mfma_f32_16x16x32_bf16 v[68:71], v[144:147], v[192:195], v[68:71]
	v_mfma_f32_16x16x32_bf16 v[64:67], v[152:155], v[192:195], v[64:67]
	v_mfma_f32_16x16x32_bf16 v[116:119], v[148:151], v[164:167], v[116:119]
	v_mfma_f32_16x16x32_bf16 v[112:115], v[156:159], v[164:167], v[112:115]
	v_mfma_f32_16x16x32_bf16 v[100:103], v[148:151], v[180:183], v[100:103]
	v_mfma_f32_16x16x32_bf16 v[96:99], v[156:159], v[180:183], v[96:99]
	v_mfma_f32_16x16x32_bf16 v[84:87], v[148:151], v[188:191], v[84:87]
	v_mfma_f32_16x16x32_bf16 v[80:83], v[156:159], v[188:191], v[80:83]
	v_mfma_f32_16x16x32_bf16 v[68:71], v[148:151], v[196:199], v[68:71]
	v_mfma_f32_16x16x32_bf16 v[64:67], v[156:159], v[196:199], v[64:67]
	s_setprio 0
	s_barrier
; #define PG8_STAGE(bufoff, rs_, soff_, voff) do { _Pragma("unroll") for (int _i = 0; _i < 2; ++_i) \
;         __builtin_amdgcn_raw_ptr_buffer_load_lds(rs_, (LAS void*)(lds + (bufoff) + ldsw + _i * 8192), 16, (int)(voff)[_i], (int)(soff_), 0, 0); } while (0)
; #define PG8_LDA(dst, b, h) do { _Pragma("unroll") for (int m = 0; m < 4; ++m) dst[m] = PG8_LD2(lds + PG8_SA(b, h) + aoff + m * 2048); } while (0)
; #define PG8_LDB(dst, b, h) do { _Pragma("unroll") for (int n = 0; n < 2; ++n) dst[n] = PG8_LD2(lds + PG8_SB(b, h) + boff + n * 2048); } while (0)
; #define PG8_WAIT_V(n) asm volatile("s_waitcnt vmcnt(" #n ")" ::: "memory")
; #define PG8_WAIT_L(n) asm volatile("s_waitcnt lgkmcnt(" #n ")" ::: "memory")
; #define PG8_BAR __builtin_amdgcn_s_barrier()
; #define PG8_SCHED __builtin_amdgcn_sched_barrier(0)
; template <class Epi, class Sched, bool ALIGN_EPI = false, bool SP2 = false, bool FP8 = false>
; __device__ __forceinline__ void gemm_phase(LAS unsigned char* lds, const Gemm g, const Sched& S, const Epi& E, int wbase) {
;     ...
;             PG8_LDB(B0, 0, 0); PG8_LDB(B1, 0, 1); PG8_SCHED; PG8_LDA(At, 0, 0); PG8_STAGE(PG8_SA(1, 1), rAc, a1 + hstep, voffA);
;             PG8_WAIT_V(8); PG8_WAIT_L(0); PG8_BAR; PG8_MMA(0, 0, At, B0); PG8_MMA(0, 1, At, B1); PG8_BAR; PG8_SCHED;
;     ...
;             PG8_WAIT_V(8); PG8_WAIT_L(0); PG8_BAR; PG8_MMA(0, 0, At, B0); PG8_MMA(0, 1, At, B1); PG8_BAR; PG8_SCHED;
;             PG8_LDA(At, 1, 1); PG8_STAGE(PG8_SB(1, 0), rB2, b3, voffB); PG8_STAGE(PG8_SB(1, 1), rB2, b3 + hstep, voffB); PG8_STAGE(PG8_SA(1, 0), rA2, a3, voffA);
;             PG8_WAIT_V(8); PG8_WAIT_L(0); PG8_BAR; PG8_MMA(1, 0, At, B0); PG8_MMA(1, 1, At, B1); PG8_BAR; PG8_SCHED;
	s_mov_b32 m0, s47
	s_bitset1_b32 s55, 7
	ds_read_b128 v[160:163], v175 offset:49152
	ds_read_b128 v[164:167], v175 offset:50176
	ds_read_b128 v[176:179], v175 offset:51200
	ds_read_b128 v[180:183], v175 offset:52224
	ds_read_b128 v[184:187], v175 offset:53248
	ds_read_b128 v[188:191], v175 offset:54272
	ds_read_b128 v[192:195], v175 offset:55296
	ds_read_b128 v[196:199], v175 offset:56320
	buffer_load_dwordx4 v169, s[4:7], s55 offen lds
	s_mov_b32 m0, s48
	s_nop 0
	buffer_load_dwordx4 v171, s[4:7], s55 offen lds
	s_add_i32 s55, s55, s33
	s_mov_b32 m0, s56
	s_nop 0
	buffer_load_dwordx4 v169, s[4:7], s55 offen lds
	s_mov_b32 m0, s57
	s_nop 0
	buffer_load_dwordx4 v171, s[4:7], s55 offen lds
	s_mov_b32 m0, s52
	s_nop 0
	buffer_load_dwordx4 v168, s[36:39], s54 offen lds
	s_mov_b32 m0, s53
	s_nop 0
	buffer_load_dwordx4 v170, s[36:39], s54 offen lds
	s_waitcnt vmcnt(8)
	s_waitcnt lgkmcnt(0)
	s_barrier
	s_setprio 1
	v_mfma_f32_16x16x32_bf16 v[60:63], v[120:123], v[160:163], v[60:63]
	v_mfma_f32_16x16x32_bf16 v[56:59], v[132:135], v[160:163], v[56:59]
	v_mfma_f32_16x16x32_bf16 v[44:47], v[120:123], v[176:179], v[44:47]
	v_mfma_f32_16x16x32_bf16 v[40:43], v[132:135], v[176:179], v[40:43]
	v_mfma_f32_16x16x32_bf16 v[28:31], v[120:123], v[184:187], v[28:31]
	v_mfma_f32_16x16x32_bf16 v[24:27], v[132:135], v[184:187], v[24:27]
	v_mfma_f32_16x16x32_bf16 v[12:15], v[120:123], v[192:195], v[12:15]
	v_mfma_f32_16x16x32_bf16 v[8:11], v[132:135], v[192:195], v[8:11]
	v_mfma_f32_16x16x32_bf16 v[60:63], v[124:127], v[164:167], v[60:63]
	v_mfma_f32_16x16x32_bf16 v[56:59], v[136:139], v[164:167], v[56:59]
	v_mfma_f32_16x16x32_bf16 v[44:47], v[124:127], v[180:183], v[44:47]
	v_mfma_f32_16x16x32_bf16 v[40:43], v[136:139], v[180:183], v[40:43]
	v_mfma_f32_16x16x32_bf16 v[28:31], v[124:127], v[188:191], v[28:31]
	v_mfma_f32_16x16x32_bf16 v[24:27], v[136:139], v[188:191], v[24:27]
	v_mfma_f32_16x16x32_bf16 v[12:15], v[124:127], v[196:199], v[12:15]
	v_mfma_f32_16x16x32_bf16 v[8:11], v[136:139], v[196:199], v[8:11]
	v_mfma_f32_16x16x32_bf16 v[52:55], v[144:147], v[160:163], v[52:55]
	v_mfma_f32_16x16x32_bf16 v[48:51], v[152:155], v[160:163], v[48:51]
	v_mfma_f32_16x16x32_bf16 v[36:39], v[144:147], v[176:179], v[36:39]
	v_mfma_f32_16x16x32_bf16 v[32:35], v[152:155], v[176:179], v[32:35]
	v_mfma_f32_16x16x32_bf16 v[20:23], v[144:147], v[184:187], v[20:23]
	v_mfma_f32_16x16x32_bf16 v[16:19], v[152:155], v[184:187], v[16:19]
	v_mfma_f32_16x16x32_bf16 v[4:7], v[144:147], v[192:195], v[4:7]
	v_mfma_f32_16x16x32_bf16 v[0:3], v[152:155], v[192:195], v[0:3]
	v_mfma_f32_16x16x32_bf16 v[52:55], v[148:151], v[164:167], v[52:55]
	v_mfma_f32_16x16x32_bf16 v[48:51], v[156:159], v[164:167], v[48:51]
	v_mfma_f32_16x16x32_bf16 v[36:39], v[148:151], v[180:183], v[36:39]
	v_mfma_f32_16x16x32_bf16 v[32:35], v[156:159], v[180:183], v[32:35]
	v_mfma_f32_16x16x32_bf16 v[20:23], v[148:151], v[188:191], v[20:23]
	v_mfma_f32_16x16x32_bf16 v[16:19], v[156:159], v[188:191], v[16:19]
	v_mfma_f32_16x16x32_bf16 v[4:7], v[148:151], v[196:199], v[4:7]
	v_mfma_f32_16x16x32_bf16 v[0:3], v[156:159], v[196:199], v[0:3]
	s_setprio 0
	s_barrier
	s_add_i32 s63, s63, 2
	s_addk_i32 s61, 0x100
	s_addk_i32 s62, 0x100
	s_cmp_ge_i32 s63, s65
	s_cbranch_scc0 .LBB0_1944
	s_branch .Lzp_after_1944
.LBB0_1944:
	v_add_u32_e32 v136, 0x10000, v174
	v_add_u32_e32 v156, 0x14000, v174
	ds_read_b128 v[120:123], v136
	ds_read_b128 v[124:127], v136 offset:1024
	ds_read_b128 v[132:135], v136 offset:2048
	ds_read_b128 v[136:139], v136 offset:3072
	ds_read_b128 v[144:147], v156
	ds_read_b128 v[148:151], v156 offset:1024
	ds_read_b128 v[152:155], v156 offset:2048
	ds_read_b128 v[156:159], v156 offset:3072
	s_add_i32 s6, s61, 0x80
	s_cmp_eq_u32 s77, s63
	s_cselect_b32 s66, s29, s6
	s_cselect_b32 s55, s60, s62
	s_or_b32 s54, s66, 0x80
	s_add_i32 s6, s33, s61
	s_mov_b32 m0, s79
	ds_read_b128 v[160:163], v175
	ds_read_b128 v[164:167], v175 offset:1024
	ds_read_b128 v[176:179], v175 offset:2048
	ds_read_b128 v[180:183], v175 offset:3072
	ds_read_b128 v[184:187], v175 offset:4096
	ds_read_b128 v[188:191], v175 offset:5120
	ds_read_b128 v[192:195], v175 offset:6144
	ds_read_b128 v[196:199], v175 offset:7168
	buffer_load_dwordx4 v168, s[36:39], s6 offen lds
	s_mov_b32 m0, s82
	s_nop 0
	buffer_load_dwordx4 v170, s[36:39], s6 offen lds
	s_waitcnt vmcnt(8)
	s_waitcnt lgkmcnt(0)
	s_barrier
	s_setprio 1
	v_mfma_f32_16x16x32_bf16 v[140:143], v[120:123], v[160:163], v[140:143]
	v_mfma_f32_16x16x32_bf16 v[128:131], v[132:135], v[160:163], v[128:131]
	v_mfma_f32_16x16x32_bf16 v[108:111], v[120:123], v[176:179], v[108:111]
	v_mfma_f32_16x16x32_bf16 v[104:107], v[132:135], v[176:179], v[104:107]
	v_mfma_f32_16x16x32_bf16 v[92:95], v[120:123], v[184:187], v[92:95]
	v_mfma_f32_16x16x32_bf16 v[88:91], v[132:135], v[184:187], v[88:91]
	v_mfma_f32_16x16x32_bf16 v[76:79], v[120:123], v[192:195], v[76:79]
	v_mfma_f32_16x16x32_bf16 v[72:75], v[132:135], v[192:195], v[72:75]
	v_mfma_f32_16x16x32_bf16 v[140:143], v[124:127], v[164:167], v[140:143]
	v_mfma_f32_16x16x32_bf16 v[128:131], v[136:139], v[164:167], v[128:131]
	v_mfma_f32_16x16x32_bf16 v[108:111], v[124:127], v[180:183], v[108:111]
	v_mfma_f32_16x16x32_bf16 v[104:107], v[136:139], v[180:183], v[104:107]
	v_mfma_f32_16x16x32_bf16 v[92:95], v[124:127], v[188:191], v[92:95]
	v_mfma_f32_16x16x32_bf16 v[88:91], v[136:139], v[188:191], v[88:91]
	v_mfma_f32_16x16x32_bf16 v[76:79], v[124:127], v[196:199], v[76:79]
	v_mfma_f32_16x16x32_bf16 v[72:75], v[136:139], v[196:199], v[72:75]
	v_mfma_f32_16x16x32_bf16 v[116:119], v[144:147], v[160:163], v[116:119]
	v_mfma_f32_16x16x32_bf16 v[112:115], v[152:155], v[160:163], v[112:115]
	v_mfma_f32_16x16x32_bf16 v[100:103], v[144:147], v[176:179], v[100:103]
	v_mfma_f32_16x16x32_bf16 v[96:99], v[152:155], v[176:179], v[96:99]
	v_mfma_f32_16x16x32_bf16 v[84:87], v[144:147], v[184:187], v[84:87]
	v_mfma_f32_16x16x32_bf16 v[80:83], v[152:155], v[184:187], v[80:83]
	v_mfma_f32_16x16x32_bf16 v[68:71], v[144:147], v[192:195], v[68:71]
	v_mfma_f32_16x16x32_bf16 v[64:67], v[152:155], v[192:195], v[64:67]
	v_mfma_f32_16x16x32_bf16 v[116:119], v[148:151], v[164:167], v[116:119]
	v_mfma_f32_16x16x32_bf16 v[112:115], v[156:159], v[164:167], v[112:115]
	v_mfma_f32_16x16x32_bf16 v[100:103], v[148:151], v[180:183], v[100:103]
	v_mfma_f32_16x16x32_bf16 v[96:99], v[156:159], v[180:183], v[96:99]
	v_mfma_f32_16x16x32_bf16 v[84:87], v[148:151], v[188:191], v[84:87]
	v_mfma_f32_16x16x32_bf16 v[80:83], v[156:159], v[188:191], v[80:83]
	v_mfma_f32_16x16x32_bf16 v[68:71], v[148:151], v[196:199], v[68:71]
	v_mfma_f32_16x16x32_bf16 v[64:67], v[156:159], v[196:199], v[64:67]
	s_setprio 0
	s_barrier
; #define PG8_STAGE(bufoff, rs_, soff_, voff) do { _Pragma("unroll") for (int _i = 0; _i < 2; ++_i) \
;         __builtin_amdgcn_raw_ptr_buffer_load_lds(rs_, (LAS void*)(lds + (bufoff) + ldsw + _i * 8192), 16, (int)(voff)[_i], (int)(soff_), 0, 0); } while (0)
; #define PG8_LDA(dst, b, h) do { _Pragma("unroll") for (int m = 0; m < 4; ++m) dst[m] = PG8_LD2(lds + PG8_SA(b, h) + aoff + m * 2048); } while (0)
; #define PG8_LDB(dst, b, h) do { _Pragma("unroll") for (int n = 0; n < 2; ++n) dst[n] = PG8_LD2(lds + PG8_SB(b, h) + boff + n * 2048); } while (0)
; #define PG8_WAIT_V(n) asm volatile("s_waitcnt vmcnt(" #n ")" ::: "memory")
; #define PG8_WAIT_L(n) asm volatile("s_waitcnt lgkmcnt(" #n ")" ::: "memory")
; #define PG8_BAR __builtin_amdgcn_s_barrier()
; #define PG8_SCHED __builtin_amdgcn_sched_barrier(0)
; template <class Epi, class Sched, bool ALIGN_EPI = false, bool SP2 = false, bool FP8 = false>
; __device__ __forceinline__ void gemm_phase(LAS unsigned char* lds, const Gemm g, const Sched& S, const Epi& E, int wbase) {
;     ...
;             PG8_LDA(At, 0, 1); PG8_STAGE(PG8_SB(0, 0), rB2, b2, voffB); PG8_STAGE(PG8_SB(0, 1), rB2, b2 + hstep, voffB); PG8_STAGE(PG8_SA(0, 0), rA2, a2, voffA);
;             PG8_WAIT_V(8); PG8_WAIT_L(0); PG8_BAR; PG8_MMA(1, 0, At, B0); PG8_MMA(1, 1, At, B1); PG8_BAR; PG8_SCHED;
;             PG8_LDB(B0, 1, 0); PG8_LDB(B1, 1, 1); PG8_SCHED; PG8_LDA(At, 1, 0); PG8_STAGE(PG8_SA(0, 1), rA2, a2 + hstep, voffA);
;             PG8_WAIT_V(8); PG8_WAIT_L(0); PG8_BAR; PG8_MMA(0, 0, At, B0); PG8_MMA(0, 1, At, B1); PG8_BAR; PG8_SCHED;
	s_mov_b32 m0, s35
	s_mov_b32 s6, s38
	s_mov_b32 s7, s39
	ds_read_b128 v[160:163], v175 offset:16384
	ds_read_b128 v[164:167], v175 offset:17408
	ds_read_b128 v[176:179], v175 offset:18432
	ds_read_b128 v[180:183], v175 offset:19456
	ds_read_b128 v[184:187], v175 offset:20480
	ds_read_b128 v[188:191], v175 offset:21504
	ds_read_b128 v[192:195], v175 offset:22528
	ds_read_b128 v[196:199], v175 offset:23552
	buffer_load_dwordx4 v169, s[4:7], s55 offen lds
	s_mov_b32 m0, s41
	s_add_i32 s67, s55, s33
	buffer_load_dwordx4 v171, s[4:7], s55 offen lds
	s_mov_b32 m0, s42
	s_nop 0
	buffer_load_dwordx4 v169, s[4:7], s67 offen lds
	s_mov_b32 m0, s43
	s_nop 0
	buffer_load_dwordx4 v171, s[4:7], s67 offen lds
	s_mov_b32 m0, s34
	s_nop 0
	buffer_load_dwordx4 v168, s[36:39], s66 offen lds
	s_mov_b32 m0, s44
	s_nop 0
	buffer_load_dwordx4 v170, s[36:39], s66 offen lds
	s_waitcnt vmcnt(8)
	s_waitcnt lgkmcnt(0)
	s_barrier
	s_setprio 1
	v_mfma_f32_16x16x32_bf16 v[60:63], v[120:123], v[160:163], v[60:63]
	v_mfma_f32_16x16x32_bf16 v[56:59], v[132:135], v[160:163], v[56:59]
	v_mfma_f32_16x16x32_bf16 v[44:47], v[120:123], v[176:179], v[44:47]
	v_mfma_f32_16x16x32_bf16 v[40:43], v[132:135], v[176:179], v[40:43]
	v_mfma_f32_16x16x32_bf16 v[28:31], v[120:123], v[184:187], v[28:31]
	v_mfma_f32_16x16x32_bf16 v[24:27], v[132:135], v[184:187], v[24:27]
	v_mfma_f32_16x16x32_bf16 v[12:15], v[120:123], v[192:195], v[12:15]
	v_mfma_f32_16x16x32_bf16 v[8:11], v[132:135], v[192:195], v[8:11]
	v_mfma_f32_16x16x32_bf16 v[60:63], v[124:127], v[164:167], v[60:63]
	v_mfma_f32_16x16x32_bf16 v[56:59], v[136:139], v[164:167], v[56:59]
	v_mfma_f32_16x16x32_bf16 v[44:47], v[124:127], v[180:183], v[44:47]
	v_mfma_f32_16x16x32_bf16 v[40:43], v[136:139], v[180:183], v[40:43]
	v_mfma_f32_16x16x32_bf16 v[28:31], v[124:127], v[188:191], v[28:31]
	v_mfma_f32_16x16x32_bf16 v[24:27], v[136:139], v[188:191], v[24:27]
	v_mfma_f32_16x16x32_bf16 v[12:15], v[124:127], v[196:199], v[12:15]
	v_mfma_f32_16x16x32_bf16 v[8:11], v[136:139], v[196:199], v[8:11]
	v_mfma_f32_16x16x32_bf16 v[52:55], v[144:147], v[160:163], v[52:55]
	v_mfma_f32_16x16x32_bf16 v[48:51], v[152:155], v[160:163], v[48:51]
	v_mfma_f32_16x16x32_bf16 v[36:39], v[144:147], v[176:179], v[36:39]
	v_mfma_f32_16x16x32_bf16 v[32:35], v[152:155], v[176:179], v[32:35]
	v_mfma_f32_16x16x32_bf16 v[20:23], v[144:147], v[184:187], v[20:23]
	v_mfma_f32_16x16x32_bf16 v[16:19], v[152:155], v[184:187], v[16:19]
	v_mfma_f32_16x16x32_bf16 v[4:7], v[144:147], v[192:195], v[4:7]
	v_mfma_f32_16x16x32_bf16 v[0:3], v[152:155], v[192:195], v[0:3]
	v_mfma_f32_16x16x32_bf16 v[52:55], v[148:151], v[164:167], v[52:55]
	v_mfma_f32_16x16x32_bf16 v[48:51], v[156:159], v[164:167], v[48:51]
	v_mfma_f32_16x16x32_bf16 v[36:39], v[148:151], v[180:183], v[36:39]
	v_mfma_f32_16x16x32_bf16 v[32:35], v[156:159], v[180:183], v[32:35]
	v_mfma_f32_16x16x32_bf16 v[20:23], v[148:151], v[188:191], v[20:23]
	v_mfma_f32_16x16x32_bf16 v[16:19], v[156:159], v[188:191], v[16:19]
	v_mfma_f32_16x16x32_bf16 v[4:7], v[148:151], v[196:199], v[4:7]
	v_mfma_f32_16x16x32_bf16 v[0:3], v[156:159], v[196:199], v[0:3]
	s_setprio 0
	s_barrier
	v_add_u32_e32 v136, 0x18000, v174
	v_add_u32_e32 v156, 0x1c000, v174
	ds_read_b128 v[120:123], v136
	ds_read_b128 v[124:127], v136 offset:1024
	ds_read_b128 v[132:135], v136 offset:2048
	ds_read_b128 v[136:139], v136 offset:3072
	ds_read_b128 v[144:147], v156
	ds_read_b128 v[148:151], v156 offset:1024
	ds_read_b128 v[152:155], v156 offset:2048
	ds_read_b128 v[156:159], v156 offset:3072
	s_add_i32 s66, s66, s33
	s_mov_b32 m0, s45
	ds_read_b128 v[160:163], v175 offset:32768
	ds_read_b128 v[164:167], v175 offset:33792
	ds_read_b128 v[176:179], v175 offset:34816
	ds_read_b128 v[180:183], v175 offset:35840
	ds_read_b128 v[184:187], v175 offset:36864
	ds_read_b128 v[188:191], v175 offset:37888
	ds_read_b128 v[192:195], v175 offset:38912
	ds_read_b128 v[196:199], v175 offset:39936
	buffer_load_dwordx4 v168, s[36:39], s66 offen lds
	s_mov_b32 m0, s46
	s_nop 0
	buffer_load_dwordx4 v170, s[36:39], s66 offen lds
	s_waitcnt vmcnt(8)
	s_waitcnt lgkmcnt(0)
	s_barrier
; #define PG8_STAGE(bufoff, rs_, soff_, voff) do { _Pragma("unroll") for (int _i = 0; _i < 2; ++_i) \
;         __builtin_amdgcn_raw_ptr_buffer_load_lds(rs_, (LAS void*)(lds + (bufoff) + ldsw + _i * 8192), 16, (int)(voff)[_i], (int)(soff_), 0, 0); } while (0)
; #define PG8_LDA(dst, b, h) do { _Pragma("unroll") for (int m = 0; m < 4; ++m) dst[m] = PG8_LD2(lds + PG8_SA(b, h) + aoff + m * 2048); } while (0)
; #define PG8_WAIT_V(n) asm volatile("s_waitcnt vmcnt(" #n ")" ::: "memory")
; #define PG8_WAIT_L(n) asm volatile("s_waitcnt lgkmcnt(" #n ")" ::: "memory")
; #define PG8_BAR __builtin_amdgcn_s_barrier()
; #define PG8_SCHED __builtin_amdgcn_sched_barrier(0)
; template <class Epi, class Sched, bool ALIGN_EPI = false, bool SP2 = false, bool FP8 = false>
; __device__ __forceinline__ void gemm_phase(LAS unsigned char* lds, const Gemm g, const Sched& S, const Epi& E, int wbase) {
;     ...
;             PG8_LDA(At, 1, 1); PG8_STAGE(PG8_SB(1, 0), rB2, b3, voffB); PG8_STAGE(PG8_SB(1, 1), rB2, b3 + hstep, voffB); PG8_STAGE(PG8_SA(1, 0), rA2, a3, voffA);
;             PG8_WAIT_V(8); PG8_WAIT_L(0); PG8_BAR; PG8_MMA(1, 0, At, B0); PG8_MMA(1, 1, At, B1); PG8_BAR; PG8_SCHED;
;     ...
;         if constexpr (ALIGN_EPI) { if (wr == 0) PG8_BAR; }
	s_setprio 1
	v_mfma_f32_16x16x32_bf16 v[140:143], v[120:123], v[160:163], v[140:143]
	v_mfma_f32_16x16x32_bf16 v[128:131], v[132:135], v[160:163], v[128:131]
	v_mfma_f32_16x16x32_bf16 v[108:111], v[120:123], v[176:179], v[108:111]
	v_mfma_f32_16x16x32_bf16 v[104:107], v[132:135], v[176:179], v[104:107]
	v_mfma_f32_16x16x32_bf16 v[92:95], v[120:123], v[184:187], v[92:95]
	v_mfma_f32_16x16x32_bf16 v[88:91], v[132:135], v[184:187], v[88:91]
	v_mfma_f32_16x16x32_bf16 v[76:79], v[120:123], v[192:195], v[76:79]
	v_mfma_f32_16x16x32_bf16 v[72:75], v[132:135], v[192:195], v[72:75]
	v_mfma_f32_16x16x32_bf16 v[140:143], v[124:127], v[164:167], v[140:143]
	v_mfma_f32_16x16x32_bf16 v[128:131], v[136:139], v[164:167], v[128:131]
	v_mfma_f32_16x16x32_bf16 v[108:111], v[124:127], v[180:183], v[108:111]
	v_mfma_f32_16x16x32_bf16 v[104:107], v[136:139], v[180:183], v[104:107]
	v_mfma_f32_16x16x32_bf16 v[92:95], v[124:127], v[188:191], v[92:95]
	v_mfma_f32_16x16x32_bf16 v[88:91], v[136:139], v[188:191], v[88:91]
	v_mfma_f32_16x16x32_bf16 v[76:79], v[124:127], v[196:199], v[76:79]
	v_mfma_f32_16x16x32_bf16 v[72:75], v[136:139], v[196:199], v[72:75]
	v_mfma_f32_16x16x32_bf16 v[116:119], v[144:147], v[160:163], v[116:119]
	v_mfma_f32_16x16x32_bf16 v[112:115], v[152:155], v[160:163], v[112:115]
	v_mfma_f32_16x16x32_bf16 v[100:103], v[144:147], v[176:179], v[100:103]
	v_mfma_f32_16x16x32_bf16 v[96:99], v[152:155], v[176:179], v[96:99]
	v_mfma_f32_16x16x32_bf16 v[84:87], v[144:147], v[184:187], v[84:87]
	v_mfma_f32_16x16x32_bf16 v[80:83], v[152:155], v[184:187], v[80:83]
	v_mfma_f32_16x16x32_bf16 v[68:71], v[144:147], v[192:195], v[68:71]
	v_mfma_f32_16x16x32_bf16 v[64:67], v[152:155], v[192:195], v[64:67]
	v_mfma_f32_16x16x32_bf16 v[116:119], v[148:151], v[164:167], v[116:119]
	v_mfma_f32_16x16x32_bf16 v[112:115], v[156:159], v[164:167], v[112:115]
	v_mfma_f32_16x16x32_bf16 v[100:103], v[148:151], v[180:183], v[100:103]
	v_mfma_f32_16x16x32_bf16 v[96:99], v[156:159], v[180:183], v[96:99]
	v_mfma_f32_16x16x32_bf16 v[84:87], v[148:151], v[188:191], v[84:87]
	v_mfma_f32_16x16x32_bf16 v[80:83], v[156:159], v[188:191], v[80:83]
	v_mfma_f32_16x16x32_bf16 v[68:71], v[148:151], v[196:199], v[68:71]
	v_mfma_f32_16x16x32_bf16 v[64:67], v[156:159], v[196:199], v[64:67]
	s_setprio 0
	s_barrier
	s_mov_b32 m0, s47
	s_bitset1_b32 s55, 7
	ds_read_b128 v[160:163], v175 offset:49152
	ds_read_b128 v[164:167], v175 offset:50176
	ds_read_b128 v[176:179], v175 offset:51200
	ds_read_b128 v[180:183], v175 offset:52224
	ds_read_b128 v[184:187], v175 offset:53248
	ds_read_b128 v[188:191], v175 offset:54272
	ds_read_b128 v[192:195], v175 offset:55296
	ds_read_b128 v[196:199], v175 offset:56320
	buffer_load_dwordx4 v169, s[4:7], s55 offen lds
	s_mov_b32 m0, s48
	s_nop 0
	buffer_load_dwordx4 v171, s[4:7], s55 offen lds
	s_add_i32 s55, s55, s33
	s_mov_b32 m0, s56
	s_nop 0
	buffer_load_dwordx4 v169, s[4:7], s55 offen lds
	s_mov_b32 m0, s57
	s_nop 0
	buffer_load_dwordx4 v171, s[4:7], s55 offen lds
	s_mov_b32 m0, s52
	s_nop 0
	buffer_load_dwordx4 v168, s[36:39], s54 offen lds
	s_mov_b32 m0, s53
	s_nop 0
	buffer_load_dwordx4 v170, s[36:39], s54 offen lds
	s_waitcnt vmcnt(8)
	s_waitcnt lgkmcnt(0)
	s_barrier
	s_setprio 1
	v_mfma_f32_16x16x32_bf16 v[60:63], v[120:123], v[160:163], v[60:63]
	v_mfma_f32_16x16x32_bf16 v[56:59], v[132:135], v[160:163], v[56:59]
	v_mfma_f32_16x16x32_bf16 v[44:47], v[120:123], v[176:179], v[44:47]
	v_mfma_f32_16x16x32_bf16 v[40:43], v[132:135], v[176:179], v[40:43]
	v_mfma_f32_16x16x32_bf16 v[28:31], v[120:123], v[184:187], v[28:31]
	v_mfma_f32_16x16x32_bf16 v[24:27], v[132:135], v[184:187], v[24:27]
	v_mfma_f32_16x16x32_bf16 v[12:15], v[120:123], v[192:195], v[12:15]
	v_mfma_f32_16x16x32_bf16 v[8:11], v[132:135], v[192:195], v[8:11]
	v_mfma_f32_16x16x32_bf16 v[60:63], v[124:127], v[164:167], v[60:63]
	v_mfma_f32_16x16x32_bf16 v[56:59], v[136:139], v[164:167], v[56:59]
	v_mfma_f32_16x16x32_bf16 v[44:47], v[124:127], v[180:183], v[44:47]
	v_mfma_f32_16x16x32_bf16 v[40:43], v[136:139], v[180:183], v[40:43]
	v_mfma_f32_16x16x32_bf16 v[28:31], v[124:127], v[188:191], v[28:31]
	v_mfma_f32_16x16x32_bf16 v[24:27], v[136:139], v[188:191], v[24:27]
	v_mfma_f32_16x16x32_bf16 v[12:15], v[124:127], v[196:199], v[12:15]
	v_mfma_f32_16x16x32_bf16 v[8:11], v[136:139], v[196:199], v[8:11]
	v_mfma_f32_16x16x32_bf16 v[52:55], v[144:147], v[160:163], v[52:55]
	v_mfma_f32_16x16x32_bf16 v[48:51], v[152:155], v[160:163], v[48:51]
	v_mfma_f32_16x16x32_bf16 v[36:39], v[144:147], v[176:179], v[36:39]
	v_mfma_f32_16x16x32_bf16 v[32:35], v[152:155], v[176:179], v[32:35]
	v_mfma_f32_16x16x32_bf16 v[20:23], v[144:147], v[184:187], v[20:23]
	v_mfma_f32_16x16x32_bf16 v[16:19], v[152:155], v[184:187], v[16:19]
	v_mfma_f32_16x16x32_bf16 v[4:7], v[144:147], v[192:195], v[4:7]
	v_mfma_f32_16x16x32_bf16 v[0:3], v[152:155], v[192:195], v[0:3]
	v_mfma_f32_16x16x32_bf16 v[52:55], v[148:151], v[164:167], v[52:55]
	v_mfma_f32_16x16x32_bf16 v[48:51], v[156:159], v[164:167], v[48:51]
	v_mfma_f32_16x16x32_bf16 v[36:39], v[148:151], v[180:183], v[36:39]
	v_mfma_f32_16x16x32_bf16 v[32:35], v[156:159], v[180:183], v[32:35]
	v_mfma_f32_16x16x32_bf16 v[20:23], v[148:151], v[188:191], v[20:23]
	v_mfma_f32_16x16x32_bf16 v[16:19], v[156:159], v[188:191], v[16:19]
	v_mfma_f32_16x16x32_bf16 v[4:7], v[148:151], v[196:199], v[4:7]
	v_mfma_f32_16x16x32_bf16 v[0:3], v[156:159], v[196:199], v[0:3]
	s_setprio 0
	s_barrier
	s_add_i32 s63, s63, 2
	s_addk_i32 s61, 0x100
	s_addk_i32 s62, 0x100
	s_cmp_ge_i32 s63, s65
	s_cbranch_scc0 .LBB0_1944
.Lzp_after_1944:
	s_and_b64 vcc, exec, s[24:25]
	s_cbranch_vccz .LBB0_1947
.LBB0_1946:
	s_barrier

; #define PG8_STAGE(bufoff, rs_, soff_, voff) do { _Pragma("unroll") for (int _i = 0; _i < 2; ++_i) \
;         __builtin_amdgcn_raw_ptr_buffer_load_lds(rs_, (LAS void*)(lds + (bufoff) + ldsw + _i * 8192), 16, (int)(voff)[_i], (int)(soff_), 0, 0); } while (0)
; #define PG8_LDA(dst, b, h) do { _Pragma("unroll") for (int m = 0; m < 4; ++m) dst[m] = PG8_LD2(lds + PG8_SA(b, h) + aoff + m * 2048); } while (0)
; #define PG8_LDB(dst, b, h) do { _Pragma("unroll") for (int n = 0; n < 2; ++n) dst[n] = PG8_LD2(lds + PG8_SB(b, h) + boff + n * 2048); } while (0)
; #define PG8_WAIT_V(n) asm volatile("s_waitcnt vmcnt(" #n ")" ::: "memory")
; #define PG8_WAIT_L(n) asm volatile("s_waitcnt lgkmcnt(" #n ")" ::: "memory")
; #define PG8_BAR __builtin_amdgcn_s_barrier()
; #define PG8_SCHED __builtin_amdgcn_sched_barrier(0)
; template <class Epi, class Sched, bool ALIGN_EPI = false, bool SP2 = false, bool FP8 = false>
; __device__ __forceinline__ void gemm_phase(LAS unsigned char* lds, const Gemm g, const Sched& S, const Epi& E, int wbase) {
;     ...
;             const unsigned a2 = last ? nA : cA + (unsigned)(t + 2) * kstep, b2 = last ? nB : cB + (unsigned)(t + 2) * kstep; const rsrc_t rA2 = (Sched::TWO && last) ? rAn : rAc, rB2 = (Sched::TWO && last) ? rBn : rBc;
;             const unsigned a3 = a2 + kstep, b3 = b2 + kstep;
;             if (last && has_next) S.a_ready(nxt);
;             if constexpr (SP2) {
;             PG8_LDB(B0, 0, 0); PG8_LDB(B1, 0, 1); PG8_SCHED; PG8_LDA(At, 0, 0); PG8_STAGE(PG8_SA(1, 1), rAc, a1 + hstep, voffA);
;             PG8_WAIT_V(8); PG8_WAIT_L(0); PG8_BAR; PG8_MMA(0, 0, At, B0); PG8_MMA(0, 1, At, B1); PG8_BAR; PG8_SCHED;
;             PG8_LDA(At, 0, 1); PG8_STAGE(PG8_SB(0, 0), rB2, b2, voffB); PG8_STAGE(PG8_SB(0, 1), rB2, b2 + hstep, voffB); PG8_STAGE(PG8_SA(0, 0), rA2, a2, voffA);
;             PG8_WAIT_V(8); PG8_WAIT_L(0); PG8_BAR; PG8_MMA(1, 0, At, B0); PG8_MMA(1, 1, At, B1); PG8_BAR; PG8_SCHED;
.LBB0_1988:
	s_lshl_b32 s95, s94, 18
	s_andn2_b64 vcc, exec, s[26:27]
	s_lshl_b32 s96, s9, 18
	s_cbranch_vccnz .LBB0_1992
	s_and_b64 s[2:3], s[34:35], exec
	s_waitcnt vmcnt(37)
	s_waitcnt vmcnt(36)
	s_waitcnt vmcnt(35)
	s_waitcnt vmcnt(32)
	s_waitcnt vmcnt(31)
	s_waitcnt vmcnt(28)
	s_waitcnt vmcnt(27)
	s_waitcnt vmcnt(24)
	s_waitcnt vmcnt(23)
	v_mov_b32_e32 v223, 0xff61b1e6
	v_mov_b32_e32 v222, 1
	v_mov_b32_e32 v173, v233
	v_mov_b32_e32 v172, 0x358637bd
	s_cselect_b32 s2, s95, s4
	s_cselect_b32 s3, s96, s5
	s_addk_i32 s4, 0x80
	s_addk_i32 s5, 0x100
	s_mov_b32 s61, 0
	s_waitcnt vmcnt(0)
	v_add_u32_e32 v136, 0x10000, v180
	v_add_u32_e32 v156, 0x14000, v180
	ds_read_b128 v[120:123], v136
	ds_read_b128 v[124:127], v136 offset:1024
	ds_read_b128 v[132:135], v136 offset:2048
	ds_read_b128 v[136:139], v136 offset:3072
	ds_read_b128 v[144:147], v156
	ds_read_b128 v[148:151], v156 offset:1024
	ds_read_b128 v[152:155], v156 offset:2048
	ds_read_b128 v[156:159], v156 offset:3072
	s_add_i32 s14, s4, 0x80
	s_cmp_eq_u32 s84, s61
	s_cselect_b32 s62, s2, s14
	s_cselect_b32 s55, s3, s5
	s_or_b32 s54, s62, 0x80
	s_add_i32 s14, s42, s4
	s_mov_b32 m0, s85
	ds_read_b128 v[160:163], v181
	ds_read_b128 v[164:167], v181 offset:1024
	ds_read_b128 v[182:185], v181 offset:2048
	ds_read_b128 v[186:189], v181 offset:3072
	ds_read_b128 v[194:197], v181 offset:4096
	ds_read_b128 v[198:201], v181 offset:5120
	ds_read_b128 v[202:205], v181 offset:6144
	ds_read_b128 v[206:209], v181 offset:7168
	buffer_load_dwordx4 v174, s[36:39], s14 offen lds
	s_mov_b32 m0, s8
	s_nop 0
	buffer_load_dwordx4 v176, s[36:39], s14 offen lds
	s_waitcnt vmcnt(8)
	s_waitcnt lgkmcnt(0)
	s_barrier
	s_setprio 1
	v_mfma_f32_16x16x128_f8f6f4 v[140:143], v[120:127], v[160:167], 0
	v_mfma_f32_16x16x128_f8f6f4 v[128:131], v[132:139], v[160:167], 0
	v_mfma_f32_16x16x128_f8f6f4 v[108:111], v[120:127], v[182:189], 0
	v_mfma_f32_16x16x128_f8f6f4 v[104:107], v[132:139], v[182:189], 0
	v_mfma_f32_16x16x128_f8f6f4 v[168:171], v[120:127], v[194:201], 0
	v_mfma_f32_16x16x128_f8f6f4 v[190:193], v[132:139], v[194:201], 0
	v_mfma_f32_16x16x128_f8f6f4 v[210:213], v[120:127], v[202:209], 0
	v_mfma_f32_16x16x128_f8f6f4 v[214:217], v[132:139], v[202:209], 0
	v_mfma_f32_16x16x128_f8f6f4 v[116:119], v[144:151], v[160:167], 0
	v_mfma_f32_16x16x128_f8f6f4 v[112:115], v[152:159], v[160:167], 0
	v_mfma_f32_16x16x128_f8f6f4 v[100:103], v[144:151], v[182:189], 0
	v_mfma_f32_16x16x128_f8f6f4 v[96:99], v[152:159], v[182:189], 0
	v_mfma_f32_16x16x128_f8f6f4 v[160:163], v[144:151], v[194:201], 0
	v_mfma_f32_16x16x128_f8f6f4 v[164:167], v[152:159], v[194:201], 0
	v_mfma_f32_16x16x128_f8f6f4 v[182:185], v[144:151], v[202:209], 0
	v_mfma_f32_16x16x128_f8f6f4 v[186:189], v[152:159], v[202:209], 0
	s_setprio 0
	s_barrier
	s_mov_b32 m0, s44
	s_mov_b32 s14, s38
	s_mov_b32 s15, s39
	s_nop 1
	ds_read_b128 v[64:67], v181 offset:16384
	ds_read_b128 v[68:71], v181 offset:17408
	ds_read_b128 v[72:75], v181 offset:18432
	ds_read_b128 v[76:79], v181 offset:19456
	ds_read_b128 v[80:83], v181 offset:20480
	ds_read_b128 v[84:87], v181 offset:21504
	ds_read_b128 v[88:91], v181 offset:22528
	ds_read_b128 v[92:95], v181 offset:23552
	buffer_load_dwordx4 v175, s[12:15], s55 offen lds
	s_mov_b32 m0, s45
	s_add_i32 s63, s55, s42
	buffer_load_dwordx4 v177, s[12:15], s55 offen lds
	s_mov_b32 m0, s46
	s_nop 0
	buffer_load_dwordx4 v175, s[12:15], s63 offen lds
	s_mov_b32 m0, s47
	s_nop 0
	buffer_load_dwordx4 v177, s[12:15], s63 offen lds
	s_mov_b32 m0, s43
	s_nop 0
	buffer_load_dwordx4 v174, s[36:39], s62 offen lds
	s_mov_b32 m0, s48
	s_nop 0
	buffer_load_dwordx4 v176, s[36:39], s62 offen lds
	s_waitcnt vmcnt(8)
	s_waitcnt lgkmcnt(0)
	s_barrier
	s_setprio 1
	v_mfma_f32_16x16x128_f8f6f4 v[60:63], v[120:127], v[64:71], 0
	v_mfma_f32_16x16x128_f8f6f4 v[56:59], v[132:139], v[64:71], 0
	v_mfma_f32_16x16x128_f8f6f4 v[194:197], v[120:127], v[72:79], 0
	v_mfma_f32_16x16x128_f8f6f4 v[198:201], v[132:139], v[72:79], 0
	v_mfma_f32_16x16x128_f8f6f4 v[202:205], v[120:127], v[80:87], 0
	v_mfma_f32_16x16x128_f8f6f4 v[206:209], v[132:139], v[80:87], 0
	v_mfma_f32_16x16x128_f8f6f4 v[218:221], v[120:127], v[88:95], 0
	v_mfma_f32_16x16x128_f8f6f4 v[226:229], v[132:139], v[88:95], 0
	v_mfma_f32_16x16x128_f8f6f4 v[52:55], v[144:151], v[64:71], 0
	v_mfma_f32_16x16x128_f8f6f4 v[48:51], v[152:159], v[64:71], 0
	v_mfma_f32_16x16x128_f8f6f4 v[230:233], v[144:151], v[72:79], 0
	v_mfma_f32_16x16x128_f8f6f4 v[234:237], v[152:159], v[72:79], 0
	v_mfma_f32_16x16x128_f8f6f4 v[238:241], v[144:151], v[80:87], 0
	v_mfma_f32_16x16x128_f8f6f4 v[242:245], v[152:159], v[80:87], 0
	v_mfma_f32_16x16x128_f8f6f4 v[246:249], v[144:151], v[88:95], 0
	v_mfma_f32_16x16x128_f8f6f4 v[250:253], v[152:159], v[88:95], 0
	s_setprio 0
	s_barrier
; #define PG8_STAGE(bufoff, rs_, soff_, voff) do { _Pragma("unroll") for (int _i = 0; _i < 2; ++_i) \
;         __builtin_amdgcn_raw_ptr_buffer_load_lds(rs_, (LAS void*)(lds + (bufoff) + ldsw + _i * 8192), 16, (int)(voff)[_i], (int)(soff_), 0, 0); } while (0)
; #define PG8_LDA(dst, b, h) do { _Pragma("unroll") for (int m = 0; m < 4; ++m) dst[m] = PG8_LD2(lds + PG8_SA(b, h) + aoff + m * 2048); } while (0)
; #define PG8_LDB(dst, b, h) do { _Pragma("unroll") for (int n = 0; n < 2; ++n) dst[n] = PG8_LD2(lds + PG8_SB(b, h) + boff + n * 2048); } while (0)
; #define PG8_WAIT_V(n) asm volatile("s_waitcnt vmcnt(" #n ")" ::: "memory")
; #define PG8_WAIT_L(n) asm volatile("s_waitcnt lgkmcnt(" #n ")" ::: "memory")
; #define PG8_BAR __builtin_amdgcn_s_barrier()
; #define PG8_SCHED __builtin_amdgcn_sched_barrier(0)
; template <class Epi, class Sched, bool ALIGN_EPI = false, bool SP2 = false, bool FP8 = false>
; __device__ __forceinline__ void gemm_phase(LAS unsigned char* lds, const Gemm g, const Sched& S, const Epi& E, int wbase) {
;     ...
;             PG8_LDB(B0, 1, 0); PG8_LDB(B1, 1, 1); PG8_SCHED; PG8_LDA(At, 1, 0); PG8_STAGE(PG8_SA(0, 1), rA2, a2 + hstep, voffA);
;             PG8_WAIT_V(8); PG8_WAIT_L(0); PG8_BAR; PG8_MMA(0, 0, At, B0); PG8_MMA(0, 1, At, B1); PG8_BAR; PG8_SCHED;
;             PG8_LDA(At, 1, 1); PG8_STAGE(PG8_SB(1, 0), rB2, b3, voffB); PG8_STAGE(PG8_SB(1, 1), rB2, b3 + hstep, voffB); PG8_STAGE(PG8_SA(1, 0), rA2, a3, voffA);
;             PG8_WAIT_V(8); PG8_WAIT_L(0); PG8_BAR; PG8_MMA(1, 0, At, B0); PG8_MMA(1, 1, At, B1); PG8_BAR; PG8_SCHED;
	v_add_u32_e32 v8, 0x18000, v180
	s_nop 3
	ds_read_b128 v[0:3], v8
	ds_read_b128 v[4:7], v8 offset:1024
	ds_read_b128 v[16:19], v8 offset:2048
	ds_read_b128 v[20:23], v8 offset:3072
	v_add_u32_e32 v8, 0x1c000, v180
	ds_read_b128 v[120:123], v8
	ds_read_b128 v[124:127], v8 offset:1024
	ds_read_b128 v[132:135], v8 offset:2048
	ds_read_b128 v[136:139], v8 offset:3072
	s_add_i32 s62, s62, s42
	s_mov_b32 m0, s52
	ds_read_b128 v[8:11], v181 offset:32768
	ds_read_b128 v[12:15], v181 offset:33792
	ds_read_b128 v[24:27], v181 offset:34816
	ds_read_b128 v[28:31], v181 offset:35840
	ds_read_b128 v[32:35], v181 offset:36864
	ds_read_b128 v[36:39], v181 offset:37888
	ds_read_b128 v[40:43], v181 offset:38912
	ds_read_b128 v[44:47], v181 offset:39936
	buffer_load_dwordx4 v174, s[36:39], s62 offen lds
	s_mov_b32 m0, s53
	s_nop 0
	buffer_load_dwordx4 v176, s[36:39], s62 offen lds
	s_waitcnt vmcnt(8)
	s_waitcnt lgkmcnt(0)
	s_barrier
	s_setprio 1
	v_mfma_f32_16x16x128_f8f6f4 v[140:143], v[0:7], v[8:15], v[140:143]
	v_mfma_f32_16x16x128_f8f6f4 v[128:131], v[16:23], v[8:15], v[128:131]
	v_mfma_f32_16x16x128_f8f6f4 v[108:111], v[0:7], v[24:31], v[108:111]
	v_mfma_f32_16x16x128_f8f6f4 v[104:107], v[16:23], v[24:31], v[104:107]
	v_mfma_f32_16x16x128_f8f6f4 v[92:95], v[0:7], v[32:39], v[168:171]
	v_mfma_f32_16x16x128_f8f6f4 v[88:91], v[16:23], v[32:39], v[190:193]
	v_mfma_f32_16x16x128_f8f6f4 v[76:79], v[0:7], v[40:47], v[210:213]
	v_mfma_f32_16x16x128_f8f6f4 v[72:75], v[16:23], v[40:47], v[214:217]
	v_mfma_f32_16x16x128_f8f6f4 v[116:119], v[120:127], v[8:15], v[116:119]
	v_mfma_f32_16x16x128_f8f6f4 v[112:115], v[132:139], v[8:15], v[112:115]
	v_mfma_f32_16x16x128_f8f6f4 v[100:103], v[120:127], v[24:31], v[100:103]
	v_mfma_f32_16x16x128_f8f6f4 v[96:99], v[132:139], v[24:31], v[96:99]
	v_mfma_f32_16x16x128_f8f6f4 v[84:87], v[120:127], v[32:39], v[160:163]
	v_mfma_f32_16x16x128_f8f6f4 v[80:83], v[132:139], v[32:39], v[164:167]
	v_mfma_f32_16x16x128_f8f6f4 v[68:71], v[120:127], v[40:47], v[182:185]
	v_mfma_f32_16x16x128_f8f6f4 v[64:67], v[132:139], v[40:47], v[186:189]
	s_setprio 0
	s_barrier
	s_mov_b32 m0, s56
	s_bitset1_b32 s55, 7
	ds_read_b128 v[32:35], v181 offset:49152
	ds_read_b128 v[36:39], v181 offset:50176
	ds_read_b128 v[144:147], v181 offset:51200
	ds_read_b128 v[148:151], v181 offset:52224
	ds_read_b128 v[152:155], v181 offset:53248
	ds_read_b128 v[156:159], v181 offset:54272
	ds_read_b128 v[160:163], v181 offset:55296
	ds_read_b128 v[164:167], v181 offset:56320
	buffer_load_dwordx4 v175, s[12:15], s55 offen lds
	s_mov_b32 m0, s57
	s_nop 0
	buffer_load_dwordx4 v177, s[12:15], s55 offen lds
	s_add_i32 s55, s55, s42
	s_mov_b32 m0, s65
	s_nop 0
	buffer_load_dwordx4 v175, s[12:15], s55 offen lds
	s_mov_b32 m0, s76
	s_nop 0
	buffer_load_dwordx4 v177, s[12:15], s55 offen lds
	s_mov_b32 m0, s58
	s_nop 0
	buffer_load_dwordx4 v174, s[36:39], s54 offen lds
	s_mov_b32 m0, s59
	s_nop 0
	buffer_load_dwordx4 v176, s[36:39], s54 offen lds
	s_waitcnt vmcnt(8)
	s_waitcnt lgkmcnt(0)
	s_barrier
	s_setprio 1
	v_mfma_f32_16x16x128_f8f6f4 v[60:63], v[0:7], v[32:39], v[60:63]
	v_mfma_f32_16x16x128_f8f6f4 v[56:59], v[16:23], v[32:39], v[56:59]
	v_mfma_f32_16x16x128_f8f6f4 v[44:47], v[0:7], v[144:151], v[194:197]
	v_mfma_f32_16x16x128_f8f6f4 v[40:43], v[16:23], v[144:151], v[198:201]
	v_mfma_f32_16x16x128_f8f6f4 v[28:31], v[0:7], v[152:159], v[202:205]
	v_mfma_f32_16x16x128_f8f6f4 v[24:27], v[16:23], v[152:159], v[206:209]
	v_mfma_f32_16x16x128_f8f6f4 v[12:15], v[0:7], v[160:167], v[218:221]
	v_mfma_f32_16x16x128_f8f6f4 v[8:11], v[16:23], v[160:167], v[226:229]
	v_mfma_f32_16x16x128_f8f6f4 v[52:55], v[120:127], v[32:39], v[52:55]
	v_mfma_f32_16x16x128_f8f6f4 v[48:51], v[132:139], v[32:39], v[48:51]
	v_mfma_f32_16x16x128_f8f6f4 v[36:39], v[120:127], v[144:151], v[230:233]
	v_mfma_f32_16x16x128_f8f6f4 v[32:35], v[132:139], v[144:151], v[234:237]
	v_mfma_f32_16x16x128_f8f6f4 v[20:23], v[120:127], v[152:159], v[238:241]
	v_mfma_f32_16x16x128_f8f6f4 v[16:19], v[132:139], v[152:159], v[242:245]
	v_mfma_f32_16x16x128_f8f6f4 v[4:7], v[120:127], v[160:167], v[246:249]
	v_mfma_f32_16x16x128_f8f6f4 v[0:3], v[132:139], v[160:167], v[250:253]
	s_setprio 0
	s_barrier
	s_add_i32 s61, s61, 2
	s_addk_i32 s4, 0x100
	s_addk_i32 s5, 0x100
	s_cmp_ge_i32 s61, s82
	s_cbranch_scc0 .LBB0_1990
	s_branch .Lzp_after_1990

; #define PG8_BAR __builtin_amdgcn_s_barrier()
; template <class Epi, class Sched, bool ALIGN_EPI = false, bool SP2 = false, bool FP8 = false>
; __device__ __forceinline__ void gemm_phase(LAS unsigned char* lds, const Gemm g, const Sched& S, const Epi& E, int wbase) {
;     ...
;         if constexpr (ALIGN_EPI) { if (wr == 0) PG8_BAR; }
;         { int fr_ = fr, fq_ = fq; asm volatile("" : "+v"(fr_), "+v"(fq_));
;           if constexpr (Epi::HAS_PRE) E(acc, cur, wr, wc, fr_, fq_, pre_); else E(acc, cur, wr, wc, fr_, fq_); } S.done(cur);
.Lzp_after_1990:
	v_mov_b32_e32 v230, v172
	v_mov_b32_e32 v233, v173
	v_mov_b32_e32 v231, v222
	v_mov_b32_e32 v234, v223
	s_and_b64 vcc, exec, s[28:29]
	s_cbranch_vccnz .LBB0_1993
	s_branch .LBB0_1994
